# speedup vs baseline: 1.0321x; 1.0005x over previous
.LBB1_4:
	s_waitcnt lgkmcnt(14)
	v_mfma_f32_32x32x16_f16 v[2:17], v[158:161], v[122:125], v[2:17]
	v_exp_f32_e32 v98, v98
	v_exp_f32_e32 v99, v99
	v_exp_f32_e32 v100, v100
	v_exp_f32_e32 v101, v101
	s_add_i32 m0, s35, s29
	v_lshl_add_u64 v[204:205], v[198:199], 0, s[14:15]
	v_lshl_add_u64 v[58:59], v[204:205], 0, s[16:17]
	global_load_lds_dwordx4 v[58:59], off
	s_waitcnt lgkmcnt(12)
	v_mfma_f32_32x32x16_f16 v[18:33], v[158:161], v[118:121], v[18:33]
	v_exp_f32_e32 v102, v102
	v_exp_f32_e32 v103, v103
	v_exp_f32_e32 v104, v104
	v_exp_f32_e32 v105, v105
	s_add_i32 m0, s35, s28
	v_lshl_add_u64 v[206:207], v[194:195], 0, s[14:15]
	v_lshl_add_u64 v[58:59], v[206:207], 0, s[16:17]
	global_load_lds_dwordx4 v[58:59], off
	v_add_u32_e32 v60, s33, v218
	ds_read_b128 v[118:121], v60
	ds_read_b128 v[178:181], v60 offset:512
	s_waitcnt lgkmcnt(12)
	v_mfma_f32_32x32x16_f16 v[2:17], v[154:157], v[114:117], v[2:17]
	v_exp_f32_e32 v106, v106
	v_exp_f32_e32 v107, v107
	v_exp_f32_e32 v108, v108
	v_exp_f32_e32 v109, v109
	s_add_i32 m0, s33, s26
	v_lshl_add_u64 v[208:209], v[202:203], 0, s[14:15]
	v_lshl_add_u64 v[58:59], v[208:209], 0, s[6:7]
	global_load_lds_dwordx4 v[58:59], off
	ds_read_b128 v[186:189], v60 offset:2048
	ds_read_b128 v[78:81], v60 offset:2560
	s_waitcnt lgkmcnt(12)
	v_mfma_f32_32x32x16_f16 v[18:33], v[154:157], v[74:77], v[18:33]
	v_exp_f32_e32 v110, v110
	v_exp_f32_e32 v111, v111
	v_exp_f32_e32 v112, v112
	v_exp_f32_e32 v113, v113
	s_add_i32 m0, s33, s25
	v_lshl_add_u64 v[210:211], v[196:197], 0, s[14:15]
	v_lshl_add_u64 v[58:59], v[210:211], 0, s[6:7]
	global_load_lds_dwordx4 v[58:59], off
	ds_read_b128 v[74:77], v60 offset:4096
	ds_read_b128 v[62:65], v60 offset:4608
	s_waitcnt lgkmcnt(12)
	v_mfma_f32_32x32x16_f16 v[2:17], v[150:153], v[70:73], v[2:17]
	v_exp_f32_e32 v82, v82
	v_exp_f32_e32 v83, v83
	v_exp_f32_e32 v84, v84
	v_exp_f32_e32 v85, v85
	ds_read_b128 v[70:73], v60 offset:6144
	ds_read_b128 v[58:61], v60 offset:6656
	s_waitcnt lgkmcnt(12)
	v_mfma_f32_32x32x16_f16 v[18:33], v[150:153], v[66:69], v[18:33]
	v_exp_f32_e32 v86, v86
	v_exp_f32_e32 v87, v87
	v_exp_f32_e32 v88, v88
	v_exp_f32_e32 v89, v89
	s_waitcnt lgkmcnt(10)
	v_mfma_f32_32x32x16_f16 v[2:17], v[146:149], v[54:57], v[2:17]
	v_exp_f32_e32 v90, v90
	v_exp_f32_e32 v91, v91
	v_exp_f32_e32 v92, v92
	v_exp_f32_e32 v93, v93
	s_waitcnt lgkmcnt(8)
	v_mfma_f32_32x32x16_f16 v[18:33], v[146:149], v[50:53], v[18:33]
	v_exp_f32_e32 v94, v94
	v_exp_f32_e32 v95, v95
	v_exp_f32_e32 v96, v96
	v_exp_f32_e32 v97, v97
	s_waitcnt vmcnt(4) lgkmcnt(0)
	s_barrier
	s_andn2_b64 vcc, exec, s[20:21]
	s_cbranch_vccnz .LBB1_6
	v_add_u32_e32 v114, s30, v200
	ds_read_b128 v[50:53], v114 offset:49248
	ds_read_b128 v[54:57], v114 offset:49216
	ds_read_b128 v[66:69], v114 offset:49184
	ds_read_b128 v[114:117], v114 offset:49152
	s_waitcnt lgkmcnt(3)
	v_pk_mul_f32 v[14:15], v[14:15], v[50:51]
	s_waitcnt lgkmcnt(2)
	v_pk_mul_f32 v[10:11], v[10:11], v[54:55]
	s_waitcnt lgkmcnt(1)
	v_pk_mul_f32 v[6:7], v[6:7], v[66:67]
	v_pk_mul_f32 v[16:17], v[16:17], v[52:53]
	v_pk_mul_f32 v[12:13], v[12:13], v[56:57]
	v_pk_mul_f32 v[8:9], v[8:9], v[68:69]
	s_waitcnt lgkmcnt(0)
	v_pk_mul_f32 v[4:5], v[4:5], v[116:117]
	v_pk_mul_f32 v[2:3], v[2:3], v[114:115]
	v_pk_mul_f32 v[30:31], v[30:31], v[50:51]
	v_pk_mul_f32 v[26:27], v[26:27], v[54:55]
	v_pk_mul_f32 v[22:23], v[22:23], v[66:67]
	v_pk_mul_f32 v[32:33], v[32:33], v[52:53]
	v_pk_mul_f32 v[28:29], v[28:29], v[56:57]
	v_pk_mul_f32 v[24:25], v[24:25], v[68:69]
	v_pk_mul_f32 v[20:21], v[20:21], v[116:117]
	v_pk_mul_f32 v[18:19], v[18:19], v[114:115]

.LBB1_10:
	s_add_i32 s22, s33, 0x2000
	s_cmpk_lg_i32 s33, 0x4000
	s_cselect_b32 s35, s22, 0
	s_waitcnt lgkmcnt(14)
	v_mfma_f32_32x32x16_f16 v[2:17], v[158:161], v[190:193], v[2:17]
	v_exp_f32_e32 v66, v130
	v_exp_f32_e32 v67, v131
	v_exp_f32_e32 v68, v132
	v_exp_f32_e32 v69, v133
	s_add_i32 m0, s33, s29
	v_lshl_add_u64 v[50:51], v[204:205], 0, s[18:19]
	global_load_lds_dwordx4 v[50:51], off
	s_waitcnt lgkmcnt(12)
	v_mfma_f32_32x32x16_f16 v[18:33], v[158:161], v[182:185], v[18:33]
	v_exp_f32_e32 v78, v142
	v_exp_f32_e32 v79, v143
	v_exp_f32_e32 v80, v144
	v_exp_f32_e32 v81, v145
	s_add_i32 m0, s33, s28
	v_lshl_add_u64 v[50:51], v[206:207], 0, s[18:19]
	global_load_lds_dwordx4 v[50:51], off
	v_add_u32_e32 v86, s35, v218
	ds_read_b128 v[82:85], v86
	ds_read_b128 v[182:185], v86 offset:512
	s_waitcnt lgkmcnt(12)
	v_mfma_f32_32x32x16_f16 v[2:17], v[154:157], v[178:181], v[2:17]
	v_exp_f32_e32 v74, v138
	v_exp_f32_e32 v75, v139
	v_exp_f32_e32 v76, v140
	v_exp_f32_e32 v77, v141
	s_add_i32 m0, s35, s26
	v_lshl_add_u64 v[50:51], v[208:209], 0, s[8:9]
	global_load_lds_dwordx4 v[50:51], off
	ds_read_b128 v[178:181], v86 offset:2048
	ds_read_b128 v[142:145], v86 offset:2560
	s_waitcnt lgkmcnt(12)
	v_mfma_f32_32x32x16_f16 v[18:33], v[154:157], v[186:189], v[18:33]
	v_exp_f32_e32 v70, v134
	v_exp_f32_e32 v71, v135
	v_exp_f32_e32 v72, v136
	v_exp_f32_e32 v73, v137
	s_add_i32 m0, s35, s25
	v_lshl_add_u64 v[50:51], v[210:211], 0, s[8:9]
	global_load_lds_dwordx4 v[50:51], off
	ds_read_b128 v[138:141], v86 offset:4096
	ds_read_b128 v[134:137], v86 offset:4608
	s_waitcnt lgkmcnt(12)
	v_mfma_f32_32x32x16_f16 v[2:17], v[150:153], v[110:113], v[2:17]
	v_exp_f32_e32 v62, v126
	v_exp_f32_e32 v63, v127
	v_exp_f32_e32 v64, v128
	v_exp_f32_e32 v65, v129
	ds_read_b128 v[130:133], v86 offset:6144
	ds_read_b128 v[126:129], v86 offset:6656
	s_waitcnt lgkmcnt(12)
	v_mfma_f32_32x32x16_f16 v[18:33], v[150:153], v[106:109], v[18:33]
	v_exp_f32_e32 v50, v114
	v_exp_f32_e32 v51, v115
	v_exp_f32_e32 v52, v116
	v_exp_f32_e32 v53, v117
	s_waitcnt lgkmcnt(10)
	v_mfma_f32_32x32x16_f16 v[2:17], v[146:149], v[102:105], v[2:17]
	v_exp_f32_e32 v54, v118
	v_exp_f32_e32 v55, v119
	v_exp_f32_e32 v56, v120
	v_exp_f32_e32 v57, v121
	s_waitcnt lgkmcnt(8)
	v_mfma_f32_32x32x16_f16 v[18:33], v[146:149], v[98:101], v[18:33]
	v_exp_f32_e32 v58, v122
	v_exp_f32_e32 v59, v123
	v_exp_f32_e32 v60, v124
	v_exp_f32_e32 v61, v125
	s_waitcnt vmcnt(4) lgkmcnt(0)
	s_barrier
	s_andn2_b64 vcc, exec, s[20:21]
	s_cbranch_vccnz .LBB1_12
	v_add_u32_e32 v98, s30, v200
	ds_read_b128 v[86:89], v98 offset:49248
	ds_read_b128 v[90:93], v98 offset:49216
	ds_read_b128 v[94:97], v98 offset:49152
	ds_read_b128 v[98:101], v98 offset:49184
	s_waitcnt lgkmcnt(3)
	v_pk_mul_f32 v[16:17], v[16:17], v[88:89]
	v_pk_mul_f32 v[14:15], v[14:15], v[86:87]
	s_waitcnt lgkmcnt(2)
	v_pk_mul_f32 v[12:13], v[12:13], v[92:93]
	v_pk_mul_f32 v[10:11], v[10:11], v[90:91]
	s_waitcnt lgkmcnt(0)
	v_pk_mul_f32 v[8:9], v[8:9], v[100:101]
	v_pk_mul_f32 v[6:7], v[6:7], v[98:99]
	v_pk_mul_f32 v[4:5], v[4:5], v[96:97]
	v_pk_mul_f32 v[2:3], v[2:3], v[94:95]
	v_pk_mul_f32 v[32:33], v[32:33], v[88:89]
	v_pk_mul_f32 v[30:31], v[30:31], v[86:87]
	v_pk_mul_f32 v[28:29], v[28:29], v[92:93]
	v_pk_mul_f32 v[26:27], v[26:27], v[90:91]
	v_pk_mul_f32 v[24:25], v[24:25], v[100:101]
	v_pk_mul_f32 v[22:23], v[22:23], v[98:99]
	v_pk_mul_f32 v[20:21], v[20:21], v[96:97]
	v_pk_mul_f32 v[18:19], v[18:19], v[94:95]

_Z8gemm2b_kILi2EEvPKtS1_ii7EpiArgs:
	s_load_dwordx4 s[4:7], s[0:1], 0x0
	s_load_dwordx2 s[12:13], s[0:1], 0x10
	s_load_dwordx4 s[72:75], s[0:1], 0x18
	s_load_dwordx4 s[76:79], s[0:1], 0x38
	s_lshl_b32 s3, s2, 3
	s_and_b32 s3, s3, 56
	s_bfe_u32 s8, s2, 0x30003
	s_or_b32 s3, s3, s8
	s_lshl_b32 s17, s3, 7
	v_readfirstlane_b32 s19, v0
	s_waitcnt lgkmcnt(0)
	s_mul_hi_i32 s9, s13, s17
	s_mul_i32 s8, s13, s17
	s_lshr_b32 s14, s19, 6
	s_lshr_b32 s2, s2, 6
	s_ashr_i32 s11, s13, 31
	s_lshl_b64 s[8:9], s[8:9], 1
	s_mulk_i32 s2, 0xc0
	s_add_u32 s4, s4, s8
	s_addc_u32 s5, s5, s9
	s_mul_hi_i32 s9, s13, s2
	s_mul_i32 s8, s13, s2
	s_ashr_i32 s3, s2, 31
	s_lshl_b64 s[8:9], s[8:9], 1
	s_add_u32 s6, s6, s8
	s_addc_u32 s7, s7, s9
	s_lshr_b32 s8, s19, 1
	v_lshrrev_b32_e32 v1, 4, v0
	s_lshl_b32 s21, s14, 10
	s_and_b32 s16, s8, 0x7fffffc0
	v_xor_b32_e32 v3, v1, v0
	s_bitcmp1_b32 s19, 6
	v_lshrrev_b32_e32 v2, 3, v0
	v_lshlrev_b32_e32 v3, 3, v3
	s_cselect_b32 s18, 0x60, 0
	v_and_b32_e32 v186, 0x7f, v0
	v_add_u32_e32 v186, s17, v186
	v_mov_b32_e32 v187, 0
	v_lshlrev_b64 v[186:187], 5, v[186:187]
	v_lshl_add_u64 v[186:187], s[74:75], 0, v[186:187]
	global_load_dwordx4 v[188:191], v[186:187], off
	global_load_dwordx4 v[192:195], v[186:187], off offset:16
	v_lshrrev_b32_e32 v186, 2, v0
	v_and_or_b32 v186, v186, 12, s18
	v_lshlrev_b32_e32 v186, 2, v186
	s_lshl_b32 s80, s2, 2
	s_add_u32 s82, s76, s80
	s_addc_u32 s83, s77, 0
	s_add_u32 s84, s78, s80
	s_addc_u32 s85, s79, 0
	global_load_dwordx4 v[196:199], v186, s[82:83]
	global_load_dwordx4 v[200:203], v186, s[84:85]
	global_load_dwordx4 v[204:207], v186, s[82:83] offset:64
	global_load_dwordx4 v[208:211], v186, s[84:85] offset:64
	s_cmp_lg_u32 0, -1
	v_mul_lo_u32 v2, s13, v2
	v_and_b32_e32 v3, 56, v3
	s_mov_b32 s10, s13
	s_cselect_b32 s8, 0, 0
	v_add_lshl_u32 v104, v2, v3, 1
	s_add_i32 s22, s21, s8
	s_nop 4
	s_mov_b32 s8, m0
	s_mov_b32 m0, s22
	s_nop 0
	global_load_lds_dwordx4 v104, s[4:5]
	s_mov_b32 m0, s8
	s_lshl_b64 s[14:15], s[10:11], 6
	s_add_u32 s8, s4, s14
	s_addc_u32 s9, s5, s15
	s_add_i32 s23, s22, 0x1000
	s_nop 4
	s_mov_b32 s24, m0
	s_mov_b32 m0, s23
	s_nop 0
	global_load_lds_dwordx4 v104, s[8:9]
	s_mov_b32 m0, s24
	s_add_u32 s8, s8, s14
	s_addc_u32 s9, s9, s15
	s_add_i32 s24, s22, 0x2000
	s_nop 4
	s_mov_b32 s25, m0
	s_mov_b32 m0, s24
	s_nop 0
	global_load_lds_dwordx4 v104, s[8:9]
	s_mov_b32 m0, s25
	s_add_u32 s8, s8, s14
	s_addc_u32 s9, s9, s15
	s_add_i32 s25, s22, 0x3000
	s_nop 4
	s_mov_b32 s26, m0
	s_mov_b32 m0, s25
	s_nop 0
	global_load_lds_dwordx4 v104, s[8:9]
	s_mov_b32 m0, s26
	s_add_i32 s26, s22, 0x4000
	s_nop 4
	s_mov_b32 s8, m0
	s_mov_b32 m0, s26
	s_nop 0
	global_load_lds_dwordx4 v104, s[6:7]
	s_mov_b32 m0, s8
	s_add_u32 s8, s6, s14
	s_addc_u32 s9, s7, s15
	s_add_i32 s27, s22, 0x5000
	s_nop 4
	s_mov_b32 s28, m0
	s_mov_b32 m0, s27
	s_nop 0
	global_load_lds_dwordx4 v104, s[8:9]
	s_mov_b32 m0, s28
	s_add_u32 s8, s8, s14
	s_addc_u32 s9, s9, s15
	s_add_i32 s28, s22, 0x6000
	s_nop 4
	s_mov_b32 s29, m0
	s_mov_b32 m0, s28
	s_nop 0
	global_load_lds_dwordx4 v104, s[8:9]
	s_mov_b32 m0, s29
	s_add_u32 s8, s8, s14
	s_addc_u32 s9, s9, s15
	s_add_i32 s29, s22, 0x7000
	s_nop 4
	s_mov_b32 s30, m0
	s_mov_b32 m0, s29
	s_nop 0
	global_load_lds_dwordx4 v104, s[8:9]
	s_mov_b32 m0, s30
	s_add_u32 s8, s8, s14
	s_addc_u32 s9, s9, s15
	s_add_i32 s30, s22, 0x8000
	s_nop 4
	s_mov_b32 s31, m0
	s_mov_b32 m0, s30
	s_nop 0
	global_load_lds_dwordx4 v104, s[8:9]
	s_mov_b32 m0, s31
	s_add_u32 s8, s8, s14
	s_addc_u32 s9, s9, s15
	s_add_i32 s31, s22, 0x9000
	s_nop 4
	s_mov_b32 s33, m0
	s_mov_b32 m0, s31
	s_nop 0
	global_load_lds_dwordx4 v104, s[8:9]
	s_mov_b32 m0, s33
	s_ashr_i32 s13, s13, 6
	s_mov_b32 s20, 1
	s_cmp_lt_i32 s13, 1
	s_cbranch_scc1 .LBB2_7
	s_lshl_b64 s[8:9], s[10:11], 5
	s_cmp_lg_u32 0, -1
	s_cselect_b32 s33, 0, 0
	s_add_i32 s34, s33, s21
	s_add_i32 s33, s34, 0xa000
	s_add_i32 s34, s34, 0xe000
	s_lshl_b64 s[8:9], s[8:9], 1
	s_add_u32 s45, s4, s8
	s_addc_u32 s46, s5, s9
	s_add_u32 s43, s45, s14
	s_addc_u32 s44, s46, s15
	s_add_u32 s41, s43, s14
	s_addc_u32 s42, s44, s15
	s_add_u32 s35, s6, s8
	s_addc_u32 s38, s7, s9
	s_add_u32 s39, s35, s14
	s_addc_u32 s40, s38, s15
	s_add_u32 s47, s39, s14
	s_addc_u32 s48, s40, s15
	s_add_u32 s49, s47, s14
	s_addc_u32 s50, s48, s15
	s_add_u32 s51, s49, s14
	s_addc_u32 s52, s50, s15
	s_lshl_b64 s[36:37], s[10:11], 7
	s_sub_u32 s36, 0, s36
	s_subb_u32 s37, 0, s37
	s_add_u32 s61, s41, s36
	s_addc_u32 s62, s42, s37
	s_add_u32 s59, s61, s14
	s_addc_u32 s60, s62, s15
	s_add_u32 s57, s59, s14
	s_addc_u32 s58, s60, s15
	s_lshl_b64 s[10:11], s[10:11], 8
	s_sub_u32 s10, 0, s10
	s_subb_u32 s11, 0, s11
	s_add_u32 s53, s51, s10
	s_addc_u32 s54, s52, s11
	s_add_u32 s55, s53, s14
	s_addc_u32 s56, s54, s15
	s_add_u32 s63, s55, s14
	s_addc_u32 s64, s56, s15
	s_add_u32 s65, s63, s14
	s_addc_u32 s66, s64, s15
	s_add_u32 s67, s65, s14
	s_addc_u32 s68, s66, s15
	s_add_u32 s10, s35, 0x80
	s_addc_u32 s11, s38, 0
	s_add_u32 s14, s39, 0x80
	s_addc_u32 s15, s40, 0
	s_add_u32 s35, s47, 0x80
	s_addc_u32 s36, s48, 0
	s_add_u32 s37, s49, 0x80
	s_addc_u32 s38, s50, 0
	s_add_u32 s39, s51, 0x80
	s_addc_u32 s40, s52, 0
	s_add_u32 s41, s41, 0x80
	s_addc_u32 s42, s42, 0
	s_add_u32 s43, s43, 0x80
	s_addc_u32 s44, s44, 0
	s_add_u32 s45, s45, 0x80
	s_addc_u32 s46, s46, 0
	s_add_u32 s47, s53, 0x100
	s_addc_u32 s48, s54, 0
	s_add_u32 s49, s55, 0x100
	s_addc_u32 s50, s56, 0
	s_add_u32 s51, s63, 0x100
	s_addc_u32 s52, s64, 0
	s_add_u32 s53, s65, 0x100
	s_addc_u32 s54, s66, 0
	s_add_u32 s55, s67, 0x100
	s_addc_u32 s56, s68, 0
	v_and_b32_e32 v2, 15, v0
	v_bfe_u32 v0, v0, 1, 3
	s_add_u32 s57, s57, 0x100
	v_bitop3_b32 v0, v1, v0, 3 bitop3:0x6c
	s_addc_u32 s58, s58, 0
	v_lshlrev_b32_e32 v105, 4, v0
	v_or_b32_e32 v0, s18, v2
	s_add_u32 s59, s59, 0x100
	v_xor_b32_e32 v106, 64, v105
	v_lshl_add_u32 v0, v0, 7, 0
	s_addc_u32 s60, s60, 0
	v_or_b32_e32 v1, s16, v2
	v_add_u32_e32 v107, v0, v105
	v_add_u32_e32 v109, v0, v106
	s_add_u32 s61, s61, 0x100
	v_mov_b32_e32 v36, 0
	v_lshl_add_u32 v108, v1, 7, 0
	s_mov_b64 s[8:9], 0
	s_addc_u32 s62, s62, 0
	v_mov_b32_e32 v37, v36
	v_mov_b32_e32 v38, v36
	v_mov_b32_e32 v39, v36
	v_mov_b32_e32 v56, v36
	v_mov_b32_e32 v57, v36
	v_mov_b32_e32 v58, v36
	v_mov_b32_e32 v59, v36
	v_mov_b32_e32 v76, v36
	v_mov_b32_e32 v77, v36
	v_mov_b32_e32 v78, v36
	v_mov_b32_e32 v79, v36
	v_mov_b32_e32 v92, v36
	v_mov_b32_e32 v93, v36
	v_mov_b32_e32 v94, v36
	v_mov_b32_e32 v95, v36
	v_mov_b32_e32 v8, v36
	v_mov_b32_e32 v9, v36
	v_mov_b32_e32 v10, v36
	v_mov_b32_e32 v11, v36
	v_mov_b32_e32 v24, v36
	v_mov_b32_e32 v25, v36
	v_mov_b32_e32 v26, v36
	v_mov_b32_e32 v27, v36
	v_mov_b32_e32 v40, v36
	v_mov_b32_e32 v41, v36
	v_mov_b32_e32 v42, v36
	v_mov_b32_e32 v43, v36
	v_mov_b32_e32 v64, v36
	v_mov_b32_e32 v65, v36
	v_mov_b32_e32 v66, v36
	v_mov_b32_e32 v67, v36
	v_mov_b32_e32 v80, v36
	v_mov_b32_e32 v81, v36
	v_mov_b32_e32 v82, v36
	v_mov_b32_e32 v83, v36
	v_mov_b32_e32 v96, v36
	v_mov_b32_e32 v97, v36
	v_mov_b32_e32 v98, v36
	v_mov_b32_e32 v99, v36
	v_mov_b32_e32 v12, v36
	v_mov_b32_e32 v13, v36
	v_mov_b32_e32 v14, v36
	v_mov_b32_e32 v15, v36
	v_mov_b32_e32 v28, v36
	v_mov_b32_e32 v29, v36
	v_mov_b32_e32 v30, v36
	v_mov_b32_e32 v31, v36
	v_mov_b32_e32 v48, v36
	v_mov_b32_e32 v49, v36
	v_mov_b32_e32 v50, v36
	v_mov_b32_e32 v51, v36
	v_mov_b32_e32 v68, v36
	v_mov_b32_e32 v69, v36
	v_mov_b32_e32 v70, v36
	v_mov_b32_e32 v71, v36
	v_mov_b32_e32 v84, v36
	v_mov_b32_e32 v85, v36
	v_mov_b32_e32 v86, v36
	v_mov_b32_e32 v87, v36
	v_mov_b32_e32 v100, v36
	v_mov_b32_e32 v101, v36
	v_mov_b32_e32 v102, v36
	v_mov_b32_e32 v103, v36
	v_mov_b32_e32 v20, v36
	v_mov_b32_e32 v21, v36
	v_mov_b32_e32 v22, v36
	v_mov_b32_e32 v23, v36
	v_mov_b32_e32 v4, v36
	v_mov_b32_e32 v5, v36
	v_mov_b32_e32 v6, v36
	v_mov_b32_e32 v7, v36
	v_mov_b32_e32 v88, v36
	v_mov_b32_e32 v89, v36
	v_mov_b32_e32 v90, v36
	v_mov_b32_e32 v91, v36
	v_mov_b32_e32 v72, v36
	v_mov_b32_e32 v73, v36
	v_mov_b32_e32 v74, v36
	v_mov_b32_e32 v75, v36
	v_mov_b32_e32 v52, v36
	v_mov_b32_e32 v53, v36
	v_mov_b32_e32 v54, v36
	v_mov_b32_e32 v55, v36
	v_mov_b32_e32 v32, v36
	v_mov_b32_e32 v33, v36
	v_mov_b32_e32 v34, v36
	v_mov_b32_e32 v35, v36
	v_mov_b32_e32 v16, v36
	v_mov_b32_e32 v17, v36
	v_mov_b32_e32 v18, v36
	v_mov_b32_e32 v19, v36
	v_mov_b32_e32 v0, v36
	v_mov_b32_e32 v1, v36
	v_mov_b32_e32 v2, v36
	v_mov_b32_e32 v3, v36
	v_add_u32_e32 v110, 0x4000, v107
	v_add_u32_e32 v111, 0x4000, v109
	s_branch .LBB2_3

.LBB2_8:
	s_mov_b64 s[4:5], s[72:73]
	s_mov_b64 s[6:7], s[74:75]
	s_mov_b64 s[8:9], s[76:77]
	s_mov_b64 s[10:11], s[78:79]
	v_mbcnt_lo_u32_b32 v44, -1, 0
	v_mbcnt_hi_u32_b32 v44, -1, v44
	s_barrier
	s_movk_i32 s0, 0x80
	v_bfi_b32 v120, 63, v44, s19
	v_cmp_gt_i32_e32 vcc, s0, v120
	s_and_saveexec_b64 s[14:15], vcc
	s_cbranch_execz .LBB2_10
	v_add_u32_e32 v46, s17, v120
	v_ashrrev_i32_e32 v47, 31, v46
	v_lshlrev_b64 v[46:47], 5, v[46:47]
	s_waitcnt lgkmcnt(0)
	v_lshl_add_u64 v[46:47], s[6:7], 0, v[46:47]
	v_mov_b64_e32 v[60:61], v[188:189]
	v_mov_b64_e32 v[62:63], v[190:191]
	v_mov_b64_e32 v[104:105], v[192:193]
	v_mov_b64_e32 v[106:107], v[194:195]
	v_mov_b32_e32 v45, 0x3727c5ac
	s_mov_b32 s0, 0xf800000
	s_waitcnt vmcnt(1)
	v_pk_add_f32 v[46:47], v[60:61], v[62:63]
	s_waitcnt vmcnt(0)
	v_pk_add_f32 v[108:109], v[104:105], v[106:107]
	s_nop 0
	v_pk_add_f32 v[46:47], v[46:47], v[108:109]
	s_nop 0
	v_fmac_f32_e32 v62, 0xbe800000, v46
	v_fmac_f32_e32 v106, 0xbe800000, v46
	v_fmamk_f32 v60, v46, 0xbe800000, v60
	v_fmamk_f32 v61, v46, 0xbe800000, v104
	v_mul_f32_e32 v62, v62, v62
	v_mul_f32_e32 v63, v106, v106
	v_fmac_f32_e32 v62, v60, v60
	v_fmac_f32_e32 v63, v61, v61
	v_add_f32_e32 v60, v62, v63
	v_fmamk_f32 v47, v60, 0x43400000, v47
	v_fmac_f32_e32 v45, 0x3aaaaaab, v47
	v_mul_f32_e32 v47, 0x4f800000, v45
	v_cmp_gt_f32_e32 vcc, s0, v45
	v_mov_b32_e32 v61, 0x260
	v_lshl_add_u32 v60, v120, 3, 0
	v_cndmask_b32_e32 v45, v45, v47, vcc
	v_sqrt_f32_e32 v47, v45
	v_mul_f32_e32 v46, 0x3e800000, v46
	v_add_u32_e32 v62, -1, v47
	v_add_u32_e32 v63, 1, v47
	v_fma_f32 v104, -v62, v47, v45
	v_fma_f32 v105, -v63, v47, v45
	v_cmp_ge_f32_e64 s[0:1], 0, v104
	s_nop 1
	v_cndmask_b32_e64 v47, v47, v62, s[0:1]
	v_cmp_lt_f32_e64 s[0:1], 0, v105
	s_nop 1
	v_cndmask_b32_e64 v47, v47, v63, s[0:1]
	v_mul_f32_e32 v62, 0x37800000, v47
	v_cndmask_b32_e32 v47, v47, v62, vcc
	v_cmp_class_f32_e32 vcc, v45, v61
	s_nop 1
	v_cndmask_b32_e32 v45, v47, v45, vcc
	v_div_scale_f32 v47, s[0:1], v45, v45, 1.0
	v_rcp_f32_e32 v61, v47
	v_div_scale_f32 v62, vcc, 1.0, v45, 1.0
	v_fma_f32 v63, -v47, v61, 1.0
	v_fmac_f32_e32 v61, v63, v61
	v_mul_f32_e32 v63, v62, v61
	v_fma_f32 v104, -v47, v63, v62
	v_fmac_f32_e32 v63, v104, v61
	v_fma_f32 v47, -v47, v63, v62
	v_div_fmas_f32 v47, v47, v61, v63
	v_div_fixup_f32 v47, v47, v45, 1.0
	ds_write_b64 v60, v[46:47] offset:51200
.LBB2_10:
	s_or_b64 exec, exec, s[14:15]
	v_lshrrev_b32_e32 v45, 2, v44
	s_lshl_b64 s[0:1], s[2:3], 2
	v_and_or_b32 v45, v45, 12, s18
	s_waitcnt lgkmcnt(0)
	s_add_u32 s18, s8, s0
	s_addc_u32 s19, s9, s1
	s_waitcnt lgkmcnt(0)
	s_barrier
	v_lshlrev_b32_e32 v124, 2, v45
	s_add_u32 s20, s10, s0
	v_mov_b64_e32 v[116:117], v[196:197]
	v_mov_b64_e32 v[118:119], v[198:199]
	s_addc_u32 s21, s11, s1
	v_mov_b64_e32 v[112:113], v[200:201]
	v_mov_b64_e32 v[114:115], v[202:203]
	v_and_or_b32 v44, v44, 15, s16
	s_movk_i32 s7, 0x190
	v_lshl_add_u32 v46, v44, 3, 0
	v_mul_lo_u32 v104, v44, s7
	v_add_u32_e32 v44, 0xc800, v46
	v_lshlrev_b32_e32 v105, 1, v45
	ds_read2_b64 v[60:63], v44 offset1:16
	ds_read2_b64 v[44:47], v44 offset0:32 offset1:48
	v_add3_u32 v121, 0, v105, v104
	v_mov_b64_e32 v[108:109], v[204:205]
	v_mov_b64_e32 v[110:111], v[206:207]
	v_mov_b64_e32 v[104:105], v[208:209]
	v_mov_b64_e32 v[106:107], v[210:211]
	s_mov_b32 s8, 0x3e6d3388
	s_mov_b32 s22, 0xbf3a00e3
	s_mov_b32 s0, 0x3f07dc22
	s_mov_b32 s16, 0xbf38aa3b
	v_mov_b64_e32 v[122:123], s[22:23]
	s_mov_b32 s14, 0x3f35f0e3
	s_mov_b32 s6, 0xbe11a98e
	s_mov_b32 s10, 0x3e027906
	s_waitcnt vmcnt(3) lgkmcnt(1)
	v_pk_fma_f32 v[100:101], v[116:117], v[60:61], v[100:101] op_sel_hi:[1,0,1] neg_lo:[1,0,0] neg_hi:[1,0,0]
	v_xor_b32_e32 v119, 0x80000000, v119
	v_xor_b32_e32 v118, 0x80000000, v118
	v_pk_fma_f32 v[102:103], v[118:119], v[60:61], v[102:103] op_sel_hi:[1,0,1]
	s_waitcnt vmcnt(2)
	v_pk_fma_f32 v[100:101], v[60:61], v[100:101], v[112:113] op_sel:[1,0,0]
	v_pk_fma_f32 v[102:103], v[60:61], v[102:103], v[114:115] op_sel:[1,0,0]
	v_and_b32_e32 v127, 0x7fffffff, v101
	v_and_b32_e32 v126, 0x7fffffff, v100
	v_and_b32_e32 v133, 0x7fffffff, v103
	v_and_b32_e32 v132, 0x7fffffff, v102
	v_pk_fma_f32 v[126:127], v[126:127], s[8:9], 1.0 op_sel_hi:[1,0,0]
	v_pk_fma_f32 v[96:97], v[116:117], v[62:63], v[96:97] op_sel_hi:[1,0,1] neg_lo:[1,0,0] neg_hi:[1,0,0]
	v_pk_fma_f32 v[132:133], v[132:133], s[8:9], 1.0 op_sel_hi:[1,0,0]
	v_rcp_f32_e32 v126, v126
	v_rcp_f32_e32 v127, v127
	v_pk_fma_f32 v[96:97], v[62:63], v[96:97], v[112:113] op_sel:[1,0,0]
	v_rcp_f32_e32 v132, v132
	v_rcp_f32_e32 v133, v133
	v_and_b32_e32 v135, 0x7fffffff, v97
	v_and_b32_e32 v134, 0x7fffffff, v96
	v_pk_mul_f32 v[130:131], v[100:101], v[100:101]
	v_pk_fma_f32 v[134:135], v[134:135], s[8:9], 1.0 op_sel_hi:[1,0,0]
	v_pk_mul_f32 v[128:129], v[102:103], v[102:103]
	v_pk_mul_f32 v[130:131], v[130:131], s[16:17] op_sel_hi:[1,0]
	v_rcp_f32_e32 v134, v134
	v_rcp_f32_e32 v135, v135
	v_pk_fma_f32 v[140:141], v[126:127], s[0:1], v[122:123] op_sel_hi:[1,0,0]
	v_pk_mul_f32 v[128:129], v[128:129], s[16:17] op_sel_hi:[1,0]
	v_exp_f32_e32 v130, v130
	v_exp_f32_e32 v131, v131
	v_pk_fma_f32 v[142:143], v[132:133], s[0:1], v[122:123] op_sel_hi:[1,0,0]
	v_pk_fma_f32 v[140:141], v[126:127], v[140:141], s[14:15] op_sel_hi:[1,1,0]
	v_exp_f32_e32 v128, v128
	v_exp_f32_e32 v129, v129
	v_pk_fma_f32 v[142:143], v[132:133], v[142:143], s[14:15] op_sel_hi:[1,1,0]
	v_pk_fma_f32 v[140:141], v[126:127], v[140:141], s[6:7] op_sel_hi:[1,1,0]
	v_pk_mul_f32 v[138:139], v[96:97], v[96:97]
	v_pk_fma_f32 v[142:143], v[132:133], v[142:143], s[6:7] op_sel_hi:[1,1,0]
	v_pk_fma_f32 v[140:141], v[126:127], v[140:141], s[10:11] op_sel_hi:[1,1,0]
	v_pk_mul_f32 v[138:139], v[138:139], s[16:17] op_sel_hi:[1,0]
	v_pk_fma_f32 v[144:145], v[134:135], s[0:1], v[122:123] op_sel_hi:[1,0,0]
	v_pk_fma_f32 v[142:143], v[132:133], v[142:143], s[10:11] op_sel_hi:[1,1,0]
	v_pk_mul_f32 v[126:127], v[126:127], v[140:141]
	v_exp_f32_e32 v138, v138
	v_exp_f32_e32 v139, v139
	v_pk_fma_f32 v[144:145], v[134:135], v[144:145], s[14:15] op_sel_hi:[1,1,0]
	v_pk_mul_f32 v[132:133], v[132:133], v[142:143]
	v_pk_mul_f32 v[126:127], v[130:131], v[126:127]
	v_pk_fma_f32 v[98:99], v[118:119], v[62:63], v[98:99] op_sel_hi:[1,0,1]
	v_pk_fma_f32 v[144:145], v[134:135], v[144:145], s[6:7] op_sel_hi:[1,1,0]
	v_pk_mul_f32 v[128:129], v[128:129], v[132:133]
	v_pk_mul_f32 v[132:133], v[100:101], v[126:127]
	v_pk_fma_f32 v[126:127], v[100:101], v[126:127], v[100:101] neg_lo:[1,0,0] neg_hi:[1,0,0]
	v_cmp_gt_f32_e32 vcc, 0, v100
	v_pk_fma_f32 v[98:99], v[62:63], v[98:99], v[114:115] op_sel:[1,0,0]
	v_pk_fma_f32 v[144:145], v[134:135], v[144:145], s[10:11] op_sel_hi:[1,1,0]
	v_cndmask_b32_e32 v100, v126, v132, vcc
	v_cmp_gt_f32_e32 vcc, 0, v101
	v_pk_mul_f32 v[134:135], v[134:135], v[144:145]
	v_and_b32_e32 v126, 0x7fffffff, v98
	v_cndmask_b32_e32 v101, v127, v133, vcc
	v_and_b32_e32 v127, 0x7fffffff, v99
	v_pk_mul_f32 v[130:131], v[138:139], v[134:135]
	v_pk_mul_f32 v[134:135], v[102:103], v[128:129]
	v_pk_fma_f32 v[128:129], v[102:103], v[128:129], v[102:103] neg_lo:[1,0,0] neg_hi:[1,0,0]
	v_cmp_gt_f32_e32 vcc, 0, v102
	v_pk_fma_f32 v[126:127], v[126:127], s[8:9], 1.0 op_sel_hi:[1,0,0]
	v_pk_mul_f32 v[138:139], v[96:97], v[130:131]
	v_cndmask_b32_e32 v102, v128, v134, vcc
	v_cmp_gt_f32_e32 vcc, 0, v103
	v_rcp_f32_e32 v126, v126
	v_rcp_f32_e32 v127, v127
	v_cndmask_b32_e32 v103, v129, v135, vcc
	v_cvt_pk_f16_f32 v100, v100, v101
	v_cvt_pk_f16_f32 v101, v102, v103
	v_pk_fma_f32 v[102:103], v[96:97], v[130:131], v[96:97] neg_lo:[1,0,0] neg_hi:[1,0,0]
	v_cmp_gt_f32_e32 vcc, 0, v96
	v_pk_mul_f32 v[136:137], v[98:99], v[98:99]
	s_waitcnt lgkmcnt(0)
	v_pk_fma_f32 v[92:93], v[116:117], v[44:45], v[92:93] op_sel_hi:[1,0,1] neg_lo:[1,0,0] neg_hi:[1,0,0]
	v_cndmask_b32_e32 v125, v102, v138, vcc
	v_cmp_gt_f32_e32 vcc, 0, v97
	v_pk_fma_f32 v[96:97], v[126:127], s[0:1], v[122:123] op_sel_hi:[1,0,0]
	v_pk_fma_f32 v[92:93], v[44:45], v[92:93], v[112:113] op_sel:[1,0,0]
	v_cndmask_b32_e32 v128, v103, v139, vcc
	v_pk_mul_f32 v[102:103], v[136:137], s[16:17] op_sel_hi:[1,0]
	v_pk_fma_f32 v[96:97], v[126:127], v[96:97], s[14:15] op_sel_hi:[1,1,0]
	v_exp_f32_e32 v102, v102
	v_exp_f32_e32 v103, v103
	v_pk_fma_f32 v[96:97], v[126:127], v[96:97], s[6:7] op_sel_hi:[1,1,0]
	v_cmp_gt_f32_e32 vcc, 0, v98
	v_pk_fma_f32 v[96:97], v[126:127], v[96:97], s[10:11] op_sel_hi:[1,1,0]
	v_pk_fma_f32 v[94:95], v[118:119], v[44:45], v[94:95] op_sel_hi:[1,0,1]
	v_pk_mul_f32 v[96:97], v[126:127], v[96:97]
	v_pk_mul_f32 v[126:127], v[92:93], v[92:93]
	v_pk_mul_f32 v[96:97], v[102:103], v[96:97]
	v_pk_mul_f32 v[126:127], v[126:127], s[16:17] op_sel_hi:[1,0]
	v_pk_mul_f32 v[102:103], v[98:99], v[96:97]
	v_pk_fma_f32 v[96:97], v[98:99], v[96:97], v[98:99] neg_lo:[1,0,0] neg_hi:[1,0,0]
	v_and_b32_e32 v98, 0x7fffffff, v92
	v_cndmask_b32_e32 v102, v96, v102, vcc
	v_cmp_gt_f32_e32 vcc, 0, v99
	v_and_b32_e32 v99, 0x7fffffff, v93
	v_pk_fma_f32 v[98:99], v[98:99], s[8:9], 1.0 op_sel_hi:[1,0,0]
	v_cndmask_b32_e32 v97, v97, v103, vcc
	v_rcp_f32_e32 v98, v98
	v_rcp_f32_e32 v99, v99
	v_cvt_pk_f16_f32 v97, v102, v97
	v_pk_fma_f32 v[94:95], v[44:45], v[94:95], v[114:115] op_sel:[1,0,0]
	v_exp_f32_e32 v126, v126
	v_pk_fma_f32 v[102:103], v[98:99], s[0:1], v[122:123] op_sel_hi:[1,0,0]
	v_exp_f32_e32 v127, v127
	v_pk_fma_f32 v[102:103], v[98:99], v[102:103], s[14:15] op_sel_hi:[1,1,0]
	v_cvt_pk_f16_f32 v96, v125, v128
	v_pk_fma_f32 v[102:103], v[98:99], v[102:103], s[6:7] op_sel_hi:[1,1,0]
	v_and_b32_e32 v129, 0x7fffffff, v95
	v_and_b32_e32 v128, 0x7fffffff, v94
	v_pk_fma_f32 v[102:103], v[98:99], v[102:103], s[10:11] op_sel_hi:[1,1,0]
	v_pk_fma_f32 v[128:129], v[128:129], s[8:9], 1.0 op_sel_hi:[1,0,0]
	v_pk_mul_f32 v[98:99], v[98:99], v[102:103]
	v_rcp_f32_e32 v128, v128
	v_rcp_f32_e32 v129, v129
	v_pk_mul_f32 v[98:99], v[126:127], v[98:99]
	v_cmp_gt_f32_e32 vcc, 0, v92
	v_pk_mul_f32 v[126:127], v[92:93], v[98:99]
	v_pk_fma_f32 v[98:99], v[92:93], v[98:99], v[92:93] neg_lo:[1,0,0] neg_hi:[1,0,0]
	v_pk_mul_f32 v[102:103], v[94:95], v[94:95]
	v_cndmask_b32_e32 v125, v98, v126, vcc
	v_cmp_gt_f32_e32 vcc, 0, v93
	v_pk_fma_f32 v[92:93], v[128:129], s[0:1], v[122:123] op_sel_hi:[1,0,0]
	v_pk_fma_f32 v[88:89], v[116:117], v[46:47], v[88:89] op_sel_hi:[1,0,1] neg_lo:[1,0,0] neg_hi:[1,0,0]
	v_cndmask_b32_e32 v126, v99, v127, vcc
	v_pk_mul_f32 v[98:99], v[102:103], s[16:17] op_sel_hi:[1,0]
	v_pk_fma_f32 v[92:93], v[128:129], v[92:93], s[14:15] op_sel_hi:[1,1,0]
	v_exp_f32_e32 v98, v98
	v_exp_f32_e32 v99, v99
	v_pk_fma_f32 v[92:93], v[128:129], v[92:93], s[6:7] op_sel_hi:[1,1,0]
	v_cmp_gt_f32_e32 vcc, 0, v94
	v_pk_fma_f32 v[92:93], v[128:129], v[92:93], s[10:11] op_sel_hi:[1,1,0]
	v_pk_fma_f32 v[88:89], v[46:47], v[88:89], v[112:113] op_sel:[1,0,0]
	v_pk_mul_f32 v[92:93], v[128:129], v[92:93]
	v_pk_mul_f32 v[102:103], v[88:89], v[88:89]
	v_pk_mul_f32 v[92:93], v[98:99], v[92:93]
	v_pk_fma_f32 v[90:91], v[118:119], v[46:47], v[90:91] op_sel_hi:[1,0,1]
	v_pk_mul_f32 v[98:99], v[94:95], v[92:93]
	v_pk_fma_f32 v[92:93], v[94:95], v[92:93], v[94:95] neg_lo:[1,0,0] neg_hi:[1,0,0]
	v_and_b32_e32 v94, 0x7fffffff, v88
	v_cndmask_b32_e32 v98, v92, v98, vcc
	v_cmp_gt_f32_e32 vcc, 0, v95
	v_and_b32_e32 v95, 0x7fffffff, v89
	v_pk_fma_f32 v[94:95], v[94:95], s[8:9], 1.0 op_sel_hi:[1,0,0]
	v_cndmask_b32_e32 v93, v93, v99, vcc
	v_rcp_f32_e32 v94, v94
	v_rcp_f32_e32 v95, v95
	v_cvt_pk_f16_f32 v93, v98, v93
	v_pk_mul_f32 v[102:103], v[102:103], s[16:17] op_sel_hi:[1,0]
	v_pk_fma_f32 v[90:91], v[46:47], v[90:91], v[114:115] op_sel:[1,0,0]
	v_pk_fma_f32 v[98:99], v[94:95], s[0:1], v[122:123] op_sel_hi:[1,0,0]
	v_exp_f32_e32 v102, v102
	v_pk_fma_f32 v[98:99], v[94:95], v[98:99], s[14:15] op_sel_hi:[1,1,0]
	v_exp_f32_e32 v103, v103
	v_pk_fma_f32 v[98:99], v[94:95], v[98:99], s[6:7] op_sel_hi:[1,1,0]
	v_and_b32_e32 v113, 0x7fffffff, v91
	v_and_b32_e32 v112, 0x7fffffff, v90
	v_pk_fma_f32 v[98:99], v[94:95], v[98:99], s[10:11] op_sel_hi:[1,1,0]
	v_pk_fma_f32 v[112:113], v[112:113], s[8:9], 1.0 op_sel_hi:[1,0,0]
	v_pk_mul_f32 v[94:95], v[94:95], v[98:99]
	v_rcp_f32_e32 v112, v112
	v_rcp_f32_e32 v113, v113
	v_pk_mul_f32 v[94:95], v[102:103], v[94:95]
	v_cmp_gt_f32_e32 vcc, 0, v88
	v_pk_mul_f32 v[102:103], v[88:89], v[94:95]
	v_pk_fma_f32 v[94:95], v[88:89], v[94:95], v[88:89] neg_lo:[1,0,0] neg_hi:[1,0,0]
	v_pk_mul_f32 v[98:99], v[90:91], v[90:91]
	v_cndmask_b32_e32 v102, v94, v102, vcc
	v_cmp_gt_f32_e32 vcc, 0, v89
	v_pk_fma_f32 v[88:89], v[112:113], s[0:1], v[122:123] op_sel_hi:[1,0,0]
	s_waitcnt vmcnt(1)
	v_pk_fma_f32 v[84:85], v[108:109], v[60:61], v[84:85] op_sel_hi:[1,0,1] neg_lo:[1,0,0] neg_hi:[1,0,0]
	v_cndmask_b32_e32 v103, v95, v103, vcc
	v_pk_mul_f32 v[94:95], v[98:99], s[16:17] op_sel_hi:[1,0]
	v_pk_fma_f32 v[88:89], v[112:113], v[88:89], s[14:15] op_sel_hi:[1,1,0]
	v_exp_f32_e32 v94, v94
	v_exp_f32_e32 v95, v95
	v_pk_fma_f32 v[88:89], v[112:113], v[88:89], s[6:7] op_sel_hi:[1,1,0]
	v_cmp_gt_f32_e32 vcc, 0, v90
	v_pk_fma_f32 v[88:89], v[112:113], v[88:89], s[10:11] op_sel_hi:[1,1,0]
	s_waitcnt vmcnt(0)
	v_pk_fma_f32 v[84:85], v[60:61], v[84:85], v[104:105] op_sel:[1,0,0]
	v_pk_mul_f32 v[88:89], v[112:113], v[88:89]
	v_pk_fma_f32 v[80:81], v[108:109], v[62:63], v[80:81] op_sel_hi:[1,0,1] neg_lo:[1,0,0] neg_hi:[1,0,0]
	v_pk_mul_f32 v[88:89], v[94:95], v[88:89]
	v_pk_fma_f32 v[80:81], v[62:63], v[80:81], v[104:105] op_sel:[1,0,0]
	v_pk_mul_f32 v[94:95], v[90:91], v[88:89]
	v_pk_fma_f32 v[88:89], v[90:91], v[88:89], v[90:91] neg_lo:[1,0,0] neg_hi:[1,0,0]
	v_pk_fma_f32 v[76:77], v[108:109], v[44:45], v[76:77] op_sel_hi:[1,0,1] neg_lo:[1,0,0] neg_hi:[1,0,0]
	v_cndmask_b32_e32 v90, v88, v94, vcc
	v_cmp_gt_f32_e32 vcc, 0, v91
	v_and_b32_e32 v94, 0x7fffffff, v84
	v_cvt_pk_f16_f32 v88, v102, v103
	v_cndmask_b32_e32 v89, v89, v95, vcc
	v_and_b32_e32 v95, 0x7fffffff, v85
	v_pk_fma_f32 v[94:95], v[94:95], s[8:9], 1.0 op_sel_hi:[1,0,0]
	v_cvt_pk_f16_f32 v89, v90, v89
	v_rcp_f32_e32 v94, v94
	v_rcp_f32_e32 v95, v95
	v_xor_b32_e32 v91, 0x80000000, v111
	v_xor_b32_e32 v90, 0x80000000, v110
	v_pk_mul_f32 v[102:103], v[84:85], v[84:85]
	v_pk_fma_f32 v[86:87], v[90:91], v[60:61], v[86:87] op_sel_hi:[1,0,1]
	v_pk_fma_f32 v[98:99], v[94:95], s[0:1], v[122:123] op_sel_hi:[1,0,0]
	v_pk_mul_f32 v[102:103], v[102:103], s[16:17] op_sel_hi:[1,0]
	v_pk_fma_f32 v[86:87], v[60:61], v[86:87], v[106:107] op_sel:[1,0,0]
	v_pk_fma_f32 v[98:99], v[94:95], v[98:99], s[14:15] op_sel_hi:[1,1,0]
	v_exp_f32_e32 v102, v102
	v_exp_f32_e32 v103, v103
	v_pk_fma_f32 v[98:99], v[94:95], v[98:99], s[6:7] op_sel_hi:[1,1,0]
	v_and_b32_e32 v111, 0x7fffffff, v87
	v_and_b32_e32 v110, 0x7fffffff, v86
	v_pk_fma_f32 v[98:99], v[94:95], v[98:99], s[10:11] op_sel_hi:[1,1,0]
	v_pk_fma_f32 v[110:111], v[110:111], s[8:9], 1.0 op_sel_hi:[1,0,0]
	v_pk_mul_f32 v[94:95], v[94:95], v[98:99]
	v_rcp_f32_e32 v110, v110
	v_rcp_f32_e32 v111, v111
	v_pk_mul_f32 v[94:95], v[102:103], v[94:95]
	v_cmp_gt_f32_e32 vcc, 0, v84
	v_pk_mul_f32 v[102:103], v[84:85], v[94:95]
	v_pk_fma_f32 v[94:95], v[84:85], v[94:95], v[84:85] neg_lo:[1,0,0] neg_hi:[1,0,0]
	v_pk_mul_f32 v[98:99], v[86:87], v[86:87]
	v_cndmask_b32_e32 v102, v94, v102, vcc
	v_cmp_gt_f32_e32 vcc, 0, v85
	v_pk_fma_f32 v[84:85], v[110:111], s[0:1], v[122:123] op_sel_hi:[1,0,0]
	v_pk_fma_f32 v[82:83], v[90:91], v[62:63], v[82:83] op_sel_hi:[1,0,1]
	v_cndmask_b32_e32 v103, v95, v103, vcc
	v_pk_mul_f32 v[94:95], v[98:99], s[16:17] op_sel_hi:[1,0]
	v_pk_fma_f32 v[84:85], v[110:111], v[84:85], s[14:15] op_sel_hi:[1,1,0]
	v_exp_f32_e32 v94, v94
	v_exp_f32_e32 v95, v95
	v_pk_fma_f32 v[84:85], v[110:111], v[84:85], s[6:7] op_sel_hi:[1,1,0]
	v_cmp_gt_f32_e32 vcc, 0, v86
	v_pk_fma_f32 v[84:85], v[110:111], v[84:85], s[10:11] op_sel_hi:[1,1,0]
	v_pk_fma_f32 v[82:83], v[62:63], v[82:83], v[106:107] op_sel:[1,0,0]
	v_pk_mul_f32 v[84:85], v[110:111], v[84:85]
	v_and_b32_e32 v99, 0x7fffffff, v83
	v_pk_mul_f32 v[84:85], v[94:95], v[84:85]
	v_and_b32_e32 v98, 0x7fffffff, v82
	v_pk_mul_f32 v[94:95], v[86:87], v[84:85]
	v_pk_fma_f32 v[84:85], v[86:87], v[84:85], v[86:87] neg_lo:[1,0,0] neg_hi:[1,0,0]
	v_pk_fma_f32 v[98:99], v[98:99], s[8:9], 1.0 op_sel_hi:[1,0,0]
	v_cndmask_b32_e32 v86, v84, v94, vcc
	v_cmp_gt_f32_e32 vcc, 0, v87
	v_and_b32_e32 v87, 0x7fffffff, v81
	v_cvt_pk_f16_f32 v84, v102, v103
	v_cndmask_b32_e32 v85, v85, v95, vcc
	v_cvt_pk_f16_f32 v85, v86, v85
	v_and_b32_e32 v86, 0x7fffffff, v80
	v_pk_fma_f32 v[86:87], v[86:87], s[8:9], 1.0 op_sel_hi:[1,0,0]
	v_pk_mul_f32 v[94:95], v[80:81], v[80:81]
	v_rcp_f32_e32 v86, v86
	v_rcp_f32_e32 v87, v87
	ds_write2_b64 v121, v[100:101], v[84:85] offset1:4
	v_pk_mul_f32 v[94:95], v[94:95], s[16:17] op_sel_hi:[1,0]
	v_rcp_f32_e32 v98, v98
	v_pk_fma_f32 v[84:85], v[86:87], s[0:1], v[122:123] op_sel_hi:[1,0,0]
	v_exp_f32_e32 v94, v94
	v_pk_fma_f32 v[84:85], v[86:87], v[84:85], s[14:15] op_sel_hi:[1,1,0]
	v_exp_f32_e32 v95, v95
	v_pk_fma_f32 v[84:85], v[86:87], v[84:85], s[6:7] op_sel_hi:[1,1,0]
	v_rcp_f32_e32 v99, v99
	v_pk_fma_f32 v[84:85], v[86:87], v[84:85], s[10:11] op_sel_hi:[1,1,0]
	v_cmp_gt_f32_e32 vcc, 0, v80
	v_pk_mul_f32 v[84:85], v[86:87], v[84:85]
	v_pk_mul_f32 v[86:87], v[82:83], v[82:83]
	v_pk_mul_f32 v[84:85], v[94:95], v[84:85]
	v_pk_fma_f32 v[76:77], v[44:45], v[76:77], v[104:105] op_sel:[1,0,0]
	v_pk_mul_f32 v[94:95], v[80:81], v[84:85]
	v_pk_fma_f32 v[84:85], v[80:81], v[84:85], v[80:81] neg_lo:[1,0,0] neg_hi:[1,0,0]
	v_pk_fma_f32 v[78:79], v[90:91], v[44:45], v[78:79] op_sel_hi:[1,0,1]
	v_cndmask_b32_e32 v94, v84, v94, vcc
	v_cmp_gt_f32_e32 vcc, 0, v81
	v_pk_fma_f32 v[80:81], v[98:99], s[0:1], v[122:123] op_sel_hi:[1,0,0]
	v_pk_fma_f32 v[78:79], v[44:45], v[78:79], v[106:107] op_sel:[1,0,0]
	v_cndmask_b32_e32 v95, v85, v95, vcc
	v_pk_mul_f32 v[84:85], v[86:87], s[16:17] op_sel_hi:[1,0]
	v_pk_fma_f32 v[80:81], v[98:99], v[80:81], s[14:15] op_sel_hi:[1,1,0]
	v_exp_f32_e32 v84, v84
	v_exp_f32_e32 v85, v85
	v_pk_fma_f32 v[80:81], v[98:99], v[80:81], s[6:7] op_sel_hi:[1,1,0]
	v_cmp_gt_f32_e32 vcc, 0, v82
	v_pk_fma_f32 v[80:81], v[98:99], v[80:81], s[10:11] op_sel_hi:[1,1,0]
	v_pk_fma_f32 v[72:73], v[108:109], v[46:47], v[72:73] op_sel_hi:[1,0,1] neg_lo:[1,0,0] neg_hi:[1,0,0]
	v_pk_mul_f32 v[80:81], v[98:99], v[80:81]
	v_pk_fma_f32 v[72:73], v[46:47], v[72:73], v[104:105] op_sel:[1,0,0]
	v_pk_mul_f32 v[80:81], v[84:85], v[80:81]
	v_cvt_pk_f16_f32 v92, v125, v126
	v_pk_mul_f32 v[84:85], v[82:83], v[80:81]
	v_pk_fma_f32 v[80:81], v[82:83], v[80:81], v[82:83] neg_lo:[1,0,0] neg_hi:[1,0,0]
	v_pk_fma_f32 v[74:75], v[90:91], v[46:47], v[74:75] op_sel_hi:[1,0,1]
	v_cndmask_b32_e32 v82, v80, v84, vcc
	v_cmp_gt_f32_e32 vcc, 0, v83
	v_and_b32_e32 v83, 0x7fffffff, v77
	v_cvt_pk_f16_f32 v80, v94, v95
	v_cndmask_b32_e32 v81, v81, v85, vcc
	v_cvt_pk_f16_f32 v81, v82, v81
	v_and_b32_e32 v82, 0x7fffffff, v76
	v_pk_fma_f32 v[82:83], v[82:83], s[8:9], 1.0 op_sel_hi:[1,0,0]
	v_add_u32_e32 v94, 0x1800, v121
	v_rcp_f32_e32 v82, v82
	v_rcp_f32_e32 v83, v83
	v_pk_mul_f32 v[84:85], v[76:77], v[76:77]
	ds_write2_b64 v94, v[96:97], v[80:81] offset0:32 offset1:36
	v_pk_mul_f32 v[84:85], v[84:85], s[16:17] op_sel_hi:[1,0]
	v_pk_fma_f32 v[80:81], v[82:83], s[0:1], v[122:123] op_sel_hi:[1,0,0]
	v_exp_f32_e32 v84, v84
	v_pk_fma_f32 v[80:81], v[82:83], v[80:81], s[14:15] op_sel_hi:[1,1,0]
	v_exp_f32_e32 v85, v85
	v_pk_fma_f32 v[80:81], v[82:83], v[80:81], s[6:7] op_sel_hi:[1,1,0]
	v_pk_mul_f32 v[96:97], v[78:79], v[78:79]
	v_pk_fma_f32 v[80:81], v[82:83], v[80:81], s[10:11] op_sel_hi:[1,1,0]
	v_cmp_gt_f32_e32 vcc, 0, v76
	v_pk_mul_f32 v[80:81], v[82:83], v[80:81]
	v_pk_mul_f32 v[96:97], v[96:97], s[16:17] op_sel_hi:[1,0]
	v_pk_mul_f32 v[80:81], v[84:85], v[80:81]
	global_load_dwordx4 v[84:87], v124, s[18:19] offset:128
	v_pk_mul_f32 v[98:99], v[76:77], v[80:81]
	v_pk_fma_f32 v[100:101], v[76:77], v[80:81], v[76:77] neg_lo:[1,0,0] neg_hi:[1,0,0]
	v_and_b32_e32 v81, 0x7fffffff, v79
	v_and_b32_e32 v80, 0x7fffffff, v78
	v_pk_fma_f32 v[102:103], v[80:81], s[8:9], 1.0 op_sel_hi:[1,0,0]
	global_load_dwordx4 v[80:83], v124, s[20:21] offset:128
	v_rcp_f32_e32 v102, v102
	v_rcp_f32_e32 v103, v103
	v_cndmask_b32_e32 v95, v100, v98, vcc
	v_cmp_gt_f32_e32 vcc, 0, v77
	v_exp_f32_e32 v96, v96
	v_pk_fma_f32 v[76:77], v[102:103], s[0:1], v[122:123] op_sel_hi:[1,0,0]
	v_exp_f32_e32 v97, v97
	v_pk_fma_f32 v[76:77], v[102:103], v[76:77], s[14:15] op_sel_hi:[1,1,0]
	v_cndmask_b32_e32 v98, v101, v99, vcc
	v_pk_fma_f32 v[76:77], v[102:103], v[76:77], s[6:7] op_sel_hi:[1,1,0]
	v_cmp_gt_f32_e32 vcc, 0, v78
	v_pk_fma_f32 v[76:77], v[102:103], v[76:77], s[10:11] op_sel_hi:[1,1,0]
	v_pk_mul_f32 v[90:91], v[72:73], v[72:73]
	v_pk_mul_f32 v[76:77], v[102:103], v[76:77]
	v_pk_mul_f32 v[90:91], v[90:91], s[16:17] op_sel_hi:[1,0]
	v_pk_mul_f32 v[76:77], v[96:97], v[76:77]
	v_pk_fma_f32 v[74:75], v[46:47], v[74:75], v[106:107] op_sel:[1,0,0]
	v_pk_mul_f32 v[96:97], v[78:79], v[76:77]
	v_pk_fma_f32 v[76:77], v[78:79], v[76:77], v[78:79] neg_lo:[1,0,0] neg_hi:[1,0,0]
	v_exp_f32_e32 v90, v90
	v_cndmask_b32_e32 v78, v76, v96, vcc
	v_cmp_gt_f32_e32 vcc, 0, v79
	v_and_b32_e32 v79, 0x7fffffff, v73
	v_cvt_pk_f16_f32 v76, v95, v98
	v_cndmask_b32_e32 v77, v77, v97, vcc
	v_cvt_pk_f16_f32 v77, v78, v77
	v_and_b32_e32 v78, 0x7fffffff, v72
	v_pk_fma_f32 v[78:79], v[78:79], s[8:9], 1.0 op_sel_hi:[1,0,0]
	v_add_u32_e32 v95, 0x3000, v121
	v_rcp_f32_e32 v78, v78
	v_rcp_f32_e32 v79, v79
	ds_write2_b64 v95, v[92:93], v[76:77] offset0:64 offset1:68
	v_exp_f32_e32 v91, v91
	v_and_b32_e32 v93, 0x7fffffff, v75
	v_pk_fma_f32 v[76:77], v[78:79], s[0:1], v[122:123] op_sel_hi:[1,0,0]
	v_and_b32_e32 v92, 0x7fffffff, v74
	v_pk_fma_f32 v[76:77], v[78:79], v[76:77], s[14:15] op_sel_hi:[1,1,0]
	v_pk_fma_f32 v[92:93], v[92:93], s[8:9], 1.0 op_sel_hi:[1,0,0]
	v_pk_fma_f32 v[76:77], v[78:79], v[76:77], s[6:7] op_sel_hi:[1,1,0]
	v_rcp_f32_e32 v92, v92
	v_pk_fma_f32 v[76:77], v[78:79], v[76:77], s[10:11] op_sel_hi:[1,1,0]
	v_rcp_f32_e32 v93, v93
	v_pk_mul_f32 v[76:77], v[78:79], v[76:77]
	v_cmp_gt_f32_e32 vcc, 0, v72
	v_pk_mul_f32 v[76:77], v[90:91], v[76:77]
	v_pk_mul_f32 v[78:79], v[74:75], v[74:75]
	v_pk_mul_f32 v[90:91], v[72:73], v[76:77]
	v_pk_fma_f32 v[76:77], v[72:73], v[76:77], v[72:73] neg_lo:[1,0,0] neg_hi:[1,0,0]
	s_nop 0
	v_cndmask_b32_e32 v90, v76, v90, vcc
	v_cmp_gt_f32_e32 vcc, 0, v73
	v_pk_fma_f32 v[72:73], v[92:93], s[0:1], v[122:123] op_sel_hi:[1,0,0]
	s_nop 0
	v_cndmask_b32_e32 v91, v77, v91, vcc
	v_pk_mul_f32 v[76:77], v[78:79], s[16:17] op_sel_hi:[1,0]
	v_pk_fma_f32 v[72:73], v[92:93], v[72:73], s[14:15] op_sel_hi:[1,1,0]
	v_exp_f32_e32 v76, v76
	v_exp_f32_e32 v77, v77
	v_pk_fma_f32 v[72:73], v[92:93], v[72:73], s[6:7] op_sel_hi:[1,1,0]
	v_cmp_gt_f32_e32 vcc, 0, v74
	v_pk_fma_f32 v[72:73], v[92:93], v[72:73], s[10:11] op_sel_hi:[1,1,0]
	s_nop 0
	v_pk_mul_f32 v[72:73], v[92:93], v[72:73]
	s_nop 0
	v_pk_mul_f32 v[72:73], v[76:77], v[72:73]
	s_nop 0
	v_pk_mul_f32 v[76:77], v[74:75], v[72:73]
	v_pk_fma_f32 v[72:73], v[74:75], v[72:73], v[74:75] neg_lo:[1,0,0] neg_hi:[1,0,0]
	s_nop 0
	v_cndmask_b32_e32 v74, v72, v76, vcc
	v_cmp_gt_f32_e32 vcc, 0, v75
	v_cvt_pk_f16_f32 v72, v90, v91
	v_add_u32_e32 v90, 0x4800, v121
	v_cndmask_b32_e32 v73, v73, v77, vcc
	v_cvt_pk_f16_f32 v73, v74, v73
	global_load_dwordx4 v[76:79], v124, s[18:19] offset:192
	s_waitcnt vmcnt(2)
	v_pk_fma_f32 v[68:69], v[84:85], v[60:61], v[68:69] op_sel_hi:[1,0,1] neg_lo:[1,0,0] neg_hi:[1,0,0]
	ds_write2_b64 v90, v[88:89], v[72:73] offset0:96 offset1:100
	global_load_dwordx4 v[72:75], v124, s[20:21] offset:192
	s_waitcnt vmcnt(2)
	v_pk_fma_f32 v[68:69], v[60:61], v[68:69], v[80:81] op_sel:[1,0,0]
	v_xor_b32_e32 v87, 0x80000000, v87
	v_and_b32_e32 v89, 0x7fffffff, v69
	v_and_b32_e32 v88, 0x7fffffff, v68
	v_pk_fma_f32 v[88:89], v[88:89], s[8:9], 1.0 op_sel_hi:[1,0,0]
	v_xor_b32_e32 v86, 0x80000000, v86
	v_rcp_f32_e32 v88, v88
	v_rcp_f32_e32 v89, v89
	v_pk_mul_f32 v[96:97], v[68:69], v[68:69]
	v_pk_fma_f32 v[70:71], v[86:87], v[60:61], v[70:71] op_sel_hi:[1,0,1]
	v_pk_mul_f32 v[96:97], v[96:97], s[16:17] op_sel_hi:[1,0]
	v_pk_fma_f32 v[92:93], v[88:89], s[0:1], v[122:123] op_sel_hi:[1,0,0]
	v_pk_fma_f32 v[70:71], v[60:61], v[70:71], v[82:83] op_sel:[1,0,0]
	v_pk_fma_f32 v[92:93], v[88:89], v[92:93], s[14:15] op_sel_hi:[1,1,0]
	v_exp_f32_e32 v96, v96
	v_exp_f32_e32 v97, v97
	v_pk_fma_f32 v[92:93], v[88:89], v[92:93], s[6:7] op_sel_hi:[1,1,0]
	v_and_b32_e32 v99, 0x7fffffff, v71
	v_and_b32_e32 v98, 0x7fffffff, v70
	v_pk_fma_f32 v[92:93], v[88:89], v[92:93], s[10:11] op_sel_hi:[1,1,0]
	v_pk_fma_f32 v[98:99], v[98:99], s[8:9], 1.0 op_sel_hi:[1,0,0]
	v_pk_mul_f32 v[88:89], v[88:89], v[92:93]
	v_rcp_f32_e32 v98, v98
	v_rcp_f32_e32 v99, v99
	v_pk_mul_f32 v[88:89], v[96:97], v[88:89]
	v_cmp_gt_f32_e32 vcc, 0, v68
	v_pk_mul_f32 v[96:97], v[68:69], v[88:89]
	v_pk_fma_f32 v[88:89], v[68:69], v[88:89], v[68:69] neg_lo:[1,0,0] neg_hi:[1,0,0]
	v_pk_mul_f32 v[92:93], v[70:71], v[70:71]
	v_cndmask_b32_e32 v91, v88, v96, vcc
	v_cmp_gt_f32_e32 vcc, 0, v69
	v_pk_fma_f32 v[68:69], v[98:99], s[0:1], v[122:123] op_sel_hi:[1,0,0]
	v_pk_fma_f32 v[64:65], v[84:85], v[62:63], v[64:65] op_sel_hi:[1,0,1] neg_lo:[1,0,0] neg_hi:[1,0,0]
	v_cndmask_b32_e32 v96, v89, v97, vcc
	v_pk_mul_f32 v[88:89], v[92:93], s[16:17] op_sel_hi:[1,0]
	v_pk_fma_f32 v[68:69], v[98:99], v[68:69], s[14:15] op_sel_hi:[1,1,0]
	v_exp_f32_e32 v88, v88
	v_exp_f32_e32 v89, v89
	v_pk_fma_f32 v[68:69], v[98:99], v[68:69], s[6:7] op_sel_hi:[1,1,0]
	v_cmp_gt_f32_e32 vcc, 0, v70
	v_pk_fma_f32 v[68:69], v[98:99], v[68:69], s[10:11] op_sel_hi:[1,1,0]
	v_pk_fma_f32 v[64:65], v[62:63], v[64:65], v[80:81] op_sel:[1,0,0]
	v_pk_mul_f32 v[68:69], v[98:99], v[68:69]
	v_pk_mul_f32 v[92:93], v[64:65], v[64:65]
	v_pk_mul_f32 v[68:69], v[88:89], v[68:69]
	v_pk_fma_f32 v[66:67], v[86:87], v[62:63], v[66:67] op_sel_hi:[1,0,1]
	v_pk_mul_f32 v[88:89], v[70:71], v[68:69]
	v_pk_fma_f32 v[68:69], v[70:71], v[68:69], v[70:71] neg_lo:[1,0,0] neg_hi:[1,0,0]
	v_and_b32_e32 v70, 0x7fffffff, v64
	v_cndmask_b32_e32 v88, v68, v88, vcc
	v_cmp_gt_f32_e32 vcc, 0, v71
	v_and_b32_e32 v71, 0x7fffffff, v65
	v_pk_fma_f32 v[70:71], v[70:71], s[8:9], 1.0 op_sel_hi:[1,0,0]
	v_cndmask_b32_e32 v69, v69, v89, vcc
	v_rcp_f32_e32 v70, v70
	v_rcp_f32_e32 v71, v71
	v_cvt_pk_f16_f32 v69, v88, v69
	v_pk_mul_f32 v[92:93], v[92:93], s[16:17] op_sel_hi:[1,0]
	v_pk_fma_f32 v[66:67], v[62:63], v[66:67], v[82:83] op_sel:[1,0,0]
	v_pk_fma_f32 v[88:89], v[70:71], s[0:1], v[122:123] op_sel_hi:[1,0,0]
	v_exp_f32_e32 v92, v92
	v_pk_fma_f32 v[88:89], v[70:71], v[88:89], s[14:15] op_sel_hi:[1,1,0]
	v_exp_f32_e32 v93, v93
	v_cvt_pk_f16_f32 v68, v91, v96
	v_pk_fma_f32 v[88:89], v[70:71], v[88:89], s[6:7] op_sel_hi:[1,1,0]
	v_and_b32_e32 v97, 0x7fffffff, v67
	v_and_b32_e32 v96, 0x7fffffff, v66
	v_pk_fma_f32 v[88:89], v[70:71], v[88:89], s[10:11] op_sel_hi:[1,1,0]
	v_pk_fma_f32 v[96:97], v[96:97], s[8:9], 1.0 op_sel_hi:[1,0,0]
	v_pk_mul_f32 v[70:71], v[70:71], v[88:89]
	v_rcp_f32_e32 v96, v96
	v_rcp_f32_e32 v97, v97
	v_pk_mul_f32 v[70:71], v[92:93], v[70:71]
	v_cmp_gt_f32_e32 vcc, 0, v64
	v_pk_mul_f32 v[92:93], v[64:65], v[70:71]
	v_pk_fma_f32 v[70:71], v[64:65], v[70:71], v[64:65] neg_lo:[1,0,0] neg_hi:[1,0,0]
	v_pk_mul_f32 v[88:89], v[66:67], v[66:67]
	v_cndmask_b32_e32 v91, v70, v92, vcc
	v_cmp_gt_f32_e32 vcc, 0, v65
	v_pk_fma_f32 v[64:65], v[96:97], s[0:1], v[122:123] op_sel_hi:[1,0,0]
	v_pk_fma_f32 v[56:57], v[84:85], v[44:45], v[56:57] op_sel_hi:[1,0,1] neg_lo:[1,0,0] neg_hi:[1,0,0]
	v_cndmask_b32_e32 v92, v71, v93, vcc
	v_pk_mul_f32 v[70:71], v[88:89], s[16:17] op_sel_hi:[1,0]
	v_pk_fma_f32 v[64:65], v[96:97], v[64:65], s[14:15] op_sel_hi:[1,1,0]
	v_exp_f32_e32 v70, v70
	v_exp_f32_e32 v71, v71
	v_pk_fma_f32 v[64:65], v[96:97], v[64:65], s[6:7] op_sel_hi:[1,1,0]
	v_cmp_gt_f32_e32 vcc, 0, v66
	v_pk_fma_f32 v[64:65], v[96:97], v[64:65], s[10:11] op_sel_hi:[1,1,0]
	v_pk_fma_f32 v[56:57], v[44:45], v[56:57], v[80:81] op_sel:[1,0,0]
	v_pk_mul_f32 v[64:65], v[96:97], v[64:65]
	v_pk_mul_f32 v[88:89], v[56:57], v[56:57]
	v_pk_mul_f32 v[64:65], v[70:71], v[64:65]
	v_pk_fma_f32 v[58:59], v[86:87], v[44:45], v[58:59] op_sel_hi:[1,0,1]
	v_pk_mul_f32 v[70:71], v[66:67], v[64:65]
	v_pk_fma_f32 v[64:65], v[66:67], v[64:65], v[66:67] neg_lo:[1,0,0] neg_hi:[1,0,0]
	v_and_b32_e32 v66, 0x7fffffff, v56
	v_cndmask_b32_e32 v70, v64, v70, vcc
	v_cmp_gt_f32_e32 vcc, 0, v67
	v_and_b32_e32 v67, 0x7fffffff, v57
	v_pk_fma_f32 v[66:67], v[66:67], s[8:9], 1.0 op_sel_hi:[1,0,0]
	v_cndmask_b32_e32 v65, v65, v71, vcc
	v_rcp_f32_e32 v66, v66
	v_rcp_f32_e32 v67, v67
	v_cvt_pk_f16_f32 v65, v70, v65
	v_pk_mul_f32 v[88:89], v[88:89], s[16:17] op_sel_hi:[1,0]
	v_pk_fma_f32 v[58:59], v[44:45], v[58:59], v[82:83] op_sel:[1,0,0]
	v_pk_fma_f32 v[70:71], v[66:67], s[0:1], v[122:123] op_sel_hi:[1,0,0]
	v_exp_f32_e32 v88, v88
	v_pk_fma_f32 v[70:71], v[66:67], v[70:71], s[14:15] op_sel_hi:[1,1,0]
	v_exp_f32_e32 v89, v89
	v_cvt_pk_f16_f32 v64, v91, v92
	v_pk_fma_f32 v[70:71], v[66:67], v[70:71], s[6:7] op_sel_hi:[1,1,0]
	v_and_b32_e32 v93, 0x7fffffff, v59
	v_and_b32_e32 v92, 0x7fffffff, v58
	v_pk_fma_f32 v[70:71], v[66:67], v[70:71], s[10:11] op_sel_hi:[1,1,0]
	v_pk_fma_f32 v[92:93], v[92:93], s[8:9], 1.0 op_sel_hi:[1,0,0]
	v_pk_mul_f32 v[66:67], v[66:67], v[70:71]
	v_rcp_f32_e32 v92, v92
	v_rcp_f32_e32 v93, v93
	v_pk_mul_f32 v[66:67], v[88:89], v[66:67]
	v_cmp_gt_f32_e32 vcc, 0, v56
	v_pk_mul_f32 v[88:89], v[56:57], v[66:67]
	v_pk_fma_f32 v[66:67], v[56:57], v[66:67], v[56:57] neg_lo:[1,0,0] neg_hi:[1,0,0]
	v_pk_mul_f32 v[70:71], v[58:59], v[58:59]
	v_cndmask_b32_e32 v88, v66, v88, vcc
	v_cmp_gt_f32_e32 vcc, 0, v57
	v_pk_fma_f32 v[56:57], v[92:93], s[0:1], v[122:123] op_sel_hi:[1,0,0]
	v_pk_fma_f32 v[52:53], v[84:85], v[46:47], v[52:53] op_sel_hi:[1,0,1] neg_lo:[1,0,0] neg_hi:[1,0,0]
	v_cndmask_b32_e32 v89, v67, v89, vcc
	v_pk_mul_f32 v[66:67], v[70:71], s[16:17] op_sel_hi:[1,0]
	v_pk_fma_f32 v[56:57], v[92:93], v[56:57], s[14:15] op_sel_hi:[1,1,0]
	v_exp_f32_e32 v66, v66
	v_exp_f32_e32 v67, v67
	v_pk_fma_f32 v[56:57], v[92:93], v[56:57], s[6:7] op_sel_hi:[1,1,0]
	v_cmp_gt_f32_e32 vcc, 0, v58
	v_pk_fma_f32 v[56:57], v[92:93], v[56:57], s[10:11] op_sel_hi:[1,1,0]
	v_pk_fma_f32 v[52:53], v[46:47], v[52:53], v[80:81] op_sel:[1,0,0]
	v_pk_mul_f32 v[56:57], v[92:93], v[56:57]
	v_pk_mul_f32 v[70:71], v[52:53], v[52:53]
	v_pk_mul_f32 v[56:57], v[66:67], v[56:57]
	v_pk_fma_f32 v[54:55], v[86:87], v[46:47], v[54:55] op_sel_hi:[1,0,1]
	v_pk_mul_f32 v[66:67], v[58:59], v[56:57]
	v_pk_fma_f32 v[56:57], v[58:59], v[56:57], v[58:59] neg_lo:[1,0,0] neg_hi:[1,0,0]
	v_and_b32_e32 v58, 0x7fffffff, v52
	v_cndmask_b32_e32 v66, v56, v66, vcc
	v_cmp_gt_f32_e32 vcc, 0, v59
	v_and_b32_e32 v59, 0x7fffffff, v53
	v_pk_fma_f32 v[58:59], v[58:59], s[8:9], 1.0 op_sel_hi:[1,0,0]
	v_cndmask_b32_e32 v57, v57, v67, vcc
	v_rcp_f32_e32 v58, v58
	v_rcp_f32_e32 v59, v59
	v_cvt_pk_f16_f32 v57, v66, v57
	v_pk_mul_f32 v[70:71], v[70:71], s[16:17] op_sel_hi:[1,0]
	v_pk_fma_f32 v[54:55], v[46:47], v[54:55], v[82:83] op_sel:[1,0,0]
	v_pk_fma_f32 v[66:67], v[58:59], s[0:1], v[122:123] op_sel_hi:[1,0,0]
	v_exp_f32_e32 v70, v70
	v_pk_fma_f32 v[66:67], v[58:59], v[66:67], s[14:15] op_sel_hi:[1,1,0]
	v_exp_f32_e32 v71, v71
	v_pk_fma_f32 v[66:67], v[58:59], v[66:67], s[6:7] op_sel_hi:[1,1,0]
	v_and_b32_e32 v81, 0x7fffffff, v55
	v_and_b32_e32 v80, 0x7fffffff, v54
	v_pk_fma_f32 v[66:67], v[58:59], v[66:67], s[10:11] op_sel_hi:[1,1,0]
	v_pk_fma_f32 v[80:81], v[80:81], s[8:9], 1.0 op_sel_hi:[1,0,0]
	v_pk_mul_f32 v[58:59], v[58:59], v[66:67]
	v_rcp_f32_e32 v80, v80
	v_rcp_f32_e32 v81, v81
	v_pk_mul_f32 v[58:59], v[70:71], v[58:59]
	v_cmp_gt_f32_e32 vcc, 0, v52
	v_pk_mul_f32 v[70:71], v[52:53], v[58:59]
	v_pk_fma_f32 v[58:59], v[52:53], v[58:59], v[52:53] neg_lo:[1,0,0] neg_hi:[1,0,0]
	v_pk_mul_f32 v[66:67], v[54:55], v[54:55]
	v_cndmask_b32_e32 v70, v58, v70, vcc
	v_cmp_gt_f32_e32 vcc, 0, v53
	v_pk_fma_f32 v[52:53], v[80:81], s[0:1], v[122:123] op_sel_hi:[1,0,0]
	s_waitcnt vmcnt(1)
	v_pk_fma_f32 v[40:41], v[76:77], v[62:63], v[40:41] op_sel_hi:[1,0,1] neg_lo:[1,0,0] neg_hi:[1,0,0]
	v_cndmask_b32_e32 v71, v59, v71, vcc
	v_pk_mul_f32 v[58:59], v[66:67], s[16:17] op_sel_hi:[1,0]
	v_pk_fma_f32 v[52:53], v[80:81], v[52:53], s[14:15] op_sel_hi:[1,1,0]
	v_exp_f32_e32 v58, v58
	v_exp_f32_e32 v59, v59
	v_pk_fma_f32 v[52:53], v[80:81], v[52:53], s[6:7] op_sel_hi:[1,1,0]
	v_cmp_gt_f32_e32 vcc, 0, v54
	v_pk_fma_f32 v[52:53], v[80:81], v[52:53], s[10:11] op_sel_hi:[1,1,0]
	s_waitcnt vmcnt(0)
	v_pk_fma_f32 v[40:41], v[62:63], v[40:41], v[72:73] op_sel:[1,0,0]
	v_pk_mul_f32 v[52:53], v[80:81], v[52:53]
	v_pk_fma_f32 v[36:37], v[76:77], v[44:45], v[36:37] op_sel_hi:[1,0,1] neg_lo:[1,0,0] neg_hi:[1,0,0]
	v_pk_mul_f32 v[52:53], v[58:59], v[52:53]
	v_pk_fma_f32 v[32:33], v[76:77], v[46:47], v[32:33] op_sel_hi:[1,0,1] neg_lo:[1,0,0] neg_hi:[1,0,0]
	v_pk_mul_f32 v[58:59], v[54:55], v[52:53]
	v_pk_fma_f32 v[52:53], v[54:55], v[52:53], v[54:55] neg_lo:[1,0,0] neg_hi:[1,0,0]
	v_pk_fma_f32 v[32:33], v[46:47], v[32:33], v[72:73] op_sel:[1,0,0]
	v_cndmask_b32_e32 v54, v52, v58, vcc
	v_cmp_gt_f32_e32 vcc, 0, v55
	v_cvt_pk_f16_f32 v52, v70, v71
	v_cvt_pk_f16_f32 v56, v88, v89
	v_cndmask_b32_e32 v53, v53, v59, vcc
	v_cvt_pk_f16_f32 v53, v54, v53
	v_pk_fma_f32 v[54:55], v[76:77], v[60:61], v[48:49] op_sel_hi:[1,0,1] neg_lo:[1,0,0] neg_hi:[1,0,0]
	v_xor_b32_e32 v49, 0x80000000, v79
	v_pk_fma_f32 v[54:55], v[60:61], v[54:55], v[72:73] op_sel:[1,0,0]
	v_xor_b32_e32 v48, 0x80000000, v78
	v_and_b32_e32 v59, 0x7fffffff, v55
	v_and_b32_e32 v58, 0x7fffffff, v54
	v_pk_fma_f32 v[58:59], v[58:59], s[8:9], 1.0 op_sel_hi:[1,0,0]
	v_pk_mul_f32 v[70:71], v[54:55], v[54:55]
	v_rcp_f32_e32 v58, v58
	v_rcp_f32_e32 v59, v59
	v_pk_fma_f32 v[50:51], v[48:49], v[60:61], v[50:51] op_sel_hi:[1,0,1]
	v_pk_mul_f32 v[70:71], v[70:71], s[16:17] op_sel_hi:[1,0]
	v_pk_fma_f32 v[50:51], v[60:61], v[50:51], v[74:75] op_sel:[1,0,0]
	v_pk_fma_f32 v[66:67], v[58:59], s[0:1], v[122:123] op_sel_hi:[1,0,0]
	v_exp_f32_e32 v70, v70
	v_pk_fma_f32 v[66:67], v[58:59], v[66:67], s[14:15] op_sel_hi:[1,1,0]
	v_exp_f32_e32 v71, v71
	v_pk_fma_f32 v[66:67], v[58:59], v[66:67], s[6:7] op_sel_hi:[1,1,0]
	v_and_b32_e32 v79, 0x7fffffff, v51
	v_and_b32_e32 v78, 0x7fffffff, v50
	v_pk_fma_f32 v[66:67], v[58:59], v[66:67], s[10:11] op_sel_hi:[1,1,0]
	v_pk_fma_f32 v[78:79], v[78:79], s[8:9], 1.0 op_sel_hi:[1,0,0]
	v_pk_mul_f32 v[58:59], v[58:59], v[66:67]
	v_rcp_f32_e32 v78, v78
	v_rcp_f32_e32 v79, v79
	v_pk_mul_f32 v[58:59], v[70:71], v[58:59]
	v_cmp_gt_f32_e32 vcc, 0, v54
	v_pk_mul_f32 v[70:71], v[54:55], v[58:59]
	v_pk_fma_f32 v[58:59], v[54:55], v[58:59], v[54:55] neg_lo:[1,0,0] neg_hi:[1,0,0]
	v_pk_mul_f32 v[66:67], v[50:51], v[50:51]
	v_cndmask_b32_e32 v70, v58, v70, vcc
	v_cmp_gt_f32_e32 vcc, 0, v55
	v_pk_fma_f32 v[54:55], v[78:79], s[0:1], v[122:123] op_sel_hi:[1,0,0]
	v_pk_fma_f32 v[42:43], v[48:49], v[62:63], v[42:43] op_sel_hi:[1,0,1]
	v_cndmask_b32_e32 v71, v59, v71, vcc
	v_pk_mul_f32 v[58:59], v[66:67], s[16:17] op_sel_hi:[1,0]
	v_pk_fma_f32 v[54:55], v[78:79], v[54:55], s[14:15] op_sel_hi:[1,1,0]
	v_exp_f32_e32 v58, v58
	v_exp_f32_e32 v59, v59
	v_pk_fma_f32 v[54:55], v[78:79], v[54:55], s[6:7] op_sel_hi:[1,1,0]
	v_cmp_gt_f32_e32 vcc, 0, v50
	v_pk_fma_f32 v[54:55], v[78:79], v[54:55], s[10:11] op_sel_hi:[1,1,0]
	v_pk_fma_f32 v[42:43], v[62:63], v[42:43], v[74:75] op_sel:[1,0,0]
	v_pk_mul_f32 v[54:55], v[78:79], v[54:55]
	v_and_b32_e32 v67, 0x7fffffff, v43
	v_pk_mul_f32 v[54:55], v[58:59], v[54:55]
	v_and_b32_e32 v66, 0x7fffffff, v42
	v_pk_mul_f32 v[58:59], v[50:51], v[54:55]
	v_pk_fma_f32 v[54:55], v[50:51], v[54:55], v[50:51] neg_lo:[1,0,0] neg_hi:[1,0,0]
	v_cvt_pk_f16_f32 v50, v70, v71
	v_cndmask_b32_e32 v54, v54, v58, vcc
	v_cmp_gt_f32_e32 vcc, 0, v51
	v_pk_fma_f32 v[66:67], v[66:67], s[8:9], 1.0 op_sel_hi:[1,0,0]
	v_pk_fma_f32 v[38:39], v[48:49], v[44:45], v[38:39] op_sel_hi:[1,0,1]
	v_cndmask_b32_e32 v51, v55, v59, vcc
	v_cvt_pk_f16_f32 v51, v54, v51
	v_and_b32_e32 v55, 0x7fffffff, v41
	v_and_b32_e32 v54, 0x7fffffff, v40
	v_pk_fma_f32 v[54:55], v[54:55], s[8:9], 1.0 op_sel_hi:[1,0,0]
	v_pk_mul_f32 v[58:59], v[40:41], v[40:41]
	v_rcp_f32_e32 v54, v54
	v_rcp_f32_e32 v55, v55
	ds_write2_b64 v121, v[68:69], v[50:51] offset0:8 offset1:12
	v_pk_mul_f32 v[58:59], v[58:59], s[16:17] op_sel_hi:[1,0]
	v_rcp_f32_e32 v66, v66
	v_pk_fma_f32 v[50:51], v[54:55], s[0:1], v[122:123] op_sel_hi:[1,0,0]
	v_exp_f32_e32 v58, v58
	v_pk_fma_f32 v[50:51], v[54:55], v[50:51], s[14:15] op_sel_hi:[1,1,0]
	v_exp_f32_e32 v59, v59
	v_pk_fma_f32 v[50:51], v[54:55], v[50:51], s[6:7] op_sel_hi:[1,1,0]
	v_rcp_f32_e32 v67, v67
	v_pk_fma_f32 v[50:51], v[54:55], v[50:51], s[10:11] op_sel_hi:[1,1,0]
	v_cmp_gt_f32_e32 vcc, 0, v40
	v_pk_mul_f32 v[50:51], v[54:55], v[50:51]
	v_pk_mul_f32 v[54:55], v[42:43], v[42:43]
	v_pk_mul_f32 v[50:51], v[58:59], v[50:51]
	v_pk_fma_f32 v[34:35], v[48:49], v[46:47], v[34:35] op_sel_hi:[1,0,1]
	v_pk_mul_f32 v[58:59], v[40:41], v[50:51]
	v_pk_fma_f32 v[50:51], v[40:41], v[50:51], v[40:41] neg_lo:[1,0,0] neg_hi:[1,0,0]
	v_pk_fma_f32 v[34:35], v[46:47], v[34:35], v[74:75] op_sel:[1,0,0]
	v_cndmask_b32_e32 v58, v50, v58, vcc
	v_cmp_gt_f32_e32 vcc, 0, v41
	v_pk_fma_f32 v[40:41], v[66:67], s[0:1], v[122:123] op_sel_hi:[1,0,0]
	s_nop 0
	v_cndmask_b32_e32 v59, v51, v59, vcc
	v_pk_mul_f32 v[50:51], v[54:55], s[16:17] op_sel_hi:[1,0]
	v_pk_fma_f32 v[40:41], v[66:67], v[40:41], s[14:15] op_sel_hi:[1,1,0]
	v_exp_f32_e32 v50, v50
	v_exp_f32_e32 v51, v51
	v_pk_fma_f32 v[40:41], v[66:67], v[40:41], s[6:7] op_sel_hi:[1,1,0]
	v_cmp_gt_f32_e32 vcc, 0, v42
	v_pk_fma_f32 v[40:41], v[66:67], v[40:41], s[10:11] op_sel_hi:[1,1,0]
	v_pk_fma_f32 v[54:55], v[44:45], v[38:39], v[74:75] op_sel:[1,0,0]
	v_pk_mul_f32 v[40:41], v[66:67], v[40:41]
	v_and_b32_e32 v69, 0x7fffffff, v55
	v_pk_mul_f32 v[40:41], v[50:51], v[40:41]
	v_and_b32_e32 v68, 0x7fffffff, v54
	v_pk_mul_f32 v[50:51], v[42:43], v[40:41]
	v_pk_fma_f32 v[40:41], v[42:43], v[40:41], v[42:43] neg_lo:[1,0,0] neg_hi:[1,0,0]
	v_pk_fma_f32 v[68:69], v[68:69], s[8:9], 1.0 op_sel_hi:[1,0,0]
	v_cndmask_b32_e32 v42, v40, v50, vcc
	v_cmp_gt_f32_e32 vcc, 0, v43
	v_cvt_pk_f16_f32 v40, v58, v59
	v_rcp_f32_e32 v68, v68
	v_cndmask_b32_e32 v41, v41, v51, vcc
	v_pk_fma_f32 v[50:51], v[44:45], v[36:37], v[72:73] op_sel:[1,0,0]
	v_cvt_pk_f16_f32 v41, v42, v41
	v_and_b32_e32 v37, 0x7fffffff, v51
	v_and_b32_e32 v36, 0x7fffffff, v50
	v_pk_fma_f32 v[36:37], v[36:37], s[8:9], 1.0 op_sel_hi:[1,0,0]
	ds_write2_b64 v94, v[64:65], v[40:41] offset0:40 offset1:44
	v_rcp_f32_e32 v36, v36
	v_rcp_f32_e32 v37, v37
	v_pk_mul_f32 v[40:41], v[50:51], v[50:51]
	v_rcp_f32_e32 v69, v69
	v_pk_mul_f32 v[40:41], v[40:41], s[16:17] op_sel_hi:[1,0]
	v_pk_fma_f32 v[38:39], v[36:37], s[0:1], v[122:123] op_sel_hi:[1,0,0]
	v_exp_f32_e32 v40, v40
	v_pk_fma_f32 v[38:39], v[36:37], v[38:39], s[14:15] op_sel_hi:[1,1,0]
	v_exp_f32_e32 v41, v41
	v_pk_fma_f32 v[38:39], v[36:37], v[38:39], s[6:7] op_sel_hi:[1,1,0]
	v_pk_mul_f32 v[58:59], v[54:55], v[54:55]
	v_pk_fma_f32 v[38:39], v[36:37], v[38:39], s[10:11] op_sel_hi:[1,1,0]
	v_cmp_gt_f32_e32 vcc, 0, v50
	v_pk_mul_f32 v[36:37], v[36:37], v[38:39]
	v_pk_mul_f32 v[58:59], v[58:59], s[16:17] op_sel_hi:[1,0]
	v_pk_mul_f32 v[36:37], v[40:41], v[36:37]
	global_load_dwordx4 v[40:43], v124, s[18:19] offset:256
	v_pk_mul_f32 v[64:65], v[50:51], v[36:37]
	v_pk_fma_f32 v[66:67], v[50:51], v[36:37], v[50:51] neg_lo:[1,0,0] neg_hi:[1,0,0]
	global_load_dwordx4 v[36:39], v124, s[20:21] offset:256
	v_cndmask_b32_e32 v64, v66, v64, vcc
	v_cmp_gt_f32_e32 vcc, 0, v51
	v_pk_fma_f32 v[50:51], v[68:69], s[0:1], v[122:123] op_sel_hi:[1,0,0]
	v_exp_f32_e32 v58, v58
	v_pk_fma_f32 v[50:51], v[68:69], v[50:51], s[14:15] op_sel_hi:[1,1,0]
	v_exp_f32_e32 v59, v59
	v_pk_fma_f32 v[50:51], v[68:69], v[50:51], s[6:7] op_sel_hi:[1,1,0]
	v_cndmask_b32_e32 v65, v67, v65, vcc
	v_pk_fma_f32 v[50:51], v[68:69], v[50:51], s[10:11] op_sel_hi:[1,1,0]
	v_cmp_gt_f32_e32 vcc, 0, v54
	v_pk_mul_f32 v[50:51], v[68:69], v[50:51]
	s_nop 0
	v_pk_mul_f32 v[50:51], v[58:59], v[50:51]
	s_nop 0
	v_pk_mul_f32 v[58:59], v[54:55], v[50:51]
	v_pk_fma_f32 v[50:51], v[54:55], v[50:51], v[54:55] neg_lo:[1,0,0] neg_hi:[1,0,0]
	s_nop 0
	v_cndmask_b32_e32 v54, v50, v58, vcc
	v_cmp_gt_f32_e32 vcc, 0, v55
	v_and_b32_e32 v55, 0x7fffffff, v33
	v_cvt_pk_f16_f32 v50, v64, v65
	v_cndmask_b32_e32 v51, v51, v59, vcc
	v_cvt_pk_f16_f32 v51, v54, v51
	v_and_b32_e32 v54, 0x7fffffff, v32
	v_pk_fma_f32 v[54:55], v[54:55], s[8:9], 1.0 op_sel_hi:[1,0,0]
	ds_write2_b64 v95, v[56:57], v[50:51] offset0:72 offset1:76
	v_rcp_f32_e32 v54, v54
	v_rcp_f32_e32 v55, v55
	v_pk_mul_f32 v[50:51], v[32:33], v[32:33]
	v_and_b32_e32 v57, 0x7fffffff, v35
	v_pk_mul_f32 v[50:51], v[50:51], s[16:17] op_sel_hi:[1,0]
	v_pk_fma_f32 v[48:49], v[54:55], s[0:1], v[122:123] op_sel_hi:[1,0,0]
	v_exp_f32_e32 v50, v50
	v_pk_fma_f32 v[48:49], v[54:55], v[48:49], s[14:15] op_sel_hi:[1,1,0]
	v_exp_f32_e32 v51, v51
	v_pk_fma_f32 v[48:49], v[54:55], v[48:49], s[6:7] op_sel_hi:[1,1,0]
	v_and_b32_e32 v56, 0x7fffffff, v34
	v_pk_fma_f32 v[48:49], v[54:55], v[48:49], s[10:11] op_sel_hi:[1,1,0]
	v_pk_fma_f32 v[56:57], v[56:57], s[8:9], 1.0 op_sel_hi:[1,0,0]
	v_pk_mul_f32 v[48:49], v[54:55], v[48:49]
	v_rcp_f32_e32 v56, v56
	v_rcp_f32_e32 v57, v57
	v_pk_mul_f32 v[48:49], v[50:51], v[48:49]
	v_cmp_gt_f32_e32 vcc, 0, v32
	v_pk_mul_f32 v[50:51], v[32:33], v[48:49]
	v_pk_fma_f32 v[48:49], v[32:33], v[48:49], v[32:33] neg_lo:[1,0,0] neg_hi:[1,0,0]
	v_pk_mul_f32 v[54:55], v[34:35], v[34:35]
	v_cndmask_b32_e32 v50, v48, v50, vcc
	v_cmp_gt_f32_e32 vcc, 0, v33
	v_pk_fma_f32 v[32:33], v[56:57], s[0:1], v[122:123] op_sel_hi:[1,0,0]
	s_nop 0
	v_cndmask_b32_e32 v51, v49, v51, vcc
	v_pk_mul_f32 v[48:49], v[54:55], s[16:17] op_sel_hi:[1,0]
	v_pk_fma_f32 v[32:33], v[56:57], v[32:33], s[14:15] op_sel_hi:[1,1,0]
	v_exp_f32_e32 v48, v48
	v_exp_f32_e32 v49, v49
	v_pk_fma_f32 v[32:33], v[56:57], v[32:33], s[6:7] op_sel_hi:[1,1,0]
	v_cmp_gt_f32_e32 vcc, 0, v34
	v_pk_fma_f32 v[32:33], v[56:57], v[32:33], s[10:11] op_sel_hi:[1,1,0]
	s_nop 0
	v_pk_mul_f32 v[32:33], v[56:57], v[32:33]
	s_nop 0
	v_pk_mul_f32 v[32:33], v[48:49], v[32:33]
	s_nop 0
	v_pk_mul_f32 v[48:49], v[34:35], v[32:33]
	v_pk_fma_f32 v[32:33], v[34:35], v[32:33], v[34:35] neg_lo:[1,0,0] neg_hi:[1,0,0]
	s_nop 0
	v_cndmask_b32_e32 v34, v32, v48, vcc
	v_cmp_gt_f32_e32 vcc, 0, v35
	v_cvt_pk_f16_f32 v32, v50, v51
	s_nop 0
	v_cndmask_b32_e32 v33, v33, v49, vcc
	v_cvt_pk_f16_f32 v33, v34, v33
	global_load_dwordx4 v[48:51], v124, s[18:19] offset:320
	ds_write2_b64 v90, v[52:53], v[32:33] offset0:104 offset1:108
	global_load_dwordx4 v[32:35], v124, s[20:21] offset:320
	s_waitcnt vmcnt(3)
	v_pk_fma_f32 v[28:29], v[40:41], v[60:61], v[28:29] op_sel_hi:[1,0,1] neg_lo:[1,0,0] neg_hi:[1,0,0]
	v_xor_b32_e32 v43, 0x80000000, v43
	v_xor_b32_e32 v42, 0x80000000, v42
	s_waitcnt vmcnt(2)
	v_pk_fma_f32 v[28:29], v[60:61], v[28:29], v[36:37] op_sel:[1,0,0]
	v_pk_fma_f32 v[30:31], v[42:43], v[60:61], v[30:31] op_sel_hi:[1,0,1]
	v_and_b32_e32 v53, 0x7fffffff, v29
	v_and_b32_e32 v52, 0x7fffffff, v28
	v_pk_fma_f32 v[52:53], v[52:53], s[8:9], 1.0 op_sel_hi:[1,0,0]
	v_pk_mul_f32 v[56:57], v[28:29], v[28:29]
	v_rcp_f32_e32 v52, v52
	v_rcp_f32_e32 v53, v53
	v_pk_mul_f32 v[56:57], v[56:57], s[16:17] op_sel_hi:[1,0]
	v_pk_fma_f32 v[30:31], v[60:61], v[30:31], v[38:39] op_sel:[1,0,0]
	v_exp_f32_e32 v56, v56
	v_pk_fma_f32 v[54:55], v[52:53], s[0:1], v[122:123] op_sel_hi:[1,0,0]
	v_exp_f32_e32 v57, v57
	v_pk_fma_f32 v[54:55], v[52:53], v[54:55], s[14:15] op_sel_hi:[1,1,0]
	v_and_b32_e32 v59, 0x7fffffff, v31
	v_pk_fma_f32 v[54:55], v[52:53], v[54:55], s[6:7] op_sel_hi:[1,1,0]
	v_and_b32_e32 v58, 0x7fffffff, v30
	v_pk_fma_f32 v[54:55], v[52:53], v[54:55], s[10:11] op_sel_hi:[1,1,0]
	v_pk_fma_f32 v[58:59], v[58:59], s[8:9], 1.0 op_sel_hi:[1,0,0]
	v_pk_mul_f32 v[52:53], v[52:53], v[54:55]
	v_rcp_f32_e32 v58, v58
	v_rcp_f32_e32 v59, v59
	v_pk_mul_f32 v[52:53], v[56:57], v[52:53]
	v_cmp_gt_f32_e32 vcc, 0, v28
	v_pk_mul_f32 v[56:57], v[28:29], v[52:53]
	v_pk_fma_f32 v[52:53], v[28:29], v[52:53], v[28:29] neg_lo:[1,0,0] neg_hi:[1,0,0]
	v_pk_mul_f32 v[54:55], v[30:31], v[30:31]
	v_cndmask_b32_e32 v56, v52, v56, vcc
	v_cmp_gt_f32_e32 vcc, 0, v29
	v_pk_fma_f32 v[28:29], v[58:59], s[0:1], v[122:123] op_sel_hi:[1,0,0]
	v_pk_fma_f32 v[24:25], v[40:41], v[62:63], v[24:25] op_sel_hi:[1,0,1] neg_lo:[1,0,0] neg_hi:[1,0,0]
	v_cndmask_b32_e32 v57, v53, v57, vcc
	v_pk_mul_f32 v[52:53], v[54:55], s[16:17] op_sel_hi:[1,0]
	v_pk_fma_f32 v[28:29], v[58:59], v[28:29], s[14:15] op_sel_hi:[1,1,0]
	v_exp_f32_e32 v52, v52
	v_exp_f32_e32 v53, v53
	v_pk_fma_f32 v[28:29], v[58:59], v[28:29], s[6:7] op_sel_hi:[1,1,0]
	v_cmp_gt_f32_e32 vcc, 0, v30
	v_pk_fma_f32 v[28:29], v[58:59], v[28:29], s[10:11] op_sel_hi:[1,1,0]
	v_pk_fma_f32 v[24:25], v[62:63], v[24:25], v[36:37] op_sel:[1,0,0]
	v_pk_mul_f32 v[28:29], v[58:59], v[28:29]
	v_pk_mul_f32 v[54:55], v[24:25], v[24:25]
	v_pk_mul_f32 v[28:29], v[52:53], v[28:29]
	v_pk_fma_f32 v[26:27], v[42:43], v[62:63], v[26:27] op_sel_hi:[1,0,1]
	v_pk_mul_f32 v[52:53], v[30:31], v[28:29]
	v_pk_fma_f32 v[28:29], v[30:31], v[28:29], v[30:31] neg_lo:[1,0,0] neg_hi:[1,0,0]
	v_and_b32_e32 v30, 0x7fffffff, v24
	v_cndmask_b32_e32 v52, v28, v52, vcc
	v_cmp_gt_f32_e32 vcc, 0, v31
	v_and_b32_e32 v31, 0x7fffffff, v25
	v_pk_fma_f32 v[30:31], v[30:31], s[8:9], 1.0 op_sel_hi:[1,0,0]
	v_cndmask_b32_e32 v29, v29, v53, vcc
	v_rcp_f32_e32 v30, v30
	v_rcp_f32_e32 v31, v31
	v_cvt_pk_f16_f32 v29, v52, v29
	v_pk_mul_f32 v[54:55], v[54:55], s[16:17] op_sel_hi:[1,0]
	v_pk_fma_f32 v[26:27], v[62:63], v[26:27], v[38:39] op_sel:[1,0,0]
	v_pk_fma_f32 v[52:53], v[30:31], s[0:1], v[122:123] op_sel_hi:[1,0,0]
	v_exp_f32_e32 v54, v54
	v_pk_fma_f32 v[52:53], v[30:31], v[52:53], s[14:15] op_sel_hi:[1,1,0]
	v_exp_f32_e32 v55, v55
	v_cvt_pk_f16_f32 v28, v56, v57
	v_pk_fma_f32 v[52:53], v[30:31], v[52:53], s[6:7] op_sel_hi:[1,1,0]
	v_and_b32_e32 v57, 0x7fffffff, v27
	v_and_b32_e32 v56, 0x7fffffff, v26
	v_pk_fma_f32 v[52:53], v[30:31], v[52:53], s[10:11] op_sel_hi:[1,1,0]
	v_pk_fma_f32 v[56:57], v[56:57], s[8:9], 1.0 op_sel_hi:[1,0,0]
	v_pk_mul_f32 v[30:31], v[30:31], v[52:53]
	v_rcp_f32_e32 v56, v56
	v_rcp_f32_e32 v57, v57
	v_pk_mul_f32 v[30:31], v[54:55], v[30:31]
	v_cmp_gt_f32_e32 vcc, 0, v24
	v_pk_mul_f32 v[54:55], v[24:25], v[30:31]
	v_pk_fma_f32 v[30:31], v[24:25], v[30:31], v[24:25] neg_lo:[1,0,0] neg_hi:[1,0,0]
	v_pk_mul_f32 v[52:53], v[26:27], v[26:27]
	v_cndmask_b32_e32 v54, v30, v54, vcc
	v_cmp_gt_f32_e32 vcc, 0, v25
	v_pk_fma_f32 v[24:25], v[56:57], s[0:1], v[122:123] op_sel_hi:[1,0,0]
	v_pk_fma_f32 v[20:21], v[40:41], v[44:45], v[20:21] op_sel_hi:[1,0,1] neg_lo:[1,0,0] neg_hi:[1,0,0]
	v_cndmask_b32_e32 v55, v31, v55, vcc
	v_pk_mul_f32 v[30:31], v[52:53], s[16:17] op_sel_hi:[1,0]
	v_pk_fma_f32 v[24:25], v[56:57], v[24:25], s[14:15] op_sel_hi:[1,1,0]
	v_exp_f32_e32 v30, v30
	v_exp_f32_e32 v31, v31
	v_pk_fma_f32 v[24:25], v[56:57], v[24:25], s[6:7] op_sel_hi:[1,1,0]
	v_cmp_gt_f32_e32 vcc, 0, v26
	v_pk_fma_f32 v[24:25], v[56:57], v[24:25], s[10:11] op_sel_hi:[1,1,0]
	v_pk_fma_f32 v[20:21], v[44:45], v[20:21], v[36:37] op_sel:[1,0,0]
	v_pk_mul_f32 v[24:25], v[56:57], v[24:25]
	v_pk_mul_f32 v[52:53], v[20:21], v[20:21]
	v_pk_mul_f32 v[24:25], v[30:31], v[24:25]
	v_pk_fma_f32 v[22:23], v[42:43], v[44:45], v[22:23] op_sel_hi:[1,0,1]
	v_pk_mul_f32 v[30:31], v[26:27], v[24:25]
	v_pk_fma_f32 v[24:25], v[26:27], v[24:25], v[26:27] neg_lo:[1,0,0] neg_hi:[1,0,0]
	v_and_b32_e32 v26, 0x7fffffff, v20
	v_cndmask_b32_e32 v30, v24, v30, vcc
	v_cmp_gt_f32_e32 vcc, 0, v27
	v_and_b32_e32 v27, 0x7fffffff, v21
	v_pk_fma_f32 v[26:27], v[26:27], s[8:9], 1.0 op_sel_hi:[1,0,0]
	v_cndmask_b32_e32 v25, v25, v31, vcc
	v_rcp_f32_e32 v26, v26
	v_rcp_f32_e32 v27, v27
	v_cvt_pk_f16_f32 v25, v30, v25
	v_pk_mul_f32 v[52:53], v[52:53], s[16:17] op_sel_hi:[1,0]
	v_pk_fma_f32 v[22:23], v[44:45], v[22:23], v[38:39] op_sel:[1,0,0]
	v_pk_fma_f32 v[30:31], v[26:27], s[0:1], v[122:123] op_sel_hi:[1,0,0]
	v_exp_f32_e32 v52, v52
	v_pk_fma_f32 v[30:31], v[26:27], v[30:31], s[14:15] op_sel_hi:[1,1,0]
	v_exp_f32_e32 v53, v53
	v_cvt_pk_f16_f32 v24, v54, v55
	v_pk_fma_f32 v[30:31], v[26:27], v[30:31], s[6:7] op_sel_hi:[1,1,0]
	v_and_b32_e32 v55, 0x7fffffff, v23
	v_and_b32_e32 v54, 0x7fffffff, v22
	v_pk_fma_f32 v[30:31], v[26:27], v[30:31], s[10:11] op_sel_hi:[1,1,0]
	v_pk_fma_f32 v[54:55], v[54:55], s[8:9], 1.0 op_sel_hi:[1,0,0]
	v_pk_mul_f32 v[26:27], v[26:27], v[30:31]
	v_rcp_f32_e32 v54, v54
	v_rcp_f32_e32 v55, v55
	v_pk_mul_f32 v[26:27], v[52:53], v[26:27]
	v_cmp_gt_f32_e32 vcc, 0, v20
	v_pk_mul_f32 v[52:53], v[20:21], v[26:27]
	v_pk_fma_f32 v[26:27], v[20:21], v[26:27], v[20:21] neg_lo:[1,0,0] neg_hi:[1,0,0]
	v_pk_mul_f32 v[30:31], v[22:23], v[22:23]
	v_cndmask_b32_e32 v52, v26, v52, vcc
	v_cmp_gt_f32_e32 vcc, 0, v21
	v_pk_fma_f32 v[20:21], v[54:55], s[0:1], v[122:123] op_sel_hi:[1,0,0]
	v_pk_fma_f32 v[16:17], v[40:41], v[46:47], v[16:17] op_sel_hi:[1,0,1] neg_lo:[1,0,0] neg_hi:[1,0,0]
	v_cndmask_b32_e32 v53, v27, v53, vcc
	v_pk_mul_f32 v[26:27], v[30:31], s[16:17] op_sel_hi:[1,0]
	v_pk_fma_f32 v[20:21], v[54:55], v[20:21], s[14:15] op_sel_hi:[1,1,0]
	v_exp_f32_e32 v26, v26
	v_exp_f32_e32 v27, v27
	v_pk_fma_f32 v[20:21], v[54:55], v[20:21], s[6:7] op_sel_hi:[1,1,0]
	v_cmp_gt_f32_e32 vcc, 0, v22
	v_pk_fma_f32 v[20:21], v[54:55], v[20:21], s[10:11] op_sel_hi:[1,1,0]
	v_pk_fma_f32 v[16:17], v[46:47], v[16:17], v[36:37] op_sel:[1,0,0]
	v_pk_mul_f32 v[20:21], v[54:55], v[20:21]
	v_pk_mul_f32 v[30:31], v[16:17], v[16:17]
	v_pk_mul_f32 v[20:21], v[26:27], v[20:21]
	v_pk_fma_f32 v[18:19], v[42:43], v[46:47], v[18:19] op_sel_hi:[1,0,1]
	v_pk_mul_f32 v[26:27], v[22:23], v[20:21]
	v_pk_fma_f32 v[20:21], v[22:23], v[20:21], v[22:23] neg_lo:[1,0,0] neg_hi:[1,0,0]
	v_and_b32_e32 v22, 0x7fffffff, v16
	v_cndmask_b32_e32 v26, v20, v26, vcc
	v_cmp_gt_f32_e32 vcc, 0, v23
	v_and_b32_e32 v23, 0x7fffffff, v17
	v_pk_fma_f32 v[22:23], v[22:23], s[8:9], 1.0 op_sel_hi:[1,0,0]
	v_cndmask_b32_e32 v21, v21, v27, vcc
	v_rcp_f32_e32 v22, v22
	v_rcp_f32_e32 v23, v23
	v_cvt_pk_f16_f32 v21, v26, v21
	v_pk_mul_f32 v[30:31], v[30:31], s[16:17] op_sel_hi:[1,0]
	v_pk_fma_f32 v[18:19], v[46:47], v[18:19], v[38:39] op_sel:[1,0,0]
	v_pk_fma_f32 v[26:27], v[22:23], s[0:1], v[122:123] op_sel_hi:[1,0,0]
	v_exp_f32_e32 v30, v30
	v_pk_fma_f32 v[26:27], v[22:23], v[26:27], s[14:15] op_sel_hi:[1,1,0]
	v_exp_f32_e32 v31, v31
	v_pk_fma_f32 v[26:27], v[22:23], v[26:27], s[6:7] op_sel_hi:[1,1,0]
	v_and_b32_e32 v37, 0x7fffffff, v19
	v_and_b32_e32 v36, 0x7fffffff, v18
	v_pk_fma_f32 v[26:27], v[22:23], v[26:27], s[10:11] op_sel_hi:[1,1,0]
	v_pk_fma_f32 v[36:37], v[36:37], s[8:9], 1.0 op_sel_hi:[1,0,0]
	v_pk_mul_f32 v[22:23], v[22:23], v[26:27]
	v_rcp_f32_e32 v36, v36
	v_rcp_f32_e32 v37, v37
	v_pk_mul_f32 v[22:23], v[30:31], v[22:23]
	v_cmp_gt_f32_e32 vcc, 0, v16
	v_pk_mul_f32 v[30:31], v[16:17], v[22:23]
	v_pk_fma_f32 v[22:23], v[16:17], v[22:23], v[16:17] neg_lo:[1,0,0] neg_hi:[1,0,0]
	v_pk_mul_f32 v[26:27], v[18:19], v[18:19]
	v_cndmask_b32_e32 v30, v22, v30, vcc
	v_cmp_gt_f32_e32 vcc, 0, v17
	v_pk_fma_f32 v[16:17], v[36:37], s[0:1], v[122:123] op_sel_hi:[1,0,0]
	s_waitcnt vmcnt(1)
	v_pk_fma_f32 v[8:9], v[48:49], v[62:63], v[8:9] op_sel_hi:[1,0,1] neg_lo:[1,0,0] neg_hi:[1,0,0]
	v_cndmask_b32_e32 v31, v23, v31, vcc
	v_pk_mul_f32 v[22:23], v[26:27], s[16:17] op_sel_hi:[1,0]
	v_pk_fma_f32 v[16:17], v[36:37], v[16:17], s[14:15] op_sel_hi:[1,1,0]
	v_exp_f32_e32 v22, v22
	v_exp_f32_e32 v23, v23
	v_pk_fma_f32 v[16:17], v[36:37], v[16:17], s[6:7] op_sel_hi:[1,1,0]
	v_cmp_gt_f32_e32 vcc, 0, v18
	v_pk_fma_f32 v[16:17], v[36:37], v[16:17], s[10:11] op_sel_hi:[1,1,0]
	s_waitcnt vmcnt(0)
	v_pk_fma_f32 v[8:9], v[62:63], v[8:9], v[32:33] op_sel:[1,0,0]
	v_pk_mul_f32 v[16:17], v[36:37], v[16:17]
	v_pk_fma_f32 v[4:5], v[48:49], v[44:45], v[4:5] op_sel_hi:[1,0,1] neg_lo:[1,0,0] neg_hi:[1,0,0]
	v_pk_mul_f32 v[16:17], v[22:23], v[16:17]
	v_pk_fma_f32 v[4:5], v[44:45], v[4:5], v[32:33] op_sel:[1,0,0]
	v_pk_mul_f32 v[22:23], v[18:19], v[16:17]
	v_pk_fma_f32 v[16:17], v[18:19], v[16:17], v[18:19] neg_lo:[1,0,0] neg_hi:[1,0,0]
	v_pk_fma_f32 v[0:1], v[48:49], v[46:47], v[0:1] op_sel_hi:[1,0,1] neg_lo:[1,0,0] neg_hi:[1,0,0]
	v_cndmask_b32_e32 v18, v16, v22, vcc
	v_cmp_gt_f32_e32 vcc, 0, v19
	v_cvt_pk_f16_f32 v16, v30, v31
	v_pk_fma_f32 v[0:1], v[46:47], v[0:1], v[32:33] op_sel:[1,0,0]
	v_cndmask_b32_e32 v17, v17, v23, vcc
	v_cvt_pk_f16_f32 v17, v18, v17
	v_pk_fma_f32 v[18:19], v[48:49], v[60:61], v[12:13] op_sel_hi:[1,0,1] neg_lo:[1,0,0] neg_hi:[1,0,0]
	v_xor_b32_e32 v13, 0x80000000, v51
	v_pk_fma_f32 v[18:19], v[60:61], v[18:19], v[32:33] op_sel:[1,0,0]
	v_xor_b32_e32 v12, 0x80000000, v50
	v_and_b32_e32 v23, 0x7fffffff, v19
	v_and_b32_e32 v22, 0x7fffffff, v18
	v_pk_fma_f32 v[22:23], v[22:23], s[8:9], 1.0 op_sel_hi:[1,0,0]
	v_pk_mul_f32 v[30:31], v[18:19], v[18:19]
	v_rcp_f32_e32 v22, v22
	v_rcp_f32_e32 v23, v23
	v_pk_fma_f32 v[14:15], v[12:13], v[60:61], v[14:15] op_sel_hi:[1,0,1]
	v_pk_mul_f32 v[30:31], v[30:31], s[16:17] op_sel_hi:[1,0]
	v_pk_fma_f32 v[14:15], v[60:61], v[14:15], v[34:35] op_sel:[1,0,0]
	v_pk_fma_f32 v[26:27], v[22:23], s[0:1], v[122:123] op_sel_hi:[1,0,0]
	v_exp_f32_e32 v30, v30
	v_pk_fma_f32 v[26:27], v[22:23], v[26:27], s[14:15] op_sel_hi:[1,1,0]
	v_exp_f32_e32 v31, v31
	v_pk_fma_f32 v[26:27], v[22:23], v[26:27], s[6:7] op_sel_hi:[1,1,0]
	v_and_b32_e32 v37, 0x7fffffff, v15
	v_and_b32_e32 v36, 0x7fffffff, v14
	v_pk_fma_f32 v[26:27], v[22:23], v[26:27], s[10:11] op_sel_hi:[1,1,0]
	v_pk_fma_f32 v[36:37], v[36:37], s[8:9], 1.0 op_sel_hi:[1,0,0]
	v_pk_mul_f32 v[22:23], v[22:23], v[26:27]
	v_rcp_f32_e32 v36, v36
	v_rcp_f32_e32 v37, v37
	v_pk_mul_f32 v[22:23], v[30:31], v[22:23]
	v_cmp_gt_f32_e32 vcc, 0, v18
	v_pk_mul_f32 v[30:31], v[18:19], v[22:23]
	v_pk_fma_f32 v[22:23], v[18:19], v[22:23], v[18:19] neg_lo:[1,0,0] neg_hi:[1,0,0]
	v_pk_mul_f32 v[26:27], v[14:15], v[14:15]
	v_cndmask_b32_e32 v30, v22, v30, vcc
	v_cmp_gt_f32_e32 vcc, 0, v19
	v_pk_fma_f32 v[18:19], v[36:37], s[0:1], v[122:123] op_sel_hi:[1,0,0]
	v_pk_fma_f32 v[10:11], v[12:13], v[62:63], v[10:11] op_sel_hi:[1,0,1]
	v_cndmask_b32_e32 v31, v23, v31, vcc
	v_pk_mul_f32 v[22:23], v[26:27], s[16:17] op_sel_hi:[1,0]
	v_pk_fma_f32 v[18:19], v[36:37], v[18:19], s[14:15] op_sel_hi:[1,1,0]
	v_exp_f32_e32 v22, v22
	v_exp_f32_e32 v23, v23
	v_pk_fma_f32 v[18:19], v[36:37], v[18:19], s[6:7] op_sel_hi:[1,1,0]
	v_cmp_gt_f32_e32 vcc, 0, v14
	v_pk_fma_f32 v[18:19], v[36:37], v[18:19], s[10:11] op_sel_hi:[1,1,0]
	v_pk_fma_f32 v[10:11], v[62:63], v[10:11], v[34:35] op_sel:[1,0,0]
	v_pk_mul_f32 v[18:19], v[36:37], v[18:19]
	v_and_b32_e32 v27, 0x7fffffff, v11
	v_pk_mul_f32 v[18:19], v[22:23], v[18:19]
	v_and_b32_e32 v26, 0x7fffffff, v10
	v_pk_mul_f32 v[22:23], v[14:15], v[18:19]
	v_pk_fma_f32 v[18:19], v[14:15], v[18:19], v[14:15] neg_lo:[1,0,0] neg_hi:[1,0,0]
	v_cvt_pk_f16_f32 v14, v30, v31
	v_cndmask_b32_e32 v18, v18, v22, vcc
	v_cmp_gt_f32_e32 vcc, 0, v15
	v_pk_fma_f32 v[26:27], v[26:27], s[8:9], 1.0 op_sel_hi:[1,0,0]
	v_pk_fma_f32 v[6:7], v[12:13], v[44:45], v[6:7] op_sel_hi:[1,0,1]
	v_cndmask_b32_e32 v15, v19, v23, vcc
	v_cvt_pk_f16_f32 v15, v18, v15
	v_and_b32_e32 v19, 0x7fffffff, v9
	v_and_b32_e32 v18, 0x7fffffff, v8
	v_pk_fma_f32 v[18:19], v[18:19], s[8:9], 1.0 op_sel_hi:[1,0,0]
	v_pk_mul_f32 v[22:23], v[8:9], v[8:9]
	v_rcp_f32_e32 v18, v18
	v_rcp_f32_e32 v19, v19
	ds_write2_b64 v121, v[28:29], v[14:15] offset0:16 offset1:20
	v_pk_mul_f32 v[22:23], v[22:23], s[16:17] op_sel_hi:[1,0]
	v_rcp_f32_e32 v26, v26
	v_pk_fma_f32 v[14:15], v[18:19], s[0:1], v[122:123] op_sel_hi:[1,0,0]
	v_exp_f32_e32 v22, v22
	v_pk_fma_f32 v[14:15], v[18:19], v[14:15], s[14:15] op_sel_hi:[1,1,0]
	v_exp_f32_e32 v23, v23
	v_pk_fma_f32 v[14:15], v[18:19], v[14:15], s[6:7] op_sel_hi:[1,1,0]
	v_rcp_f32_e32 v27, v27
	v_pk_fma_f32 v[14:15], v[18:19], v[14:15], s[10:11] op_sel_hi:[1,1,0]
	v_cmp_gt_f32_e32 vcc, 0, v8
	v_pk_mul_f32 v[14:15], v[18:19], v[14:15]
	v_pk_mul_f32 v[18:19], v[10:11], v[10:11]
	v_pk_mul_f32 v[14:15], v[22:23], v[14:15]
	v_pk_fma_f32 v[6:7], v[44:45], v[6:7], v[34:35] op_sel:[1,0,0]
	v_pk_mul_f32 v[22:23], v[8:9], v[14:15]
	v_pk_fma_f32 v[14:15], v[8:9], v[14:15], v[8:9] neg_lo:[1,0,0] neg_hi:[1,0,0]
	v_cvt_pk_f16_f32 v20, v52, v53
	v_cndmask_b32_e32 v22, v14, v22, vcc
	v_cmp_gt_f32_e32 vcc, 0, v9
	v_pk_fma_f32 v[8:9], v[26:27], s[0:1], v[122:123] op_sel_hi:[1,0,0]
	v_pk_fma_f32 v[2:3], v[12:13], v[46:47], v[2:3] op_sel_hi:[1,0,1]
	v_cndmask_b32_e32 v23, v15, v23, vcc
	v_pk_mul_f32 v[14:15], v[18:19], s[16:17] op_sel_hi:[1,0]
	v_pk_fma_f32 v[8:9], v[26:27], v[8:9], s[14:15] op_sel_hi:[1,1,0]
	v_exp_f32_e32 v14, v14
	v_exp_f32_e32 v15, v15
	v_pk_fma_f32 v[8:9], v[26:27], v[8:9], s[6:7] op_sel_hi:[1,1,0]
	v_cmp_gt_f32_e32 vcc, 0, v10
	v_pk_fma_f32 v[8:9], v[26:27], v[8:9], s[10:11] op_sel_hi:[1,1,0]
	v_and_b32_e32 v19, 0x7fffffff, v7
	v_pk_mul_f32 v[8:9], v[26:27], v[8:9]
	v_and_b32_e32 v18, 0x7fffffff, v6
	v_pk_mul_f32 v[8:9], v[14:15], v[8:9]
	v_pk_fma_f32 v[18:19], v[18:19], s[8:9], 1.0 op_sel_hi:[1,0,0]
	v_pk_mul_f32 v[14:15], v[10:11], v[8:9]
	v_pk_fma_f32 v[8:9], v[10:11], v[8:9], v[10:11] neg_lo:[1,0,0] neg_hi:[1,0,0]
	v_rcp_f32_e32 v18, v18
	v_cndmask_b32_e32 v10, v8, v14, vcc
	v_cmp_gt_f32_e32 vcc, 0, v11
	v_and_b32_e32 v11, 0x7fffffff, v5
	v_cvt_pk_f16_f32 v8, v22, v23
	v_cndmask_b32_e32 v9, v9, v15, vcc
	v_cvt_pk_f16_f32 v9, v10, v9
	v_and_b32_e32 v10, 0x7fffffff, v4
	v_pk_fma_f32 v[10:11], v[10:11], s[8:9], 1.0 op_sel_hi:[1,0,0]
	v_pk_mul_f32 v[14:15], v[4:5], v[4:5]
	v_rcp_f32_e32 v10, v10
	v_rcp_f32_e32 v11, v11
	ds_write2_b64 v94, v[24:25], v[8:9] offset0:48 offset1:52
	v_pk_mul_f32 v[14:15], v[14:15], s[16:17] op_sel_hi:[1,0]
	v_rcp_f32_e32 v19, v19
	v_pk_fma_f32 v[8:9], v[10:11], s[0:1], v[122:123] op_sel_hi:[1,0,0]
	v_exp_f32_e32 v14, v14
	v_pk_fma_f32 v[8:9], v[10:11], v[8:9], s[14:15] op_sel_hi:[1,1,0]
	v_exp_f32_e32 v15, v15
	v_pk_fma_f32 v[8:9], v[10:11], v[8:9], s[6:7] op_sel_hi:[1,1,0]
	v_cmp_gt_f32_e32 vcc, 0, v4
	v_pk_fma_f32 v[8:9], v[10:11], v[8:9], s[10:11] op_sel_hi:[1,1,0]
	v_pk_fma_f32 v[2:3], v[46:47], v[2:3], v[34:35] op_sel:[1,0,0]
	v_pk_mul_f32 v[8:9], v[10:11], v[8:9]
	v_pk_mul_f32 v[10:11], v[6:7], v[6:7]
	v_pk_mul_f32 v[8:9], v[14:15], v[8:9]
	s_nop 0
	v_pk_mul_f32 v[14:15], v[4:5], v[8:9]
	v_pk_fma_f32 v[8:9], v[4:5], v[8:9], v[4:5] neg_lo:[1,0,0] neg_hi:[1,0,0]
	s_nop 0
	v_cndmask_b32_e32 v14, v8, v14, vcc
	v_cmp_gt_f32_e32 vcc, 0, v5
	v_pk_fma_f32 v[4:5], v[18:19], s[0:1], v[122:123] op_sel_hi:[1,0,0]
	s_nop 0
	v_cndmask_b32_e32 v15, v9, v15, vcc
	v_pk_mul_f32 v[8:9], v[10:11], s[16:17] op_sel_hi:[1,0]
	v_pk_fma_f32 v[4:5], v[18:19], v[4:5], s[14:15] op_sel_hi:[1,1,0]
	v_exp_f32_e32 v8, v8
	v_exp_f32_e32 v9, v9
	v_pk_fma_f32 v[4:5], v[18:19], v[4:5], s[6:7] op_sel_hi:[1,1,0]
	v_cmp_gt_f32_e32 vcc, 0, v6
	v_pk_fma_f32 v[4:5], v[18:19], v[4:5], s[10:11] op_sel_hi:[1,1,0]
	v_and_b32_e32 v11, 0x7fffffff, v3
	v_pk_mul_f32 v[4:5], v[18:19], v[4:5]
	v_and_b32_e32 v10, 0x7fffffff, v2
	v_pk_mul_f32 v[4:5], v[8:9], v[4:5]
	v_pk_fma_f32 v[10:11], v[10:11], s[8:9], 1.0 op_sel_hi:[1,0,0]
	v_pk_mul_f32 v[8:9], v[6:7], v[4:5]
	v_pk_fma_f32 v[4:5], v[6:7], v[4:5], v[6:7] neg_lo:[1,0,0] neg_hi:[1,0,0]
	v_rcp_f32_e32 v10, v10
	v_cndmask_b32_e32 v6, v4, v8, vcc
	v_cmp_gt_f32_e32 vcc, 0, v7
	v_and_b32_e32 v7, 0x7fffffff, v1
	v_cvt_pk_f16_f32 v4, v14, v15
	v_cndmask_b32_e32 v5, v5, v9, vcc
	v_cvt_pk_f16_f32 v5, v6, v5
	v_and_b32_e32 v6, 0x7fffffff, v0
	v_pk_fma_f32 v[6:7], v[6:7], s[8:9], 1.0 op_sel_hi:[1,0,0]
	v_pk_mul_f32 v[8:9], v[0:1], v[0:1]
	v_rcp_f32_e32 v6, v6
	v_rcp_f32_e32 v7, v7
	ds_write2_b64 v95, v[20:21], v[4:5] offset0:80 offset1:84
	v_pk_mul_f32 v[8:9], v[8:9], s[16:17] op_sel_hi:[1,0]
	v_rcp_f32_e32 v11, v11
	v_pk_fma_f32 v[4:5], v[6:7], s[0:1], v[122:123] op_sel_hi:[1,0,0]
	v_exp_f32_e32 v8, v8
	v_pk_fma_f32 v[4:5], v[6:7], v[4:5], s[14:15] op_sel_hi:[1,1,0]
	v_exp_f32_e32 v9, v9
	v_pk_fma_f32 v[4:5], v[6:7], v[4:5], s[6:7] op_sel_hi:[1,1,0]
	v_cmp_gt_f32_e32 vcc, 0, v0
	v_pk_fma_f32 v[4:5], v[6:7], v[4:5], s[10:11] op_sel_hi:[1,1,0]
	s_nop 0
	v_pk_mul_f32 v[4:5], v[6:7], v[4:5]
	v_pk_mul_f32 v[6:7], v[2:3], v[2:3]
	v_pk_mul_f32 v[4:5], v[8:9], v[4:5]
	s_nop 0
	v_pk_mul_f32 v[8:9], v[0:1], v[4:5]
	v_pk_fma_f32 v[4:5], v[0:1], v[4:5], v[0:1] neg_lo:[1,0,0] neg_hi:[1,0,0]
	s_nop 0
	v_cndmask_b32_e32 v8, v4, v8, vcc
	v_cmp_gt_f32_e32 vcc, 0, v1
	v_pk_fma_f32 v[0:1], v[10:11], s[0:1], v[122:123] op_sel_hi:[1,0,0]
	s_lshl_b64 s[0:1], s[2:3], 1
	v_cndmask_b32_e32 v9, v5, v9, vcc
	v_pk_mul_f32 v[4:5], v[6:7], s[16:17] op_sel_hi:[1,0]
	v_pk_fma_f32 v[0:1], v[10:11], v[0:1], s[14:15] op_sel_hi:[1,1,0]
	v_exp_f32_e32 v4, v4
	v_exp_f32_e32 v5, v5
	v_pk_fma_f32 v[0:1], v[10:11], v[0:1], s[6:7] op_sel_hi:[1,1,0]
	v_cmp_gt_f32_e32 vcc, 0, v2
	v_pk_fma_f32 v[0:1], v[10:11], v[0:1], s[10:11] op_sel_hi:[1,1,0]
	s_mov_b32 s2, 0x2aaaaaab
	v_pk_mul_f32 v[0:1], v[10:11], v[0:1]
	s_add_u32 s0, s4, s0
	v_pk_mul_f32 v[0:1], v[4:5], v[0:1]
	s_movk_i32 s3, 0xffe8
	v_pk_mul_f32 v[4:5], v[2:3], v[0:1]
	v_pk_fma_f32 v[0:1], v[2:3], v[0:1], v[2:3] neg_lo:[1,0,0] neg_hi:[1,0,0]
	s_addc_u32 s1, s5, s1
	v_cndmask_b32_e32 v2, v0, v4, vcc
	v_cmp_gt_f32_e32 vcc, 0, v3
	v_cvt_pk_f16_f32 v0, v8, v9
	s_nop 0
	v_cndmask_b32_e32 v1, v1, v5, vcc
	v_cvt_pk_f16_f32 v1, v2, v1
	ds_write2_b64 v90, v[16:17], v[0:1] offset0:112 offset1:116
	v_mul_hi_i32 v0, v120, s2
	v_lshrrev_b32_e32 v1, 31, v0
	v_ashrrev_i32_e32 v0, 2, v0
	v_add_u32_e32 v6, v0, v1
	v_mad_u64_u32 v[4:5], s[4:5], v6, s3, v[120:121]
	v_add_u32_e32 v5, s17, v6
	v_mul_lo_u32 v0, v6, s7
	v_lshlrev_b32_e32 v1, 4, v4
	v_mad_i64_i32 v[6:7], s[4:5], v5, s12, 0
	v_lshlrev_b32_e32 v4, 3, v4
	v_lshl_add_u64 v[6:7], v[6:7], 1, s[0:1]
	v_ashrrev_i32_e32 v5, 31, v4
	v_lshl_add_u64 v[8:9], v[4:5], 1, v[6:7]
	v_add_u32_e32 v4, 0x100, v120
	v_mul_hi_i32 v5, v4, s2
	s_waitcnt lgkmcnt(0)
	s_barrier
	v_add3_u32 v0, 0, v0, v1
	v_lshrrev_b32_e32 v6, 31, v5
	v_ashrrev_i32_e32 v5, 2, v5
	ds_read_b128 v[0:3], v0
	v_add_u32_e32 v12, v5, v6
	v_mad_u64_u32 v[10:11], s[4:5], v12, s3, v[4:5]
	v_mul_lo_u32 v4, v12, s7
	v_lshlrev_b32_e32 v5, 4, v10
	v_add3_u32 v4, 0, v4, v5
	ds_read_b128 v[4:7], v4
	s_waitcnt lgkmcnt(1)
	global_store_dwordx4 v[8:9], v[0:3], off sc1
	s_nop 1
	v_add_u32_e32 v0, s17, v12
	v_mad_i64_i32 v[0:1], s[4:5], v0, s12, 0
	v_lshlrev_b32_e32 v2, 3, v10
	v_lshl_add_u64 v[0:1], v[0:1], 1, s[0:1]
	v_ashrrev_i32_e32 v3, 31, v2
	v_lshl_add_u64 v[0:1], v[2:3], 1, v[0:1]
	s_waitcnt lgkmcnt(0)
	global_store_dwordx4 v[0:1], v[4:7], off sc1
	v_add_u32_e32 v0, 0x200, v120
	v_mul_hi_i32 v1, v0, s2
	v_lshrrev_b32_e32 v2, 31, v1
	v_ashrrev_i32_e32 v1, 2, v1
	v_add_u32_e32 v6, v1, v2
	v_mad_u64_u32 v[4:5], s[4:5], v6, s3, v[0:1]
	v_add_u32_e32 v5, s17, v6
	v_mul_lo_u32 v0, v6, s7
	v_lshlrev_b32_e32 v1, 4, v4
	v_mad_i64_i32 v[6:7], s[4:5], v5, s12, 0
	v_lshlrev_b32_e32 v4, 3, v4
	v_lshl_add_u64 v[6:7], v[6:7], 1, s[0:1]
	v_ashrrev_i32_e32 v5, 31, v4
	v_lshl_add_u64 v[8:9], v[4:5], 1, v[6:7]
	v_add_u32_e32 v4, 0x300, v120
	v_mul_hi_i32 v5, v4, s2
	v_add3_u32 v0, 0, v0, v1
	v_lshrrev_b32_e32 v6, 31, v5
	v_ashrrev_i32_e32 v5, 2, v5
	ds_read_b128 v[0:3], v0
	v_add_u32_e32 v12, v5, v6
	v_mad_u64_u32 v[10:11], s[4:5], v12, s3, v[4:5]
	v_mul_lo_u32 v4, v12, s7
	v_lshlrev_b32_e32 v5, 4, v10
	v_add3_u32 v4, 0, v4, v5
	ds_read_b128 v[4:7], v4
	s_waitcnt lgkmcnt(1)
	global_store_dwordx4 v[8:9], v[0:3], off sc1
	s_nop 1
	v_add_u32_e32 v0, s17, v12
	v_mad_i64_i32 v[0:1], s[4:5], v0, s12, 0
	v_lshlrev_b32_e32 v2, 3, v10
	v_lshl_add_u64 v[0:1], v[0:1], 1, s[0:1]
	v_ashrrev_i32_e32 v3, 31, v2
	v_lshl_add_u64 v[0:1], v[2:3], 1, v[0:1]
	s_waitcnt lgkmcnt(0)
	global_store_dwordx4 v[0:1], v[4:7], off sc1
	v_add_u32_e32 v0, 0x400, v120
	v_mul_hi_i32 v1, v0, s2
	v_lshrrev_b32_e32 v2, 31, v1
	v_ashrrev_i32_e32 v1, 2, v1
	v_add_u32_e32 v6, v1, v2
	v_mad_u64_u32 v[4:5], s[4:5], v6, s3, v[0:1]
	v_add_u32_e32 v5, s17, v6
	v_mul_lo_u32 v0, v6, s7
	v_lshlrev_b32_e32 v1, 4, v4
	v_mad_i64_i32 v[6:7], s[4:5], v5, s12, 0
	v_lshlrev_b32_e32 v4, 3, v4
	v_lshl_add_u64 v[6:7], v[6:7], 1, s[0:1]
	v_ashrrev_i32_e32 v5, 31, v4
	v_lshl_add_u64 v[8:9], v[4:5], 1, v[6:7]
	v_add_u32_e32 v4, 0x500, v120
	v_mul_hi_i32 v5, v4, s2
	v_add3_u32 v0, 0, v0, v1
	v_lshrrev_b32_e32 v6, 31, v5
	v_ashrrev_i32_e32 v5, 2, v5
	ds_read_b128 v[0:3], v0
	v_add_u32_e32 v12, v5, v6
	v_mad_u64_u32 v[10:11], s[4:5], v12, s3, v[4:5]
	v_mul_lo_u32 v4, v12, s7
	v_lshlrev_b32_e32 v5, 4, v10
	v_add3_u32 v4, 0, v4, v5
	ds_read_b128 v[4:7], v4
	s_waitcnt lgkmcnt(1)
	global_store_dwordx4 v[8:9], v[0:3], off sc1
	s_nop 1
	v_add_u32_e32 v0, s17, v12
	v_mad_i64_i32 v[0:1], s[4:5], v0, s12, 0
	v_lshlrev_b32_e32 v2, 3, v10
	v_lshl_add_u64 v[0:1], v[0:1], 1, s[0:1]
	v_ashrrev_i32_e32 v3, 31, v2
	v_lshl_add_u64 v[0:1], v[2:3], 1, v[0:1]
	s_waitcnt lgkmcnt(0)
	global_store_dwordx4 v[0:1], v[4:7], off sc1
	v_add_u32_e32 v0, 0x600, v120
	v_mul_hi_i32 v1, v0, s2
	v_lshrrev_b32_e32 v2, 31, v1
	v_ashrrev_i32_e32 v1, 2, v1
	v_add_u32_e32 v6, v1, v2
	v_mad_u64_u32 v[4:5], s[4:5], v6, s3, v[0:1]
	v_add_u32_e32 v5, s17, v6
	v_mul_lo_u32 v0, v6, s7
	v_lshlrev_b32_e32 v1, 4, v4
	v_mad_i64_i32 v[6:7], s[4:5], v5, s12, 0
	v_lshlrev_b32_e32 v4, 3, v4
	v_lshl_add_u64 v[6:7], v[6:7], 1, s[0:1]
	v_ashrrev_i32_e32 v5, 31, v4
	v_lshl_add_u64 v[8:9], v[4:5], 1, v[6:7]
	v_add_u32_e32 v4, 0x700, v120
	v_mul_hi_i32 v5, v4, s2
	v_add3_u32 v0, 0, v0, v1
	v_lshrrev_b32_e32 v6, 31, v5
	v_ashrrev_i32_e32 v5, 2, v5
	ds_read_b128 v[0:3], v0
	v_add_u32_e32 v12, v5, v6
	v_mad_u64_u32 v[10:11], s[4:5], v12, s3, v[4:5]
	v_mul_lo_u32 v4, v12, s7
	v_lshlrev_b32_e32 v5, 4, v10
	v_add3_u32 v4, 0, v4, v5
	ds_read_b128 v[4:7], v4
	s_waitcnt lgkmcnt(1)
	global_store_dwordx4 v[8:9], v[0:3], off sc1
	s_nop 1
	v_add_u32_e32 v0, s17, v12
	v_mad_i64_i32 v[0:1], s[4:5], v0, s12, 0
	v_lshlrev_b32_e32 v2, 3, v10
	v_lshl_add_u64 v[0:1], v[0:1], 1, s[0:1]
	v_ashrrev_i32_e32 v3, 31, v2
	v_lshl_add_u64 v[0:1], v[2:3], 1, v[0:1]
	s_waitcnt lgkmcnt(0)
	global_store_dwordx4 v[0:1], v[4:7], off sc1
	v_add_u32_e32 v0, 0x800, v120
	v_mul_hi_i32 v1, v0, s2
	v_lshrrev_b32_e32 v2, 31, v1
	v_ashrrev_i32_e32 v1, 2, v1
	v_add_u32_e32 v6, v1, v2
	v_mad_u64_u32 v[4:5], s[4:5], v6, s3, v[0:1]
	v_add_u32_e32 v5, s17, v6
	v_mul_lo_u32 v0, v6, s7
	v_lshlrev_b32_e32 v1, 4, v4
	v_mad_i64_i32 v[6:7], s[4:5], v5, s12, 0
	v_lshlrev_b32_e32 v4, 3, v4
	v_lshl_add_u64 v[6:7], v[6:7], 1, s[0:1]
	v_ashrrev_i32_e32 v5, 31, v4
	v_lshl_add_u64 v[8:9], v[4:5], 1, v[6:7]
	v_add_u32_e32 v4, 0x900, v120
	v_mul_hi_i32 v5, v4, s2
	v_add3_u32 v0, 0, v0, v1
	v_lshrrev_b32_e32 v6, 31, v5
	v_ashrrev_i32_e32 v5, 2, v5
	ds_read_b128 v[0:3], v0
	v_add_u32_e32 v12, v5, v6
	v_mad_u64_u32 v[10:11], s[4:5], v12, s3, v[4:5]
	v_mul_lo_u32 v4, v12, s7
	v_lshlrev_b32_e32 v5, 4, v10
	v_add3_u32 v4, 0, v4, v5
	ds_read_b128 v[4:7], v4
	s_waitcnt lgkmcnt(1)
	global_store_dwordx4 v[8:9], v[0:3], off sc1
	s_nop 1
	v_add_u32_e32 v0, s17, v12
	v_mad_i64_i32 v[0:1], s[4:5], v0, s12, 0
	v_lshlrev_b32_e32 v2, 3, v10
	v_lshl_add_u64 v[0:1], v[0:1], 1, s[0:1]
	v_ashrrev_i32_e32 v3, 31, v2
	v_lshl_add_u64 v[0:1], v[2:3], 1, v[0:1]
	s_waitcnt lgkmcnt(0)
	global_store_dwordx4 v[0:1], v[4:7], off sc1
	v_add_u32_e32 v0, 0xa00, v120
	v_mul_hi_i32 v1, v0, s2
	v_lshrrev_b32_e32 v2, 31, v1
	v_ashrrev_i32_e32 v1, 2, v1
	v_add_u32_e32 v6, v1, v2
	v_mad_u64_u32 v[4:5], s[4:5], v6, s3, v[0:1]
	v_add_u32_e32 v5, s17, v6
	v_mul_lo_u32 v0, v6, s7
	v_lshlrev_b32_e32 v1, 4, v4
	v_mad_i64_i32 v[6:7], s[4:5], v5, s12, 0
	v_lshlrev_b32_e32 v4, 3, v4
	v_lshl_add_u64 v[6:7], v[6:7], 1, s[0:1]
	v_ashrrev_i32_e32 v5, 31, v4
	v_lshl_add_u64 v[8:9], v[4:5], 1, v[6:7]
	v_add_u32_e32 v4, 0xb00, v120
	v_mul_hi_i32 v5, v4, s2
	v_add3_u32 v0, 0, v0, v1
	v_lshrrev_b32_e32 v6, 31, v5
	v_ashrrev_i32_e32 v5, 2, v5
	ds_read_b128 v[0:3], v0
	v_add_u32_e32 v12, v5, v6
	v_mad_u64_u32 v[10:11], s[2:3], v12, s3, v[4:5]
	v_mul_lo_u32 v4, v12, s7
	v_lshlrev_b32_e32 v5, 4, v10
	v_add3_u32 v4, 0, v4, v5
	ds_read_b128 v[4:7], v4
	s_waitcnt lgkmcnt(1)
	global_store_dwordx4 v[8:9], v[0:3], off sc1
	s_nop 1
	v_add_u32_e32 v0, s17, v12
	v_mad_i64_i32 v[0:1], s[2:3], v0, s12, 0
	v_lshlrev_b32_e32 v2, 3, v10
	v_lshl_add_u64 v[0:1], v[0:1], 1, s[0:1]
	v_ashrrev_i32_e32 v3, 31, v2
	v_lshl_add_u64 v[0:1], v[2:3], 1, v[0:1]
	s_waitcnt lgkmcnt(0)
	global_store_dwordx4 v[0:1], v[4:7], off sc1
	s_endpgm
	.p2align	8

	.amdhsa_kernel _Z8gemm2b_kILi2EEvPKtS1_ii7EpiArgs
		.amdhsa_group_segment_fixed_size 0
		.amdhsa_private_segment_fixed_size 0
		.amdhsa_kernarg_size 88
		.amdhsa_user_sgpr_count 2
		.amdhsa_user_sgpr_dispatch_ptr 0
		.amdhsa_user_sgpr_queue_ptr 0
		.amdhsa_user_sgpr_kernarg_segment_ptr 1
		.amdhsa_user_sgpr_dispatch_id 0
		.amdhsa_user_sgpr_kernarg_preload_length 0
		.amdhsa_user_sgpr_kernarg_preload_offset 0
		.amdhsa_user_sgpr_private_segment_size 0
		.amdhsa_uses_dynamic_stack 0
		.amdhsa_enable_private_segment 0
		.amdhsa_system_sgpr_workgroup_id_x 1
		.amdhsa_system_sgpr_workgroup_id_y 0
		.amdhsa_system_sgpr_workgroup_id_z 0
		.amdhsa_system_sgpr_workgroup_info 0
		.amdhsa_system_vgpr_workitem_id 0
		.amdhsa_next_free_vgpr 212
		.amdhsa_next_free_sgpr 86
		.amdhsa_accum_offset 212
		.amdhsa_reserve_vcc 1
		.amdhsa_float_round_mode_32 0
		.amdhsa_float_round_mode_16_64 0
		.amdhsa_float_denorm_mode_32 3
		.amdhsa_float_denorm_mode_16_64 3
		.amdhsa_dx10_clamp 1
		.amdhsa_ieee_mode 1
		.amdhsa_fp16_overflow 0
		.amdhsa_tg_split 0
		.amdhsa_exception_fp_ieee_invalid_op 0
		.amdhsa_exception_fp_denorm_src 0
		.amdhsa_exception_fp_ieee_div_zero 0
		.amdhsa_exception_fp_ieee_overflow 0
		.amdhsa_exception_fp_ieee_underflow 0
		.amdhsa_exception_fp_ieee_inexact 0
		.amdhsa_exception_int_div_zero 0
	.end_amdhsa_kernel

.Lgk_loop_dnA:
	s_waitcnt vmcnt(5) lgkmcnt(0)
	s_barrier
	s_mov_b32 m0, s25
	s_add_u32 s54, s54, 0x80
	s_addc_u32 s55, s55, 0
	global_load_lds_dwordx4 v84, s[54:55]
	s_mov_b32 m0, s26
	s_add_u32 s56, s56, 0x80
	s_addc_u32 s57, s57, 0
	global_load_lds_dwordx4 v84, s[56:57]
	s_mov_b32 m0, s27
	s_add_u32 s58, s58, 0x80
	s_addc_u32 s59, s59, 0
	global_load_lds_dwordx4 v84, s[58:59]
	s_mov_b32 m0, s28
	s_add_u32 s60, s60, 0x80
	s_addc_u32 s61, s61, 0
	global_load_lds_dwordx4 v84, s[60:61]
	s_mov_b32 m0, s29
	s_add_u32 s62, s62, 0x80
	s_addc_u32 s63, s63, 0
	global_load_lds_dwordx4 v84, s[62:63]
	v_mfma_f32_16x16x32_f16 v[120:123], v[212:215], v[196:199], v[120:123]
	ds_read_b128 v[168:171], v79 offset:40960
	v_mfma_f32_16x16x32_f16 v[124:127], v[216:219], v[196:199], v[124:127]
	ds_read_b128 v[184:187], v82 offset:57344
	v_mfma_f32_16x16x32_f16 v[128:131], v[220:223], v[196:199], v[128:131]
	ds_read_b128 v[188:191], v82 offset:59392
	v_mfma_f32_16x16x32_f16 v[132:135], v[212:215], v[200:203], v[132:135]
	ds_read_b128 v[192:195], v82 offset:61440
	v_mfma_f32_16x16x32_f16 v[136:139], v[216:219], v[200:203], v[136:139]
	ds_read_b128 v[172:175], v79 offset:43008
	v_mfma_f32_16x16x32_f16 v[140:143], v[220:223], v[200:203], v[140:143]
	ds_read_b128 v[176:179], v79 offset:45056
	v_mfma_f32_16x16x32_f16 v[144:147], v[212:215], v[204:207], v[144:147]
	ds_read_b128 v[180:183], v79 offset:47104
	v_mfma_f32_16x16x32_f16 v[148:151], v[216:219], v[204:207], v[148:151]
	v_mfma_f32_16x16x32_f16 v[152:155], v[220:223], v[204:207], v[152:155]
	v_mfma_f32_16x16x32_f16 v[156:159], v[212:215], v[208:211], v[156:159]
	v_mfma_f32_16x16x32_f16 v[160:163], v[216:219], v[208:211], v[160:163]
	v_mfma_f32_16x16x32_f16 v[164:167], v[220:223], v[208:211], v[164:167]
	s_waitcnt lgkmcnt(0)
	v_mfma_f32_16x16x32_f16 v[120:123], v[184:187], v[168:171], v[120:123]
	ds_read_b128 v[196:199], v83 offset:40960
	v_mfma_f32_16x16x32_f16 v[124:127], v[188:191], v[168:171], v[124:127]
	ds_read_b128 v[212:215], v81 offset:57344
	v_mfma_f32_16x16x32_f16 v[128:131], v[192:195], v[168:171], v[128:131]
	ds_read_b128 v[216:219], v81 offset:59392
	v_mfma_f32_16x16x32_f16 v[132:135], v[184:187], v[172:175], v[132:135]
	ds_read_b128 v[220:223], v81 offset:61440
	v_mfma_f32_16x16x32_f16 v[136:139], v[188:191], v[172:175], v[136:139]
	ds_read_b128 v[200:203], v83 offset:43008
	v_mfma_f32_16x16x32_f16 v[140:143], v[192:195], v[172:175], v[140:143]
	ds_read_b128 v[204:207], v83 offset:45056
	v_mfma_f32_16x16x32_f16 v[144:147], v[184:187], v[176:179], v[144:147]
	ds_read_b128 v[208:211], v83 offset:47104
	v_mfma_f32_16x16x32_f16 v[148:151], v[188:191], v[176:179], v[148:151]
	v_mfma_f32_16x16x32_f16 v[152:155], v[192:195], v[176:179], v[152:155]
	v_mfma_f32_16x16x32_f16 v[156:159], v[184:187], v[180:183], v[156:159]
	v_mfma_f32_16x16x32_f16 v[160:163], v[188:191], v[180:183], v[160:163]
	v_mfma_f32_16x16x32_f16 v[164:167], v[192:195], v[180:183], v[164:167]
	s_waitcnt vmcnt(5) lgkmcnt(0)
	s_barrier
	s_mov_b32 m0, s30
	s_add_u32 s54, s54, 0x80
	s_addc_u32 s55, s55, 0
	global_load_lds_dwordx4 v84, s[54:55]
	s_mov_b32 m0, s31
	s_add_u32 s56, s56, 0x80
	s_addc_u32 s57, s57, 0
	global_load_lds_dwordx4 v84, s[56:57]
	s_mov_b32 m0, s33
	s_add_u32 s58, s58, 0x80
	s_addc_u32 s59, s59, 0
	global_load_lds_dwordx4 v84, s[58:59]
	s_mov_b32 m0, s34
	s_add_u32 s60, s60, 0x80
	s_addc_u32 s61, s61, 0
	global_load_lds_dwordx4 v84, s[60:61]
	s_mov_b32 m0, s35
	s_add_u32 s62, s62, 0x80
	s_addc_u32 s63, s63, 0
	global_load_lds_dwordx4 v84, s[62:63]
	v_mfma_f32_16x16x32_f16 v[120:123], v[212:215], v[196:199], v[120:123]
	ds_read_b128 v[168:171], v100 offset:0
	v_mfma_f32_16x16x32_f16 v[124:127], v[216:219], v[196:199], v[124:127]
	ds_read_b128 v[184:187], v102 offset:16384
	v_mfma_f32_16x16x32_f16 v[128:131], v[220:223], v[196:199], v[128:131]
	ds_read_b128 v[188:191], v102 offset:18432
	v_mfma_f32_16x16x32_f16 v[132:135], v[212:215], v[200:203], v[132:135]
	ds_read_b128 v[192:195], v102 offset:20480
	v_mfma_f32_16x16x32_f16 v[136:139], v[216:219], v[200:203], v[136:139]
	ds_read_b128 v[172:175], v100 offset:2048
	v_mfma_f32_16x16x32_f16 v[140:143], v[220:223], v[200:203], v[140:143]
	ds_read_b128 v[176:179], v100 offset:4096
	v_mfma_f32_16x16x32_f16 v[144:147], v[212:215], v[204:207], v[144:147]
	ds_read_b128 v[180:183], v100 offset:6144
	v_mfma_f32_16x16x32_f16 v[148:151], v[216:219], v[204:207], v[148:151]
	v_mfma_f32_16x16x32_f16 v[152:155], v[220:223], v[204:207], v[152:155]
	v_mfma_f32_16x16x32_f16 v[156:159], v[212:215], v[208:211], v[156:159]
	v_mfma_f32_16x16x32_f16 v[160:163], v[216:219], v[208:211], v[160:163]
	v_mfma_f32_16x16x32_f16 v[164:167], v[220:223], v[208:211], v[164:167]
	s_waitcnt lgkmcnt(0)
	v_mfma_f32_16x16x32_f16 v[120:123], v[184:187], v[168:171], v[120:123]
	ds_read_b128 v[196:199], v101 offset:0
	v_mfma_f32_16x16x32_f16 v[124:127], v[188:191], v[168:171], v[124:127]
	ds_read_b128 v[212:215], v103 offset:16384
	v_mfma_f32_16x16x32_f16 v[128:131], v[192:195], v[168:171], v[128:131]
	ds_read_b128 v[216:219], v103 offset:18432
	v_mfma_f32_16x16x32_f16 v[132:135], v[184:187], v[172:175], v[132:135]
	ds_read_b128 v[220:223], v103 offset:20480
	v_mfma_f32_16x16x32_f16 v[136:139], v[188:191], v[172:175], v[136:139]
	ds_read_b128 v[200:203], v101 offset:2048
	v_mfma_f32_16x16x32_f16 v[140:143], v[192:195], v[172:175], v[140:143]
	ds_read_b128 v[204:207], v101 offset:4096
	v_mfma_f32_16x16x32_f16 v[144:147], v[184:187], v[176:179], v[144:147]
	ds_read_b128 v[208:211], v101 offset:6144
	v_mfma_f32_16x16x32_f16 v[148:151], v[188:191], v[176:179], v[148:151]
	v_mfma_f32_16x16x32_f16 v[152:155], v[192:195], v[176:179], v[152:155]
	v_mfma_f32_16x16x32_f16 v[156:159], v[184:187], v[180:183], v[156:159]
	v_mfma_f32_16x16x32_f16 v[160:163], v[188:191], v[180:183], v[160:163]
	v_mfma_f32_16x16x32_f16 v[164:167], v[192:195], v[180:183], v[164:167]
	s_waitcnt vmcnt(5) lgkmcnt(0)
	s_barrier
	s_mov_b32 m0, s36
	s_add_u32 s54, s54, 0x80
	s_addc_u32 s55, s55, 0
	global_load_lds_dwordx4 v84, s[54:55]
	s_mov_b32 m0, s37
	s_add_u32 s56, s56, 0x80
	s_addc_u32 s57, s57, 0
	global_load_lds_dwordx4 v84, s[56:57]
	s_mov_b32 m0, s38
	s_add_u32 s58, s58, 0x80
	s_addc_u32 s59, s59, 0
	global_load_lds_dwordx4 v84, s[58:59]
	s_mov_b32 m0, s39
	s_add_u32 s60, s60, 0x80
	s_addc_u32 s61, s61, 0
	global_load_lds_dwordx4 v84, s[60:61]
	s_mov_b32 m0, s40
	s_add_u32 s62, s62, 0x80
	s_addc_u32 s63, s63, 0
	global_load_lds_dwordx4 v84, s[62:63]
	v_mfma_f32_16x16x32_f16 v[120:123], v[212:215], v[196:199], v[120:123]
	ds_read_b128 v[168:171], v79 offset:0
	v_mfma_f32_16x16x32_f16 v[124:127], v[216:219], v[196:199], v[124:127]
	ds_read_b128 v[184:187], v82 offset:16384
	v_mfma_f32_16x16x32_f16 v[128:131], v[220:223], v[196:199], v[128:131]
	ds_read_b128 v[188:191], v82 offset:18432
	v_mfma_f32_16x16x32_f16 v[132:135], v[212:215], v[200:203], v[132:135]
	ds_read_b128 v[192:195], v82 offset:20480
	v_mfma_f32_16x16x32_f16 v[136:139], v[216:219], v[200:203], v[136:139]
	ds_read_b128 v[172:175], v79 offset:2048
	v_mfma_f32_16x16x32_f16 v[140:143], v[220:223], v[200:203], v[140:143]
	ds_read_b128 v[176:179], v79 offset:4096
	v_mfma_f32_16x16x32_f16 v[144:147], v[212:215], v[204:207], v[144:147]
	ds_read_b128 v[180:183], v79 offset:6144
	v_mfma_f32_16x16x32_f16 v[148:151], v[216:219], v[204:207], v[148:151]
	v_mfma_f32_16x16x32_f16 v[152:155], v[220:223], v[204:207], v[152:155]
	v_mfma_f32_16x16x32_f16 v[156:159], v[212:215], v[208:211], v[156:159]
	v_mfma_f32_16x16x32_f16 v[160:163], v[216:219], v[208:211], v[160:163]
	v_mfma_f32_16x16x32_f16 v[164:167], v[220:223], v[208:211], v[164:167]
	s_waitcnt lgkmcnt(0)
	v_mfma_f32_16x16x32_f16 v[120:123], v[184:187], v[168:171], v[120:123]
	ds_read_b128 v[196:199], v83 offset:0
	v_mfma_f32_16x16x32_f16 v[124:127], v[188:191], v[168:171], v[124:127]
	ds_read_b128 v[212:215], v81 offset:16384
	v_mfma_f32_16x16x32_f16 v[128:131], v[192:195], v[168:171], v[128:131]
	ds_read_b128 v[216:219], v81 offset:18432
	v_mfma_f32_16x16x32_f16 v[132:135], v[184:187], v[172:175], v[132:135]
	ds_read_b128 v[220:223], v81 offset:20480
	v_mfma_f32_16x16x32_f16 v[136:139], v[188:191], v[172:175], v[136:139]
	ds_read_b128 v[200:203], v83 offset:2048
	v_mfma_f32_16x16x32_f16 v[140:143], v[192:195], v[172:175], v[140:143]
	ds_read_b128 v[204:207], v83 offset:4096
	v_mfma_f32_16x16x32_f16 v[144:147], v[184:187], v[176:179], v[144:147]
	ds_read_b128 v[208:211], v83 offset:6144
	v_mfma_f32_16x16x32_f16 v[148:151], v[188:191], v[176:179], v[148:151]
	v_mfma_f32_16x16x32_f16 v[152:155], v[192:195], v[176:179], v[152:155]
	v_mfma_f32_16x16x32_f16 v[156:159], v[184:187], v[180:183], v[156:159]
	v_mfma_f32_16x16x32_f16 v[160:163], v[188:191], v[180:183], v[160:163]
	v_mfma_f32_16x16x32_f16 v[164:167], v[192:195], v[180:183], v[164:167]
	s_add_i32 s64, s64, -1
	s_cmp_lg_u32 s64, 0
	s_cbranch_scc1 .Lgk_loop_dnA
	v_bfe_u32 v96, v0, 4, 2
	v_lshlrev_b32_e32 v96, 2, v96
	s_add_i32 s77, s23, s0
	v_or_b32_e32 v98, s77, v96
	v_ashrrev_i32_e32 v99, 31, v98
	v_lshl_add_u64 v[98:99], v[98:99], 2, s[14:15]
	global_load_dwordx4 v[104:107], v[98:99], off
	global_load_dwordx4 v[108:111], v[98:99], off offset:64
	global_load_dwordx4 v[112:115], v[98:99], off offset:128
	v_mov_b32_e32 v50, v0
	v_mul_u32_u24_e32 v51, 0xaab, v50
	v_lshrrev_b32_e32 v51, 17, v51
	v_mad_i32_i24 v52, v51, s76, v50
	v_mul_u32_u24_e32 v26, 0x300, v51
	v_lshl_add_u32 v26, v52, 2, v26
	v_mul_u32_u24_e32 v38, 0x310, v51
	v_lshl_add_u32 v38, v52, 4, v38
	v_lshlrev_b32_e32 v50, 1, v26
	global_load_dwordx2 v[2:3], v50, s[72:73] nt
	v_or_b32_e32 v50, 512, v0
	v_mul_u32_u24_e32 v51, 0xaab, v50
	v_lshrrev_b32_e32 v51, 17, v51
	v_mad_i32_i24 v52, v51, s76, v50
	v_mul_u32_u24_e32 v27, 0x300, v51
	v_lshl_add_u32 v27, v52, 2, v27
	v_mul_u32_u24_e32 v39, 0x310, v51
	v_lshl_add_u32 v39, v52, 4, v39
	v_lshlrev_b32_e32 v50, 1, v27
	global_load_dwordx2 v[4:5], v50, s[72:73] nt
	v_or_b32_e32 v50, 1024, v0
	v_mul_u32_u24_e32 v51, 0xaab, v50
	v_lshrrev_b32_e32 v51, 17, v51
	v_mad_i32_i24 v52, v51, s76, v50
	v_mul_u32_u24_e32 v28, 0x300, v51
	v_lshl_add_u32 v28, v52, 2, v28
	v_mul_u32_u24_e32 v40, 0x310, v51
	v_lshl_add_u32 v40, v52, 4, v40
	v_lshlrev_b32_e32 v50, 1, v28
	global_load_dwordx2 v[6:7], v50, s[72:73] nt
	v_or_b32_e32 v50, 1536, v0
	v_mul_u32_u24_e32 v51, 0xaab, v50
	v_lshrrev_b32_e32 v51, 17, v51
	v_mad_i32_i24 v52, v51, s76, v50
	v_mul_u32_u24_e32 v29, 0x300, v51
	v_lshl_add_u32 v29, v52, 2, v29
	v_mul_u32_u24_e32 v41, 0x310, v51
	v_lshl_add_u32 v41, v52, 4, v41
	v_lshlrev_b32_e32 v50, 1, v29
	global_load_dwordx2 v[8:9], v50, s[72:73] nt
	v_or_b32_e32 v50, 2048, v0
	v_mul_u32_u24_e32 v51, 0xaab, v50
	v_lshrrev_b32_e32 v51, 17, v51
	v_mad_i32_i24 v52, v51, s76, v50
	v_mul_u32_u24_e32 v30, 0x300, v51
	v_lshl_add_u32 v30, v52, 2, v30
	v_mul_u32_u24_e32 v42, 0x310, v51
	v_lshl_add_u32 v42, v52, 4, v42
	v_lshlrev_b32_e32 v50, 1, v30
	global_load_dwordx2 v[10:11], v50, s[72:73] nt
	v_or_b32_e32 v50, 2560, v0
	v_mul_u32_u24_e32 v51, 0xaab, v50
	v_lshrrev_b32_e32 v51, 17, v51
	v_mad_i32_i24 v52, v51, s76, v50
	v_mul_u32_u24_e32 v31, 0x300, v51
	v_lshl_add_u32 v31, v52, 2, v31
	v_mul_u32_u24_e32 v43, 0x310, v51
	v_lshl_add_u32 v43, v52, 4, v43
	v_lshlrev_b32_e32 v50, 1, v31
	global_load_dwordx2 v[12:13], v50, s[72:73] nt
	v_or_b32_e32 v50, 3072, v0
	v_mul_u32_u24_e32 v51, 0xaab, v50
	v_lshrrev_b32_e32 v51, 17, v51
	v_mad_i32_i24 v52, v51, s76, v50
	v_mul_u32_u24_e32 v32, 0x300, v51
	v_lshl_add_u32 v32, v52, 2, v32
	v_mul_u32_u24_e32 v44, 0x310, v51
	v_lshl_add_u32 v44, v52, 4, v44
	v_lshlrev_b32_e32 v50, 1, v32
	global_load_dwordx2 v[14:15], v50, s[72:73] nt
	v_or_b32_e32 v50, 3584, v0
	v_mul_u32_u24_e32 v51, 0xaab, v50
	v_lshrrev_b32_e32 v51, 17, v51
	v_mad_i32_i24 v52, v51, s76, v50
	v_mul_u32_u24_e32 v33, 0x300, v51
	v_lshl_add_u32 v33, v52, 2, v33
	v_mul_u32_u24_e32 v45, 0x310, v51
	v_lshl_add_u32 v45, v52, 4, v45
	v_lshlrev_b32_e32 v50, 1, v33
	global_load_dwordx2 v[16:17], v50, s[72:73] nt
	v_or_b32_e32 v50, 4096, v0
	v_mul_u32_u24_e32 v51, 0xaab, v50
	v_lshrrev_b32_e32 v51, 17, v51
	v_mad_i32_i24 v52, v51, s76, v50
	v_mul_u32_u24_e32 v34, 0x300, v51
	v_lshl_add_u32 v34, v52, 2, v34
	v_mul_u32_u24_e32 v46, 0x310, v51
	v_lshl_add_u32 v46, v52, 4, v46
	v_lshlrev_b32_e32 v50, 1, v34
	global_load_dwordx2 v[18:19], v50, s[72:73] nt
	v_or_b32_e32 v50, 4608, v0
	v_mul_u32_u24_e32 v51, 0xaab, v50
	v_lshrrev_b32_e32 v51, 17, v51
	v_mad_i32_i24 v52, v51, s76, v50
	v_mul_u32_u24_e32 v35, 0x300, v51
	v_lshl_add_u32 v35, v52, 2, v35
	v_mul_u32_u24_e32 v47, 0x310, v51
	v_lshl_add_u32 v47, v52, 4, v47
	v_lshlrev_b32_e32 v50, 1, v35
	global_load_dwordx2 v[20:21], v50, s[72:73] nt
	v_or_b32_e32 v50, 5120, v0
	v_mul_u32_u24_e32 v51, 0xaab, v50
	v_lshrrev_b32_e32 v51, 17, v51
	v_mad_i32_i24 v52, v51, s76, v50
	v_mul_u32_u24_e32 v36, 0x300, v51
	v_lshl_add_u32 v36, v52, 2, v36
	v_mul_u32_u24_e32 v48, 0x310, v51
	v_lshl_add_u32 v48, v52, 4, v48
	v_lshlrev_b32_e32 v50, 1, v36
	global_load_dwordx2 v[22:23], v50, s[72:73] nt
	v_or_b32_e32 v50, 5632, v0
	v_mul_u32_u24_e32 v51, 0xaab, v50
	v_lshrrev_b32_e32 v51, 17, v51
	v_mad_i32_i24 v52, v51, s76, v50
	v_mul_u32_u24_e32 v37, 0x300, v51
	v_lshl_add_u32 v37, v52, 2, v37
	v_mul_u32_u24_e32 v49, 0x310, v51
	v_lshl_add_u32 v49, v52, 4, v49
	v_lshlrev_b32_e32 v50, 1, v37
	global_load_dwordx2 v[24:25], v50, s[72:73] nt
	s_waitcnt vmcnt(20) lgkmcnt(0)
	s_barrier
	v_mfma_f32_16x16x32_f16 v[120:123], v[212:215], v[196:199], v[120:123]
	ds_read_b128 v[168:171], v79 offset:40960
	v_mfma_f32_16x16x32_f16 v[124:127], v[216:219], v[196:199], v[124:127]
	ds_read_b128 v[184:187], v82 offset:57344
	v_mfma_f32_16x16x32_f16 v[128:131], v[220:223], v[196:199], v[128:131]
	ds_read_b128 v[188:191], v82 offset:59392
	v_mfma_f32_16x16x32_f16 v[132:135], v[212:215], v[200:203], v[132:135]
	ds_read_b128 v[192:195], v82 offset:61440
	v_mfma_f32_16x16x32_f16 v[136:139], v[216:219], v[200:203], v[136:139]
	ds_read_b128 v[172:175], v79 offset:43008
	v_mfma_f32_16x16x32_f16 v[140:143], v[220:223], v[200:203], v[140:143]
	ds_read_b128 v[176:179], v79 offset:45056
	v_mfma_f32_16x16x32_f16 v[144:147], v[212:215], v[204:207], v[144:147]
	ds_read_b128 v[180:183], v79 offset:47104
	v_mfma_f32_16x16x32_f16 v[148:151], v[216:219], v[204:207], v[148:151]
	v_mfma_f32_16x16x32_f16 v[152:155], v[220:223], v[204:207], v[152:155]
	v_mfma_f32_16x16x32_f16 v[156:159], v[212:215], v[208:211], v[156:159]
	v_mfma_f32_16x16x32_f16 v[160:163], v[216:219], v[208:211], v[160:163]
	v_mfma_f32_16x16x32_f16 v[164:167], v[220:223], v[208:211], v[164:167]
	s_waitcnt lgkmcnt(0)
	v_mfma_f32_16x16x32_f16 v[120:123], v[184:187], v[168:171], v[120:123]
	ds_read_b128 v[196:199], v83 offset:40960
	v_mfma_f32_16x16x32_f16 v[124:127], v[188:191], v[168:171], v[124:127]
	ds_read_b128 v[212:215], v81 offset:57344
	v_mfma_f32_16x16x32_f16 v[128:131], v[192:195], v[168:171], v[128:131]
	ds_read_b128 v[216:219], v81 offset:59392
	v_mfma_f32_16x16x32_f16 v[132:135], v[184:187], v[172:175], v[132:135]
	ds_read_b128 v[220:223], v81 offset:61440
	v_mfma_f32_16x16x32_f16 v[136:139], v[188:191], v[172:175], v[136:139]
	ds_read_b128 v[200:203], v83 offset:43008
	v_mfma_f32_16x16x32_f16 v[140:143], v[192:195], v[172:175], v[140:143]
	ds_read_b128 v[204:207], v83 offset:45056
	v_mfma_f32_16x16x32_f16 v[144:147], v[184:187], v[176:179], v[144:147]
	ds_read_b128 v[208:211], v83 offset:47104
	v_mfma_f32_16x16x32_f16 v[148:151], v[188:191], v[176:179], v[148:151]
	v_mfma_f32_16x16x32_f16 v[152:155], v[192:195], v[176:179], v[152:155]
	v_mfma_f32_16x16x32_f16 v[156:159], v[184:187], v[180:183], v[156:159]
	v_mfma_f32_16x16x32_f16 v[160:163], v[188:191], v[180:183], v[160:163]
	v_mfma_f32_16x16x32_f16 v[164:167], v[192:195], v[180:183], v[164:167]
	s_waitcnt vmcnt(15) lgkmcnt(0)
	s_barrier
	v_mfma_f32_16x16x32_f16 v[120:123], v[212:215], v[196:199], v[120:123]
	ds_read_b128 v[168:171], v100 offset:0
	v_mfma_f32_16x16x32_f16 v[124:127], v[216:219], v[196:199], v[124:127]
	ds_read_b128 v[184:187], v102 offset:16384
	v_mfma_f32_16x16x32_f16 v[128:131], v[220:223], v[196:199], v[128:131]
	ds_read_b128 v[188:191], v102 offset:18432
	v_mfma_f32_16x16x32_f16 v[132:135], v[212:215], v[200:203], v[132:135]
	ds_read_b128 v[192:195], v102 offset:20480
	v_mfma_f32_16x16x32_f16 v[136:139], v[216:219], v[200:203], v[136:139]
	ds_read_b128 v[172:175], v100 offset:2048
	v_mfma_f32_16x16x32_f16 v[140:143], v[220:223], v[200:203], v[140:143]
	ds_read_b128 v[176:179], v100 offset:4096
	v_mfma_f32_16x16x32_f16 v[144:147], v[212:215], v[204:207], v[144:147]
	ds_read_b128 v[180:183], v100 offset:6144
	v_mfma_f32_16x16x32_f16 v[148:151], v[216:219], v[204:207], v[148:151]
	v_mfma_f32_16x16x32_f16 v[152:155], v[220:223], v[204:207], v[152:155]
	v_mfma_f32_16x16x32_f16 v[156:159], v[212:215], v[208:211], v[156:159]
	v_mfma_f32_16x16x32_f16 v[160:163], v[216:219], v[208:211], v[160:163]
	v_mfma_f32_16x16x32_f16 v[164:167], v[220:223], v[208:211], v[164:167]
	s_waitcnt lgkmcnt(0)
	v_mfma_f32_16x16x32_f16 v[120:123], v[184:187], v[168:171], v[120:123]
	ds_read_b128 v[196:199], v101 offset:0
	v_mfma_f32_16x16x32_f16 v[124:127], v[188:191], v[168:171], v[124:127]
	ds_read_b128 v[212:215], v103 offset:16384
	v_mfma_f32_16x16x32_f16 v[128:131], v[192:195], v[168:171], v[128:131]
	ds_read_b128 v[216:219], v103 offset:18432
	v_mfma_f32_16x16x32_f16 v[132:135], v[184:187], v[172:175], v[132:135]
	ds_read_b128 v[220:223], v103 offset:20480
	v_mfma_f32_16x16x32_f16 v[136:139], v[188:191], v[172:175], v[136:139]
	ds_read_b128 v[200:203], v101 offset:2048
	v_mfma_f32_16x16x32_f16 v[140:143], v[192:195], v[172:175], v[140:143]
	ds_read_b128 v[204:207], v101 offset:4096
	v_mfma_f32_16x16x32_f16 v[144:147], v[184:187], v[176:179], v[144:147]
	ds_read_b128 v[208:211], v101 offset:6144
	v_mfma_f32_16x16x32_f16 v[148:151], v[188:191], v[176:179], v[148:151]
	v_mfma_f32_16x16x32_f16 v[152:155], v[192:195], v[176:179], v[152:155]
	v_mfma_f32_16x16x32_f16 v[156:159], v[184:187], v[180:183], v[156:159]
	v_mfma_f32_16x16x32_f16 v[160:163], v[188:191], v[180:183], v[160:163]
	v_mfma_f32_16x16x32_f16 v[164:167], v[192:195], v[180:183], v[164:167]
	s_waitcnt lgkmcnt(0)
	v_mfma_f32_16x16x32_f16 v[120:123], v[212:215], v[196:199], v[120:123]
	v_mfma_f32_16x16x32_f16 v[124:127], v[216:219], v[196:199], v[124:127]
	v_mfma_f32_16x16x32_f16 v[128:131], v[220:223], v[196:199], v[128:131]
	v_mfma_f32_16x16x32_f16 v[132:135], v[212:215], v[200:203], v[132:135]
	v_mfma_f32_16x16x32_f16 v[136:139], v[216:219], v[200:203], v[136:139]
	v_mfma_f32_16x16x32_f16 v[140:143], v[220:223], v[200:203], v[140:143]
	v_mfma_f32_16x16x32_f16 v[144:147], v[212:215], v[204:207], v[144:147]
	v_mfma_f32_16x16x32_f16 v[148:151], v[216:219], v[204:207], v[148:151]
	v_mfma_f32_16x16x32_f16 v[152:155], v[220:223], v[204:207], v[152:155]
	v_mfma_f32_16x16x32_f16 v[156:159], v[212:215], v[208:211], v[156:159]
	v_mfma_f32_16x16x32_f16 v[160:163], v[216:219], v[208:211], v[160:163]
	v_mfma_f32_16x16x32_f16 v[164:167], v[220:223], v[208:211], v[164:167]
	s_branch .Lgk_loop_dn_done
.Lgk_loop_dnB:
	s_waitcnt vmcnt(5) lgkmcnt(0)
	s_barrier
	v_mfma_f32_16x16x32_f16 v[120:123], v[212:215], v[196:199], v[120:123]
	ds_read_b128 v[168:171], v79 offset:40960
	v_mfma_f32_16x16x32_f16 v[124:127], v[216:219], v[196:199], v[124:127]
	ds_read_b128 v[184:187], v82 offset:57344
	v_mfma_f32_16x16x32_f16 v[128:131], v[220:223], v[196:199], v[128:131]
	ds_read_b128 v[188:191], v82 offset:59392
	v_mfma_f32_16x16x32_f16 v[132:135], v[212:215], v[200:203], v[132:135]
	ds_read_b128 v[192:195], v82 offset:61440
	v_mfma_f32_16x16x32_f16 v[136:139], v[216:219], v[200:203], v[136:139]
	ds_read_b128 v[172:175], v79 offset:43008
	v_mfma_f32_16x16x32_f16 v[140:143], v[220:223], v[200:203], v[140:143]
	ds_read_b128 v[176:179], v79 offset:45056
	v_mfma_f32_16x16x32_f16 v[144:147], v[212:215], v[204:207], v[144:147]
	ds_read_b128 v[180:183], v79 offset:47104
	v_mfma_f32_16x16x32_f16 v[148:151], v[216:219], v[204:207], v[148:151]
	v_mfma_f32_16x16x32_f16 v[152:155], v[220:223], v[204:207], v[152:155]
	v_mfma_f32_16x16x32_f16 v[156:159], v[212:215], v[208:211], v[156:159]
	v_mfma_f32_16x16x32_f16 v[160:163], v[216:219], v[208:211], v[160:163]
	v_mfma_f32_16x16x32_f16 v[164:167], v[220:223], v[208:211], v[164:167]
	s_waitcnt lgkmcnt(0)
	v_mfma_f32_16x16x32_f16 v[120:123], v[184:187], v[168:171], v[120:123]
	ds_read_b128 v[196:199], v83 offset:40960
	v_mfma_f32_16x16x32_f16 v[124:127], v[188:191], v[168:171], v[124:127]
	ds_read_b128 v[212:215], v81 offset:57344
	v_mfma_f32_16x16x32_f16 v[128:131], v[192:195], v[168:171], v[128:131]
	ds_read_b128 v[216:219], v81 offset:59392
	v_mfma_f32_16x16x32_f16 v[132:135], v[184:187], v[172:175], v[132:135]
	ds_read_b128 v[220:223], v81 offset:61440
	v_mfma_f32_16x16x32_f16 v[136:139], v[188:191], v[172:175], v[136:139]
	ds_read_b128 v[200:203], v83 offset:43008
	v_mfma_f32_16x16x32_f16 v[140:143], v[192:195], v[172:175], v[140:143]
	ds_read_b128 v[204:207], v83 offset:45056
	v_mfma_f32_16x16x32_f16 v[144:147], v[184:187], v[176:179], v[144:147]
	ds_read_b128 v[208:211], v83 offset:47104
	v_mfma_f32_16x16x32_f16 v[148:151], v[188:191], v[176:179], v[148:151]
	v_mfma_f32_16x16x32_f16 v[152:155], v[192:195], v[176:179], v[152:155]
	v_mfma_f32_16x16x32_f16 v[156:159], v[184:187], v[180:183], v[156:159]
	v_mfma_f32_16x16x32_f16 v[160:163], v[188:191], v[180:183], v[160:163]
	v_mfma_f32_16x16x32_f16 v[164:167], v[192:195], v[180:183], v[164:167]
	s_mov_b32 m0, s25
	s_add_u32 s54, s54, 0x80
	s_addc_u32 s55, s55, 0
	global_load_lds_dwordx4 v84, s[54:55]
	s_mov_b32 m0, s26
	s_add_u32 s56, s56, 0x80
	s_addc_u32 s57, s57, 0
	global_load_lds_dwordx4 v84, s[56:57]
	s_mov_b32 m0, s27
	s_add_u32 s58, s58, 0x80
	s_addc_u32 s59, s59, 0
	global_load_lds_dwordx4 v84, s[58:59]
	s_mov_b32 m0, s28
	s_add_u32 s60, s60, 0x80
	s_addc_u32 s61, s61, 0
	global_load_lds_dwordx4 v84, s[60:61]
	s_mov_b32 m0, s29
	s_add_u32 s62, s62, 0x80
	s_addc_u32 s63, s63, 0
	global_load_lds_dwordx4 v84, s[62:63]
	s_waitcnt vmcnt(5) lgkmcnt(0)
	s_barrier
	v_mfma_f32_16x16x32_f16 v[120:123], v[212:215], v[196:199], v[120:123]
	ds_read_b128 v[168:171], v100 offset:0
	v_mfma_f32_16x16x32_f16 v[124:127], v[216:219], v[196:199], v[124:127]
	ds_read_b128 v[184:187], v102 offset:16384
	v_mfma_f32_16x16x32_f16 v[128:131], v[220:223], v[196:199], v[128:131]
	ds_read_b128 v[188:191], v102 offset:18432
	v_mfma_f32_16x16x32_f16 v[132:135], v[212:215], v[200:203], v[132:135]
	ds_read_b128 v[192:195], v102 offset:20480
	v_mfma_f32_16x16x32_f16 v[136:139], v[216:219], v[200:203], v[136:139]
	ds_read_b128 v[172:175], v100 offset:2048
	v_mfma_f32_16x16x32_f16 v[140:143], v[220:223], v[200:203], v[140:143]
	ds_read_b128 v[176:179], v100 offset:4096
	v_mfma_f32_16x16x32_f16 v[144:147], v[212:215], v[204:207], v[144:147]
	ds_read_b128 v[180:183], v100 offset:6144
	v_mfma_f32_16x16x32_f16 v[148:151], v[216:219], v[204:207], v[148:151]
	v_mfma_f32_16x16x32_f16 v[152:155], v[220:223], v[204:207], v[152:155]
	v_mfma_f32_16x16x32_f16 v[156:159], v[212:215], v[208:211], v[156:159]
	v_mfma_f32_16x16x32_f16 v[160:163], v[216:219], v[208:211], v[160:163]
	v_mfma_f32_16x16x32_f16 v[164:167], v[220:223], v[208:211], v[164:167]
	s_waitcnt lgkmcnt(0)
	v_mfma_f32_16x16x32_f16 v[120:123], v[184:187], v[168:171], v[120:123]
	ds_read_b128 v[196:199], v101 offset:0
	v_mfma_f32_16x16x32_f16 v[124:127], v[188:191], v[168:171], v[124:127]
	ds_read_b128 v[212:215], v103 offset:16384
	v_mfma_f32_16x16x32_f16 v[128:131], v[192:195], v[168:171], v[128:131]
	ds_read_b128 v[216:219], v103 offset:18432
	v_mfma_f32_16x16x32_f16 v[132:135], v[184:187], v[172:175], v[132:135]
	ds_read_b128 v[220:223], v103 offset:20480
	v_mfma_f32_16x16x32_f16 v[136:139], v[188:191], v[172:175], v[136:139]
	ds_read_b128 v[200:203], v101 offset:2048
	v_mfma_f32_16x16x32_f16 v[140:143], v[192:195], v[172:175], v[140:143]
	ds_read_b128 v[204:207], v101 offset:4096
	v_mfma_f32_16x16x32_f16 v[144:147], v[184:187], v[176:179], v[144:147]
	ds_read_b128 v[208:211], v101 offset:6144
	v_mfma_f32_16x16x32_f16 v[148:151], v[188:191], v[176:179], v[148:151]
	v_mfma_f32_16x16x32_f16 v[152:155], v[192:195], v[176:179], v[152:155]
	v_mfma_f32_16x16x32_f16 v[156:159], v[184:187], v[180:183], v[156:159]
	v_mfma_f32_16x16x32_f16 v[160:163], v[188:191], v[180:183], v[160:163]
	v_mfma_f32_16x16x32_f16 v[164:167], v[192:195], v[180:183], v[164:167]
	s_mov_b32 m0, s30
	s_add_u32 s54, s54, 0x80
	s_addc_u32 s55, s55, 0
	global_load_lds_dwordx4 v84, s[54:55]
	s_mov_b32 m0, s31
	s_add_u32 s56, s56, 0x80
	s_addc_u32 s57, s57, 0
	global_load_lds_dwordx4 v84, s[56:57]
	s_mov_b32 m0, s33
	s_add_u32 s58, s58, 0x80
	s_addc_u32 s59, s59, 0
	global_load_lds_dwordx4 v84, s[58:59]
	s_mov_b32 m0, s34
	s_add_u32 s60, s60, 0x80
	s_addc_u32 s61, s61, 0
	global_load_lds_dwordx4 v84, s[60:61]
	s_mov_b32 m0, s35
	s_add_u32 s62, s62, 0x80
	s_addc_u32 s63, s63, 0
	global_load_lds_dwordx4 v84, s[62:63]
	s_waitcnt vmcnt(5) lgkmcnt(0)
	s_barrier
	v_mfma_f32_16x16x32_f16 v[120:123], v[212:215], v[196:199], v[120:123]
	ds_read_b128 v[168:171], v79 offset:0
	v_mfma_f32_16x16x32_f16 v[124:127], v[216:219], v[196:199], v[124:127]
	ds_read_b128 v[184:187], v82 offset:16384
	v_mfma_f32_16x16x32_f16 v[128:131], v[220:223], v[196:199], v[128:131]
	ds_read_b128 v[188:191], v82 offset:18432
	v_mfma_f32_16x16x32_f16 v[132:135], v[212:215], v[200:203], v[132:135]
	ds_read_b128 v[192:195], v82 offset:20480
	v_mfma_f32_16x16x32_f16 v[136:139], v[216:219], v[200:203], v[136:139]
	ds_read_b128 v[172:175], v79 offset:2048
	v_mfma_f32_16x16x32_f16 v[140:143], v[220:223], v[200:203], v[140:143]
	ds_read_b128 v[176:179], v79 offset:4096
	v_mfma_f32_16x16x32_f16 v[144:147], v[212:215], v[204:207], v[144:147]
	ds_read_b128 v[180:183], v79 offset:6144
	v_mfma_f32_16x16x32_f16 v[148:151], v[216:219], v[204:207], v[148:151]
	v_mfma_f32_16x16x32_f16 v[152:155], v[220:223], v[204:207], v[152:155]
	v_mfma_f32_16x16x32_f16 v[156:159], v[212:215], v[208:211], v[156:159]
	v_mfma_f32_16x16x32_f16 v[160:163], v[216:219], v[208:211], v[160:163]
	v_mfma_f32_16x16x32_f16 v[164:167], v[220:223], v[208:211], v[164:167]
	s_waitcnt lgkmcnt(0)
	v_mfma_f32_16x16x32_f16 v[120:123], v[184:187], v[168:171], v[120:123]
	ds_read_b128 v[196:199], v83 offset:0
	v_mfma_f32_16x16x32_f16 v[124:127], v[188:191], v[168:171], v[124:127]
	ds_read_b128 v[212:215], v81 offset:16384
	v_mfma_f32_16x16x32_f16 v[128:131], v[192:195], v[168:171], v[128:131]
	ds_read_b128 v[216:219], v81 offset:18432
	v_mfma_f32_16x16x32_f16 v[132:135], v[184:187], v[172:175], v[132:135]
	ds_read_b128 v[220:223], v81 offset:20480
	v_mfma_f32_16x16x32_f16 v[136:139], v[188:191], v[172:175], v[136:139]
	ds_read_b128 v[200:203], v83 offset:2048
	v_mfma_f32_16x16x32_f16 v[140:143], v[192:195], v[172:175], v[140:143]
	ds_read_b128 v[204:207], v83 offset:4096
	v_mfma_f32_16x16x32_f16 v[144:147], v[184:187], v[176:179], v[144:147]
	ds_read_b128 v[208:211], v83 offset:6144
	v_mfma_f32_16x16x32_f16 v[148:151], v[188:191], v[176:179], v[148:151]
	v_mfma_f32_16x16x32_f16 v[152:155], v[192:195], v[176:179], v[152:155]
	v_mfma_f32_16x16x32_f16 v[156:159], v[184:187], v[180:183], v[156:159]
	v_mfma_f32_16x16x32_f16 v[160:163], v[188:191], v[180:183], v[160:163]
	v_mfma_f32_16x16x32_f16 v[164:167], v[192:195], v[180:183], v[164:167]
	s_mov_b32 m0, s36
	s_add_u32 s54, s54, 0x80
	s_addc_u32 s55, s55, 0
	global_load_lds_dwordx4 v84, s[54:55]
	s_mov_b32 m0, s37
	s_add_u32 s56, s56, 0x80
	s_addc_u32 s57, s57, 0
	global_load_lds_dwordx4 v84, s[56:57]
	s_mov_b32 m0, s38
	s_add_u32 s58, s58, 0x80
	s_addc_u32 s59, s59, 0
	global_load_lds_dwordx4 v84, s[58:59]
	s_mov_b32 m0, s39
	s_add_u32 s60, s60, 0x80
	s_addc_u32 s61, s61, 0
	global_load_lds_dwordx4 v84, s[60:61]
	s_mov_b32 m0, s40
	s_add_u32 s62, s62, 0x80
	s_addc_u32 s63, s63, 0
	global_load_lds_dwordx4 v84, s[62:63]
	s_add_i32 s64, s64, -1
	s_cmp_lg_u32 s64, 0
	s_cbranch_scc1 .Lgk_loop_dnB
	v_bfe_u32 v96, v0, 4, 2
	v_lshlrev_b32_e32 v96, 2, v96
	s_add_i32 s77, s23, s0
	v_or_b32_e32 v98, s77, v96
	v_ashrrev_i32_e32 v99, 31, v98
	v_lshl_add_u64 v[98:99], v[98:99], 2, s[14:15]
	global_load_dwordx4 v[104:107], v[98:99], off
	global_load_dwordx4 v[108:111], v[98:99], off offset:64
	global_load_dwordx4 v[112:115], v[98:99], off offset:128
	v_mov_b32_e32 v50, v0
	v_mul_u32_u24_e32 v51, 0xaab, v50
	v_lshrrev_b32_e32 v51, 17, v51
	v_mad_i32_i24 v52, v51, s76, v50
	v_mul_u32_u24_e32 v26, 0x300, v51
	v_lshl_add_u32 v26, v52, 2, v26
	v_mul_u32_u24_e32 v38, 0x310, v51
	v_lshl_add_u32 v38, v52, 4, v38
	v_lshlrev_b32_e32 v50, 1, v26
	global_load_dwordx2 v[2:3], v50, s[72:73] nt
	v_or_b32_e32 v50, 512, v0
	v_mul_u32_u24_e32 v51, 0xaab, v50
	v_lshrrev_b32_e32 v51, 17, v51
	v_mad_i32_i24 v52, v51, s76, v50
	v_mul_u32_u24_e32 v27, 0x300, v51
	v_lshl_add_u32 v27, v52, 2, v27
	v_mul_u32_u24_e32 v39, 0x310, v51
	v_lshl_add_u32 v39, v52, 4, v39
	v_lshlrev_b32_e32 v50, 1, v27
	global_load_dwordx2 v[4:5], v50, s[72:73] nt
	v_or_b32_e32 v50, 1024, v0
	v_mul_u32_u24_e32 v51, 0xaab, v50
	v_lshrrev_b32_e32 v51, 17, v51
	v_mad_i32_i24 v52, v51, s76, v50
	v_mul_u32_u24_e32 v28, 0x300, v51
	v_lshl_add_u32 v28, v52, 2, v28
	v_mul_u32_u24_e32 v40, 0x310, v51
	v_lshl_add_u32 v40, v52, 4, v40
	v_lshlrev_b32_e32 v50, 1, v28
	global_load_dwordx2 v[6:7], v50, s[72:73] nt
	v_or_b32_e32 v50, 1536, v0
	v_mul_u32_u24_e32 v51, 0xaab, v50
	v_lshrrev_b32_e32 v51, 17, v51
	v_mad_i32_i24 v52, v51, s76, v50
	v_mul_u32_u24_e32 v29, 0x300, v51
	v_lshl_add_u32 v29, v52, 2, v29
	v_mul_u32_u24_e32 v41, 0x310, v51
	v_lshl_add_u32 v41, v52, 4, v41
	v_lshlrev_b32_e32 v50, 1, v29
	global_load_dwordx2 v[8:9], v50, s[72:73] nt
	v_or_b32_e32 v50, 2048, v0
	v_mul_u32_u24_e32 v51, 0xaab, v50
	v_lshrrev_b32_e32 v51, 17, v51
	v_mad_i32_i24 v52, v51, s76, v50
	v_mul_u32_u24_e32 v30, 0x300, v51
	v_lshl_add_u32 v30, v52, 2, v30
	v_mul_u32_u24_e32 v42, 0x310, v51
	v_lshl_add_u32 v42, v52, 4, v42
	v_lshlrev_b32_e32 v50, 1, v30
	global_load_dwordx2 v[10:11], v50, s[72:73] nt
	v_or_b32_e32 v50, 2560, v0
	v_mul_u32_u24_e32 v51, 0xaab, v50
	v_lshrrev_b32_e32 v51, 17, v51
	v_mad_i32_i24 v52, v51, s76, v50
	v_mul_u32_u24_e32 v31, 0x300, v51
	v_lshl_add_u32 v31, v52, 2, v31
	v_mul_u32_u24_e32 v43, 0x310, v51
	v_lshl_add_u32 v43, v52, 4, v43
	v_lshlrev_b32_e32 v50, 1, v31
	global_load_dwordx2 v[12:13], v50, s[72:73] nt
	v_or_b32_e32 v50, 3072, v0
	v_mul_u32_u24_e32 v51, 0xaab, v50
	v_lshrrev_b32_e32 v51, 17, v51
	v_mad_i32_i24 v52, v51, s76, v50
	v_mul_u32_u24_e32 v32, 0x300, v51
	v_lshl_add_u32 v32, v52, 2, v32
	v_mul_u32_u24_e32 v44, 0x310, v51
	v_lshl_add_u32 v44, v52, 4, v44
	v_lshlrev_b32_e32 v50, 1, v32
	global_load_dwordx2 v[14:15], v50, s[72:73] nt
	v_or_b32_e32 v50, 3584, v0
	v_mul_u32_u24_e32 v51, 0xaab, v50
	v_lshrrev_b32_e32 v51, 17, v51
	v_mad_i32_i24 v52, v51, s76, v50
	v_mul_u32_u24_e32 v33, 0x300, v51
	v_lshl_add_u32 v33, v52, 2, v33
	v_mul_u32_u24_e32 v45, 0x310, v51
	v_lshl_add_u32 v45, v52, 4, v45
	v_lshlrev_b32_e32 v50, 1, v33
	global_load_dwordx2 v[16:17], v50, s[72:73] nt
	v_or_b32_e32 v50, 4096, v0
	v_mul_u32_u24_e32 v51, 0xaab, v50
	v_lshrrev_b32_e32 v51, 17, v51
	v_mad_i32_i24 v52, v51, s76, v50
	v_mul_u32_u24_e32 v34, 0x300, v51
	v_lshl_add_u32 v34, v52, 2, v34
	v_mul_u32_u24_e32 v46, 0x310, v51
	v_lshl_add_u32 v46, v52, 4, v46
	v_lshlrev_b32_e32 v50, 1, v34
	global_load_dwordx2 v[18:19], v50, s[72:73] nt
	v_or_b32_e32 v50, 4608, v0
	v_mul_u32_u24_e32 v51, 0xaab, v50
	v_lshrrev_b32_e32 v51, 17, v51
	v_mad_i32_i24 v52, v51, s76, v50
	v_mul_u32_u24_e32 v35, 0x300, v51
	v_lshl_add_u32 v35, v52, 2, v35
	v_mul_u32_u24_e32 v47, 0x310, v51
	v_lshl_add_u32 v47, v52, 4, v47
	v_lshlrev_b32_e32 v50, 1, v35
	global_load_dwordx2 v[20:21], v50, s[72:73] nt
	v_or_b32_e32 v50, 5120, v0
	v_mul_u32_u24_e32 v51, 0xaab, v50
	v_lshrrev_b32_e32 v51, 17, v51
	v_mad_i32_i24 v52, v51, s76, v50
	v_mul_u32_u24_e32 v36, 0x300, v51
	v_lshl_add_u32 v36, v52, 2, v36
	v_mul_u32_u24_e32 v48, 0x310, v51
	v_lshl_add_u32 v48, v52, 4, v48
	v_lshlrev_b32_e32 v50, 1, v36
	global_load_dwordx2 v[22:23], v50, s[72:73] nt
	v_or_b32_e32 v50, 5632, v0
	v_mul_u32_u24_e32 v51, 0xaab, v50
	v_lshrrev_b32_e32 v51, 17, v51
	v_mad_i32_i24 v52, v51, s76, v50
	v_mul_u32_u24_e32 v37, 0x300, v51
	v_lshl_add_u32 v37, v52, 2, v37
	v_mul_u32_u24_e32 v49, 0x310, v51
	v_lshl_add_u32 v49, v52, 4, v49
	v_lshlrev_b32_e32 v50, 1, v37
	global_load_dwordx2 v[24:25], v50, s[72:73] nt
	s_waitcnt vmcnt(20) lgkmcnt(0)
	s_barrier
	v_mfma_f32_16x16x32_f16 v[120:123], v[212:215], v[196:199], v[120:123]
	ds_read_b128 v[168:171], v79 offset:40960
	v_mfma_f32_16x16x32_f16 v[124:127], v[216:219], v[196:199], v[124:127]
	ds_read_b128 v[184:187], v82 offset:57344
	v_mfma_f32_16x16x32_f16 v[128:131], v[220:223], v[196:199], v[128:131]
	ds_read_b128 v[188:191], v82 offset:59392
	v_mfma_f32_16x16x32_f16 v[132:135], v[212:215], v[200:203], v[132:135]
	ds_read_b128 v[192:195], v82 offset:61440
	v_mfma_f32_16x16x32_f16 v[136:139], v[216:219], v[200:203], v[136:139]
	ds_read_b128 v[172:175], v79 offset:43008
	v_mfma_f32_16x16x32_f16 v[140:143], v[220:223], v[200:203], v[140:143]
	ds_read_b128 v[176:179], v79 offset:45056
	v_mfma_f32_16x16x32_f16 v[144:147], v[212:215], v[204:207], v[144:147]
	ds_read_b128 v[180:183], v79 offset:47104
	v_mfma_f32_16x16x32_f16 v[148:151], v[216:219], v[204:207], v[148:151]
	v_mfma_f32_16x16x32_f16 v[152:155], v[220:223], v[204:207], v[152:155]
	v_mfma_f32_16x16x32_f16 v[156:159], v[212:215], v[208:211], v[156:159]
	v_mfma_f32_16x16x32_f16 v[160:163], v[216:219], v[208:211], v[160:163]
	v_mfma_f32_16x16x32_f16 v[164:167], v[220:223], v[208:211], v[164:167]
	s_waitcnt lgkmcnt(0)
	v_mfma_f32_16x16x32_f16 v[120:123], v[184:187], v[168:171], v[120:123]
	ds_read_b128 v[196:199], v83 offset:40960
	v_mfma_f32_16x16x32_f16 v[124:127], v[188:191], v[168:171], v[124:127]
	ds_read_b128 v[212:215], v81 offset:57344
	v_mfma_f32_16x16x32_f16 v[128:131], v[192:195], v[168:171], v[128:131]
	ds_read_b128 v[216:219], v81 offset:59392
	v_mfma_f32_16x16x32_f16 v[132:135], v[184:187], v[172:175], v[132:135]
	ds_read_b128 v[220:223], v81 offset:61440
	v_mfma_f32_16x16x32_f16 v[136:139], v[188:191], v[172:175], v[136:139]
	ds_read_b128 v[200:203], v83 offset:43008
	v_mfma_f32_16x16x32_f16 v[140:143], v[192:195], v[172:175], v[140:143]
	ds_read_b128 v[204:207], v83 offset:45056
	v_mfma_f32_16x16x32_f16 v[144:147], v[184:187], v[176:179], v[144:147]
	ds_read_b128 v[208:211], v83 offset:47104
	v_mfma_f32_16x16x32_f16 v[148:151], v[188:191], v[176:179], v[148:151]
	v_mfma_f32_16x16x32_f16 v[152:155], v[192:195], v[176:179], v[152:155]
	v_mfma_f32_16x16x32_f16 v[156:159], v[184:187], v[180:183], v[156:159]
	v_mfma_f32_16x16x32_f16 v[160:163], v[188:191], v[180:183], v[160:163]
	v_mfma_f32_16x16x32_f16 v[164:167], v[192:195], v[180:183], v[164:167]
	s_waitcnt vmcnt(15) lgkmcnt(0)
	s_barrier
	v_mfma_f32_16x16x32_f16 v[120:123], v[212:215], v[196:199], v[120:123]
	ds_read_b128 v[168:171], v100 offset:0
	v_mfma_f32_16x16x32_f16 v[124:127], v[216:219], v[196:199], v[124:127]
	ds_read_b128 v[184:187], v102 offset:16384
	v_mfma_f32_16x16x32_f16 v[128:131], v[220:223], v[196:199], v[128:131]
	ds_read_b128 v[188:191], v102 offset:18432
	v_mfma_f32_16x16x32_f16 v[132:135], v[212:215], v[200:203], v[132:135]
	ds_read_b128 v[192:195], v102 offset:20480
	v_mfma_f32_16x16x32_f16 v[136:139], v[216:219], v[200:203], v[136:139]
	ds_read_b128 v[172:175], v100 offset:2048
	v_mfma_f32_16x16x32_f16 v[140:143], v[220:223], v[200:203], v[140:143]
	ds_read_b128 v[176:179], v100 offset:4096
	v_mfma_f32_16x16x32_f16 v[144:147], v[212:215], v[204:207], v[144:147]
	ds_read_b128 v[180:183], v100 offset:6144
	v_mfma_f32_16x16x32_f16 v[148:151], v[216:219], v[204:207], v[148:151]
	v_mfma_f32_16x16x32_f16 v[152:155], v[220:223], v[204:207], v[152:155]
	v_mfma_f32_16x16x32_f16 v[156:159], v[212:215], v[208:211], v[156:159]
	v_mfma_f32_16x16x32_f16 v[160:163], v[216:219], v[208:211], v[160:163]
	v_mfma_f32_16x16x32_f16 v[164:167], v[220:223], v[208:211], v[164:167]
	s_waitcnt lgkmcnt(0)
	v_mfma_f32_16x16x32_f16 v[120:123], v[184:187], v[168:171], v[120:123]
	ds_read_b128 v[196:199], v101 offset:0
	v_mfma_f32_16x16x32_f16 v[124:127], v[188:191], v[168:171], v[124:127]
	ds_read_b128 v[212:215], v103 offset:16384
	v_mfma_f32_16x16x32_f16 v[128:131], v[192:195], v[168:171], v[128:131]
	ds_read_b128 v[216:219], v103 offset:18432
	v_mfma_f32_16x16x32_f16 v[132:135], v[184:187], v[172:175], v[132:135]
	ds_read_b128 v[220:223], v103 offset:20480
	v_mfma_f32_16x16x32_f16 v[136:139], v[188:191], v[172:175], v[136:139]
	ds_read_b128 v[200:203], v101 offset:2048
	v_mfma_f32_16x16x32_f16 v[140:143], v[192:195], v[172:175], v[140:143]
	ds_read_b128 v[204:207], v101 offset:4096
	v_mfma_f32_16x16x32_f16 v[144:147], v[184:187], v[176:179], v[144:147]
	ds_read_b128 v[208:211], v101 offset:6144
	v_mfma_f32_16x16x32_f16 v[148:151], v[188:191], v[176:179], v[148:151]
	v_mfma_f32_16x16x32_f16 v[152:155], v[192:195], v[176:179], v[152:155]
	v_mfma_f32_16x16x32_f16 v[156:159], v[184:187], v[180:183], v[156:159]
	v_mfma_f32_16x16x32_f16 v[160:163], v[188:191], v[180:183], v[160:163]
	v_mfma_f32_16x16x32_f16 v[164:167], v[192:195], v[180:183], v[164:167]
	s_waitcnt lgkmcnt(0)
	v_mfma_f32_16x16x32_f16 v[120:123], v[212:215], v[196:199], v[120:123]
	v_mfma_f32_16x16x32_f16 v[124:127], v[216:219], v[196:199], v[124:127]
	v_mfma_f32_16x16x32_f16 v[128:131], v[220:223], v[196:199], v[128:131]
	v_mfma_f32_16x16x32_f16 v[132:135], v[212:215], v[200:203], v[132:135]
	v_mfma_f32_16x16x32_f16 v[136:139], v[216:219], v[200:203], v[136:139]
	v_mfma_f32_16x16x32_f16 v[140:143], v[220:223], v[200:203], v[140:143]
	v_mfma_f32_16x16x32_f16 v[144:147], v[212:215], v[204:207], v[144:147]
	v_mfma_f32_16x16x32_f16 v[148:151], v[216:219], v[204:207], v[148:151]
	v_mfma_f32_16x16x32_f16 v[152:155], v[220:223], v[204:207], v[152:155]
	v_mfma_f32_16x16x32_f16 v[156:159], v[212:215], v[208:211], v[156:159]
	v_mfma_f32_16x16x32_f16 v[160:163], v[216:219], v[208:211], v[160:163]
	v_mfma_f32_16x16x32_f16 v[164:167], v[220:223], v[208:211], v[164:167]
.Lgk_loop_dn_done:
	s_nop 7
	s_nop 3
	s_movk_i32 s4, 0x310
	v_mul_lo_u32 v1, v1, s4
	v_or_b32_e32 v97, s23, v96
	v_lshlrev_b32_e32 v97, 2, v97
	v_add3_u32 v1, 0, v97, v1
	s_waitcnt lgkmcnt(0)
	s_barrier
	s_waitcnt vmcnt(0)
	v_pk_add_f32 v[120:121], v[104:105], v[120:121]
	v_pk_add_f32 v[122:123], v[106:107], v[122:123]
	ds_write_b128 v1, v[120:123] offset:0
	v_pk_add_f32 v[124:125], v[108:109], v[124:125]
	v_pk_add_f32 v[126:127], v[110:111], v[126:127]
	ds_write_b128 v1, v[124:127] offset:64
	v_pk_add_f32 v[128:129], v[112:113], v[128:129]
	v_pk_add_f32 v[130:131], v[114:115], v[130:131]
	ds_write_b128 v1, v[128:131] offset:128
	v_pk_add_f32 v[132:133], v[104:105], v[132:133]
	v_pk_add_f32 v[134:135], v[106:107], v[134:135]
	ds_write_b128 v1, v[132:135] offset:12544
	v_pk_add_f32 v[136:137], v[108:109], v[136:137]
	v_pk_add_f32 v[138:139], v[110:111], v[138:139]
	ds_write_b128 v1, v[136:139] offset:12608
	v_pk_add_f32 v[140:141], v[112:113], v[140:141]
	v_pk_add_f32 v[142:143], v[114:115], v[142:143]
	ds_write_b128 v1, v[140:143] offset:12672
	v_pk_add_f32 v[144:145], v[104:105], v[144:145]
	v_pk_add_f32 v[146:147], v[106:107], v[146:147]
	ds_write_b128 v1, v[144:147] offset:25088
	v_pk_add_f32 v[148:149], v[108:109], v[148:149]
	v_pk_add_f32 v[150:151], v[110:111], v[150:151]
	ds_write_b128 v1, v[148:151] offset:25152
	v_pk_add_f32 v[152:153], v[112:113], v[152:153]
	v_pk_add_f32 v[154:155], v[114:115], v[154:155]
	ds_write_b128 v1, v[152:155] offset:25216
	v_pk_add_f32 v[156:157], v[104:105], v[156:157]
	v_pk_add_f32 v[158:159], v[106:107], v[158:159]
	ds_write_b128 v1, v[156:159] offset:37632
	v_pk_add_f32 v[160:161], v[108:109], v[160:161]
	v_pk_add_f32 v[162:163], v[110:111], v[162:163]
	ds_write_b128 v1, v[160:163] offset:37696
	v_pk_add_f32 v[164:165], v[112:113], v[164:165]
	v_pk_add_f32 v[166:167], v[114:115], v[166:167]
	ds_write_b128 v1, v[164:167] offset:37760
	s_waitcnt lgkmcnt(0)
	s_barrier
	ds_read_b128 v[120:123], v38
	ds_read_b128 v[124:127], v39
	ds_read_b128 v[128:131], v40
	ds_read_b128 v[132:135], v41
	ds_read_b128 v[136:139], v42
	ds_read_b128 v[140:143], v43
	ds_read_b128 v[144:147], v44
	ds_read_b128 v[148:151], v45
	ds_read_b128 v[152:155], v46
	ds_read_b128 v[156:159], v47
	ds_read_b128 v[160:163], v48
	ds_read_b128 v[164:167], v49
	v_cvt_f32_f16_e32 v50, v2
	v_cvt_f32_f16_sdwa v51, v2 dst_sel:DWORD dst_unused:UNUSED_PAD src0_sel:WORD_1
	v_cvt_f32_f16_e32 v52, v3
	v_cvt_f32_f16_sdwa v53, v3 dst_sel:DWORD dst_unused:UNUSED_PAD src0_sel:WORD_1
	v_lshlrev_b32_e32 v26, 2, v26
	s_waitcnt lgkmcnt(11)
	v_pk_add_f32 v[120:121], v[120:121], v[50:51]
	v_pk_add_f32 v[122:123], v[122:123], v[52:53]
	global_store_dwordx4 v26, v[120:123], s[74:75] nt
	v_cvt_f32_f16_e32 v50, v4
	v_cvt_f32_f16_sdwa v51, v4 dst_sel:DWORD dst_unused:UNUSED_PAD src0_sel:WORD_1
	v_cvt_f32_f16_e32 v52, v5
	v_cvt_f32_f16_sdwa v53, v5 dst_sel:DWORD dst_unused:UNUSED_PAD src0_sel:WORD_1
	v_lshlrev_b32_e32 v27, 2, v27
	s_waitcnt lgkmcnt(10)
	v_pk_add_f32 v[124:125], v[124:125], v[50:51]
	v_pk_add_f32 v[126:127], v[126:127], v[52:53]
	global_store_dwordx4 v27, v[124:127], s[74:75] nt
	v_cvt_f32_f16_e32 v50, v6
	v_cvt_f32_f16_sdwa v51, v6 dst_sel:DWORD dst_unused:UNUSED_PAD src0_sel:WORD_1
	v_cvt_f32_f16_e32 v52, v7
	v_cvt_f32_f16_sdwa v53, v7 dst_sel:DWORD dst_unused:UNUSED_PAD src0_sel:WORD_1
	v_lshlrev_b32_e32 v28, 2, v28
	s_waitcnt lgkmcnt(9)
	v_pk_add_f32 v[128:129], v[128:129], v[50:51]
	v_pk_add_f32 v[130:131], v[130:131], v[52:53]
	global_store_dwordx4 v28, v[128:131], s[74:75] nt
	v_cvt_f32_f16_e32 v50, v8
	v_cvt_f32_f16_sdwa v51, v8 dst_sel:DWORD dst_unused:UNUSED_PAD src0_sel:WORD_1
	v_cvt_f32_f16_e32 v52, v9
	v_cvt_f32_f16_sdwa v53, v9 dst_sel:DWORD dst_unused:UNUSED_PAD src0_sel:WORD_1
	v_lshlrev_b32_e32 v29, 2, v29
	s_waitcnt lgkmcnt(8)
	v_pk_add_f32 v[132:133], v[132:133], v[50:51]
	v_pk_add_f32 v[134:135], v[134:135], v[52:53]
	global_store_dwordx4 v29, v[132:135], s[74:75] nt
	v_cvt_f32_f16_e32 v50, v10
	v_cvt_f32_f16_sdwa v51, v10 dst_sel:DWORD dst_unused:UNUSED_PAD src0_sel:WORD_1
	v_cvt_f32_f16_e32 v52, v11
	v_cvt_f32_f16_sdwa v53, v11 dst_sel:DWORD dst_unused:UNUSED_PAD src0_sel:WORD_1
	v_lshlrev_b32_e32 v30, 2, v30
	s_waitcnt lgkmcnt(7)
	v_pk_add_f32 v[136:137], v[136:137], v[50:51]
	v_pk_add_f32 v[138:139], v[138:139], v[52:53]
	global_store_dwordx4 v30, v[136:139], s[74:75] nt
	v_cvt_f32_f16_e32 v50, v12
	v_cvt_f32_f16_sdwa v51, v12 dst_sel:DWORD dst_unused:UNUSED_PAD src0_sel:WORD_1
	v_cvt_f32_f16_e32 v52, v13
	v_cvt_f32_f16_sdwa v53, v13 dst_sel:DWORD dst_unused:UNUSED_PAD src0_sel:WORD_1
	v_lshlrev_b32_e32 v31, 2, v31
	s_waitcnt lgkmcnt(6)
	v_pk_add_f32 v[140:141], v[140:141], v[50:51]
	v_pk_add_f32 v[142:143], v[142:143], v[52:53]
	global_store_dwordx4 v31, v[140:143], s[74:75] nt
	v_cvt_f32_f16_e32 v50, v14
	v_cvt_f32_f16_sdwa v51, v14 dst_sel:DWORD dst_unused:UNUSED_PAD src0_sel:WORD_1
	v_cvt_f32_f16_e32 v52, v15
	v_cvt_f32_f16_sdwa v53, v15 dst_sel:DWORD dst_unused:UNUSED_PAD src0_sel:WORD_1
	v_lshlrev_b32_e32 v32, 2, v32
	s_waitcnt lgkmcnt(5)
	v_pk_add_f32 v[144:145], v[144:145], v[50:51]
	v_pk_add_f32 v[146:147], v[146:147], v[52:53]
	global_store_dwordx4 v32, v[144:147], s[74:75] nt
	v_cvt_f32_f16_e32 v50, v16
	v_cvt_f32_f16_sdwa v51, v16 dst_sel:DWORD dst_unused:UNUSED_PAD src0_sel:WORD_1
	v_cvt_f32_f16_e32 v52, v17
	v_cvt_f32_f16_sdwa v53, v17 dst_sel:DWORD dst_unused:UNUSED_PAD src0_sel:WORD_1
	v_lshlrev_b32_e32 v33, 2, v33
	s_waitcnt lgkmcnt(4)
	v_pk_add_f32 v[148:149], v[148:149], v[50:51]
	v_pk_add_f32 v[150:151], v[150:151], v[52:53]
	global_store_dwordx4 v33, v[148:151], s[74:75] nt
	v_cvt_f32_f16_e32 v50, v18
	v_cvt_f32_f16_sdwa v51, v18 dst_sel:DWORD dst_unused:UNUSED_PAD src0_sel:WORD_1
	v_cvt_f32_f16_e32 v52, v19
	v_cvt_f32_f16_sdwa v53, v19 dst_sel:DWORD dst_unused:UNUSED_PAD src0_sel:WORD_1
	v_lshlrev_b32_e32 v34, 2, v34
	s_waitcnt lgkmcnt(3)
	v_pk_add_f32 v[152:153], v[152:153], v[50:51]
	v_pk_add_f32 v[154:155], v[154:155], v[52:53]
	global_store_dwordx4 v34, v[152:155], s[74:75] nt
	v_cvt_f32_f16_e32 v50, v20
	v_cvt_f32_f16_sdwa v51, v20 dst_sel:DWORD dst_unused:UNUSED_PAD src0_sel:WORD_1
	v_cvt_f32_f16_e32 v52, v21
	v_cvt_f32_f16_sdwa v53, v21 dst_sel:DWORD dst_unused:UNUSED_PAD src0_sel:WORD_1
	v_lshlrev_b32_e32 v35, 2, v35
	s_waitcnt lgkmcnt(2)
	v_pk_add_f32 v[156:157], v[156:157], v[50:51]
	v_pk_add_f32 v[158:159], v[158:159], v[52:53]
	global_store_dwordx4 v35, v[156:159], s[74:75] nt
	v_cvt_f32_f16_e32 v50, v22
	v_cvt_f32_f16_sdwa v51, v22 dst_sel:DWORD dst_unused:UNUSED_PAD src0_sel:WORD_1
	v_cvt_f32_f16_e32 v52, v23
	v_cvt_f32_f16_sdwa v53, v23 dst_sel:DWORD dst_unused:UNUSED_PAD src0_sel:WORD_1
	v_lshlrev_b32_e32 v36, 2, v36
	s_waitcnt lgkmcnt(1)
	v_pk_add_f32 v[160:161], v[160:161], v[50:51]
	v_pk_add_f32 v[162:163], v[162:163], v[52:53]
	global_store_dwordx4 v36, v[160:163], s[74:75] nt
	v_cvt_f32_f16_e32 v50, v24
	v_cvt_f32_f16_sdwa v51, v24 dst_sel:DWORD dst_unused:UNUSED_PAD src0_sel:WORD_1
	v_cvt_f32_f16_e32 v52, v25
	v_cvt_f32_f16_sdwa v53, v25 dst_sel:DWORD dst_unused:UNUSED_PAD src0_sel:WORD_1
	v_lshlrev_b32_e32 v37, 2, v37
	s_waitcnt lgkmcnt(0)
	v_pk_add_f32 v[164:165], v[164:165], v[50:51]
	v_pk_add_f32 v[166:167], v[166:167], v[52:53]
	global_store_dwordx4 v37, v[164:167], s[74:75] nt
	s_endpgm
	.p2align	8

amdhsa.kernels:
  - .agpr_count:     0
    .args:
      - .offset:         0
        .size:           144
        .value_kind:     by_value
    .group_segment_fixed_size: 16640
    .kernarg_segment_align: 8
    .kernarg_segment_size: 144
    .language:       OpenCL C
    .language_version:
      - 2
      - 0
    .max_flat_workgroup_size: 256
    .name:           _Z8prep_ln18PrepArgs
    .private_segment_fixed_size: 0
    .sgpr_count:     18
    .sgpr_spill_count: 0
    .symbol:         _Z8prep_ln18PrepArgs.kd
    .uniform_work_group_size: 1
    .uses_dynamic_stack: false
    .vgpr_count:     61
    .vgpr_spill_count: 0
    .wavefront_size: 64
  - .agpr_count:     0
    .args:
      - .address_space:  global
        .offset:         0
        .size:           8
        .value_kind:     global_buffer
      - .address_space:  global
        .offset:         8
        .size:           8
        .value_kind:     global_buffer
      - .address_space:  global
        .offset:         16
        .size:           8
        .value_kind:     global_buffer
      - .address_space:  global
        .offset:         24
        .size:           8
        .value_kind:     global_buffer
      - .offset:         32
        .size:           144
        .value_kind:     by_value
    .group_segment_fixed_size: 0
    .kernarg_segment_align: 8
    .kernarg_segment_size: 176
    .language:       OpenCL C
    .language_version:
      - 2
      - 0
    .max_flat_workgroup_size: 256
    .name:           _Z10attn64_fwdPKtS0_S0_Pt8PrepArgs
    .private_segment_fixed_size: 0
    .sgpr_count:     42
    .sgpr_spill_count: 0
    .symbol:         _Z10attn64_fwdPKtS0_S0_Pt8PrepArgs.kd
    .uniform_work_group_size: 1
    .uses_dynamic_stack: false
    .vgpr_count:     221
    .vgpr_spill_count: 0
    .wavefront_size: 64
  - .agpr_count:     0
    .args:
      - .address_space:  global
        .offset:         0
        .size:           8
        .value_kind:     global_buffer
      - .address_space:  global
        .offset:         8
        .size:           8
        .value_kind:     global_buffer
      - .offset:         16
        .size:           4
        .value_kind:     by_value
      - .offset:         20
        .size:           4
        .value_kind:     by_value
      - .offset:         24
        .size:           64
        .value_kind:     by_value
    .group_segment_fixed_size: 0
    .kernarg_segment_align: 8
    .kernarg_segment_size: 88
    .language:       OpenCL C
    .language_version:
      - 2
      - 0
    .max_flat_workgroup_size: 256
    .name:           _Z8gemm2b_kILi2EEvPKtS1_ii7EpiArgs
    .private_segment_fixed_size: 0
    .sgpr_count:     92
    .sgpr_spill_count: 0
    .symbol:         _Z8gemm2b_kILi2EEvPKtS1_ii7EpiArgs.kd
    .uniform_work_group_size: 1
    .uses_dynamic_stack: false
    .vgpr_count:     212
    .vgpr_spill_count: 0
    .wavefront_size: 64
  - .agpr_count:     0
    .args:
      - .address_space:  global
        .offset:         0
        .size:           8
        .value_kind:     global_buffer
      - .address_space:  global
        .offset:         8
        .size:           8
        .value_kind:     global_buffer
      - .offset:         16
        .size:           4
        .value_kind:     by_value
      - .offset:         20
        .size:           4
        .value_kind:     by_value
      - .offset:         24
        .size:           64
        .value_kind:     by_value
    .group_segment_fixed_size: 0
    .kernarg_segment_align: 8
    .kernarg_segment_size: 88
    .language:       OpenCL C
    .language_version:
      - 2
      - 0
    .max_flat_workgroup_size: 256
    .name:           _Z8gemm2b_kILi0EEvPKtS1_ii7EpiArgs
    .private_segment_fixed_size: 0
    .sgpr_count:     85
    .sgpr_spill_count: 0
    .symbol:         _Z8gemm2b_kILi0EEvPKtS1_ii7EpiArgs.kd
    .uniform_work_group_size: 1
    .uses_dynamic_stack: false
    .vgpr_count:     186
    .vgpr_spill_count: 0
    .wavefront_size: 64
  - .agpr_count:     0
    .args:
      - .address_space:  global
        .offset:         0
        .size:           8
        .value_kind:     global_buffer
      - .address_space:  global
        .offset:         8
        .size:           8
        .value_kind:     global_buffer
      - .offset:         16
        .size:           4
        .value_kind:     by_value
      - .offset:         20
        .size:           4
        .value_kind:     by_value
      - .offset:         24
        .size:           64
        .value_kind:     by_value
    .group_segment_fixed_size: 0
    .kernarg_segment_align: 8
    .kernarg_segment_size: 88
    .language:       OpenCL C
    .language_version:
      - 2
      - 0
    .max_flat_workgroup_size: 512
    .name:           _Z6gemm_kILi1ELb1ELb0ELb1ELb1ELb0EEvPKtS1_ii7EpiArgs
    .private_segment_fixed_size: 0
    .sgpr_count:     61
    .sgpr_spill_count: 0
    .symbol:         _Z6gemm_kILi1ELb1ELb0ELb1ELb1ELb0EEvPKtS1_ii7EpiArgs.kd
    .uniform_work_group_size: 1
    .uses_dynamic_stack: false
    .vgpr_count:     116
    .vgpr_spill_count: 0
    .wavefront_size: 64
  - .agpr_count:     0
    .args:
      - .address_space:  global
        .offset:         0
        .size:           8
        .value_kind:     global_buffer
      - .address_space:  global
        .offset:         8
        .size:           8
        .value_kind:     global_buffer
      - .offset:         16
        .size:           4
        .value_kind:     by_value
      - .offset:         20
        .size:           4
        .value_kind:     by_value
      - .offset:         24
        .size:           64
        .value_kind:     by_value
    .group_segment_fixed_size: 0
    .kernarg_segment_align: 8
    .kernarg_segment_size: 88
    .language:       OpenCL C
    .language_version:
      - 2
      - 0
    .max_flat_workgroup_size: 512
    .name:           _Z6gemm_kILi1ELb1ELb1ELb0ELb0ELb1EEvPKtS1_ii7EpiArgs
    .private_segment_fixed_size: 0
    .sgpr_count:     84
    .sgpr_spill_count: 0
    .symbol:         _Z6gemm_kILi1ELb1ELb1ELb0ELb0ELb1EEvPKtS1_ii7EpiArgs.kd
    .uniform_work_group_size: 1
    .uses_dynamic_stack: false
    .vgpr_count:     224
    .vgpr_spill_count: 0
    .wavefront_size: 64
